# GU SwiGLU epilogue packed-f32 + interleaved chains; GEMM epilogue stores write-through sc1; GU first K-iteration peeled with C=0 (no acc zeroing)
# speedup vs baseline: 1.0013x; 1.0013x over previous
; #define PG8_STR(x) PG8_STR2(x)
; #define PG8_STAGE(bufoff, gbase, voff) do { _Pragma("unroll") for (int _i = 0; _i < 2; ++_i) \
;         __builtin_amdgcn_global_load_lds((const unsigned*)((const char*)(gbase) + (voff)[_i]), (PG8_LAS unsigned*)(lds + (bufoff) + ldsw + _i * 8192), 16, 0, 0); } while (0)
; #define PG8_LDA(dst, b, h) do { _Pragma("unroll") for (int m = 0; m < 4; ++m) _Pragma("unroll") for (int k = 0; k < 2; ++k) dst[m][k] = *(const PG8_LAS bf16x8*)(lds + PG8_SA(b, h) + aoff + m * 2048 + k * 1024); } while (0)
; #define PG8_LDB(dst, b, h) do { _Pragma("unroll") for (int n = 0; n < 2; ++n) _Pragma("unroll") for (int k = 0; k < 2; ++k) dst[n][k] = *(const PG8_LAS bf16x8*)(lds + PG8_SB(b, h) + boff + n * 2048 + k * 1024); } while (0)
; #define PG8_WAIT_V(n) asm volatile("s_waitcnt vmcnt(" #n ")" ::: "memory")
; #define PG8_WAIT_L(n) asm volatile("s_waitcnt lgkmcnt(" #n ")" ::: "memory")
; template <class Epi, class Sched, bool ALIGN_EPI = false, bool SP2 = false>
; __device__ __forceinline__ void gemm_phase(PG8_LAS unsigned char* lds, const Gemm g, const Sched& S, const Epi& E) {
;     ...
;     for (;;) {
;         const bool has_next = S.next(ui + 1, nxt);
;         const char* nA = has_next ? (const char*)g.A + (size_t)nxt.pm * tstepA : cA; const char* nB = has_next ? (const char*)g.Bt + (size_t)nxt.pn * tstepB : cB;
;         for (int t = 0; t < nt; t += 2) {
;     ...
;             asm volatile(".p2align 6\n\t.rept " PG8_STR(KLOOP_ALIGN) "\n\ts_nop 0\n\t.endr");
;     ...
;             const bool last = (t == nt - 2);
;             const char* a1 = cA + (size_t)(t + 1) * kstep;
;             const char* a2 = last ? nA : cA + (size_t)(t + 2) * kstep; const char* b2 = last ? nB : cB + (size_t)(t + 2) * kstep;
;             const char* a3 = a2 + kstep; const char* b3 = b2 + kstep;
;             if (last && has_next) S.a_ready(nxt);
;             if constexpr (SP2) {
;             PG8_LDB(B0, 0, 0); PG8_LDB(B1, 0, 1); PG8_SCHED; PG8_LDA(At, 0, 0); PG8_STAGE(PG8_SA(1, 1), a1 + hstepA, voffA);
;             PG8_WAIT_V(8); PG8_WAIT_L(0); PG8_BAR; PG8_MMA(0, 0, At, B0); PG8_MMA(0, 1, At, B1); PG8_BAR; PG8_SCHED;
;             PG8_LDA(At, 0, 1); PG8_STAGE(PG8_SB(0, 0), b2, voffB); PG8_STAGE(PG8_SB(0, 1), b2 + hstepB, voffB); PG8_STAGE(PG8_SA(0, 0), a2, voffA);
;             PG8_WAIT_V(8); PG8_WAIT_L(0); PG8_BAR; PG8_MMA(1, 0, At, B0); PG8_MMA(1, 1, At, B1); PG8_BAR; PG8_SCHED;
.LBB0_152:
	s_ashr_i32 s15, s14, 31
	s_lshl_b64 s[16:17], s[14:15], 19
	s_add_u32 s16, s31, s16
	s_addc_u32 s17, s33, s17
	s_and_b64 s[18:19], s[2:3], exec
	s_cselect_b32 s15, s17, s25
	s_cselect_b32 s49, s16, s24
	s_ashr_i32 s13, s12, 31
	s_lshl_b64 s[18:19], s[12:13], 19
	s_add_u32 s18, s34, s18
	s_addc_u32 s19, s35, s19
	s_and_b64 s[26:27], s[2:3], exec
	s_cselect_b32 s13, s19, s23
	s_cselect_b32 s50, s18, s22
	s_add_u32 s51, s22, 0x100
	s_addc_u32 s52, s23, 0
	s_add_u32 s22, s24, 0x40080
	s_addc_u32 s23, s25, 0
	s_mov_b32 s53, -2
	s_add_u32 s24, s22, 0xfffc0080
	s_addc_u32 s25, s23, -1
	s_add_i32 s54, 0, 0x10000
	s_cmp_eq_u32 s53, 12
	s_cselect_b32 s27, s15, s25
	s_cselect_b32 s26, s49, s24
	v_add_u32_e32 v144, s54, v147
	s_cselect_b32 s25, s13, s52
	s_cselect_b32 s24, s50, s51
	s_add_i32 s56, 0, 0x14000
	ds_read_b128 v[150:153], v144
	ds_read_b128 v[154:157], v144 offset:1024
	ds_read_b128 v[158:161], v144 offset:2048
	ds_read_b128 v[162:165], v144 offset:3072
	v_add_u32_e32 v144, s56, v147
	ds_read_b128 v[166:169], v144
	ds_read_b128 v[170:173], v144 offset:1024
	ds_read_b128 v[174:177], v144 offset:2048
	ds_read_b128 v[178:181], v144 offset:3072
	v_lshl_add_u64 v[144:145], s[22:23], 0, v[142:143]
	s_add_i32 m0, s41, 0xc000
	ds_read_b128 v[182:185], v149
	ds_read_b128 v[186:189], v149 offset:1024
	ds_read_b128 v[190:193], v149 offset:2048
	ds_read_b128 v[194:197], v149 offset:3072
	ds_read_b128 v[210:213], v149 offset:4096
	ds_read_b128 v[226:229], v149 offset:5120
	ds_read_b128 v[230:233], v149 offset:6144
	ds_read_b128 v[234:237], v149 offset:7168
	global_load_lds_dwordx4 v[144:145], off
	v_lshl_add_u64 v[144:145], s[22:23], 0, v[140:141]
	s_add_i32 m0, s41, 0xe000
	s_nop 0
	global_load_lds_dwordx4 v[144:145], off
	s_waitcnt vmcnt(8)
	s_waitcnt lgkmcnt(0)
	s_barrier
	s_setprio 1
	s_waitcnt lgkmcnt(0)
	v_mfma_f32_16x16x32_bf16 v[128:131], v[150:153], v[182:185], 0
	v_mfma_f32_16x16x32_bf16 v[120:123], v[158:161], v[182:185], 0
	v_mfma_f32_16x16x32_bf16 v[112:115], v[150:153], v[190:193], 0
	v_mfma_f32_16x16x32_bf16 v[104:107], v[158:161], v[190:193], 0
	v_mfma_f32_16x16x32_bf16 v[96:99], v[150:153], v[210:213], 0
	v_mfma_f32_16x16x32_bf16 v[88:91], v[158:161], v[210:213], 0
	v_mfma_f32_16x16x32_bf16 v[80:83], v[150:153], v[230:233], 0
	v_mfma_f32_16x16x32_bf16 v[72:75], v[158:161], v[230:233], 0
	v_mfma_f32_16x16x32_bf16 v[128:131], v[154:157], v[186:189], v[128:131]
	v_mfma_f32_16x16x32_bf16 v[120:123], v[162:165], v[186:189], v[120:123]
	v_mfma_f32_16x16x32_bf16 v[112:115], v[154:157], v[194:197], v[112:115]
	v_mfma_f32_16x16x32_bf16 v[104:107], v[162:165], v[194:197], v[104:107]
	v_mfma_f32_16x16x32_bf16 v[96:99], v[154:157], v[226:229], v[96:99]
	v_mfma_f32_16x16x32_bf16 v[88:91], v[162:165], v[226:229], v[88:91]
	v_mfma_f32_16x16x32_bf16 v[80:83], v[154:157], v[234:237], v[80:83]
	v_mfma_f32_16x16x32_bf16 v[72:75], v[162:165], v[234:237], v[72:75]
	s_setprio 0
	s_setprio 1
	v_mfma_f32_16x16x32_bf16 v[124:127], v[166:169], v[182:185], 0
	v_mfma_f32_16x16x32_bf16 v[116:119], v[174:177], v[182:185], 0
	v_mfma_f32_16x16x32_bf16 v[108:111], v[166:169], v[190:193], 0
	v_mfma_f32_16x16x32_bf16 v[100:103], v[174:177], v[190:193], 0
	v_mfma_f32_16x16x32_bf16 v[92:95], v[166:169], v[210:213], 0
	v_mfma_f32_16x16x32_bf16 v[84:87], v[174:177], v[210:213], 0
	v_mfma_f32_16x16x32_bf16 v[76:79], v[166:169], v[230:233], 0
	v_mfma_f32_16x16x32_bf16 v[68:71], v[174:177], v[230:233], 0
	v_mfma_f32_16x16x32_bf16 v[124:127], v[170:173], v[186:189], v[124:127]
	v_mfma_f32_16x16x32_bf16 v[116:119], v[178:181], v[186:189], v[116:119]
	v_mfma_f32_16x16x32_bf16 v[108:111], v[170:173], v[194:197], v[108:111]
	v_mfma_f32_16x16x32_bf16 v[100:103], v[178:181], v[194:197], v[100:103]
	v_mfma_f32_16x16x32_bf16 v[92:95], v[170:173], v[226:229], v[92:95]
	v_mfma_f32_16x16x32_bf16 v[84:87], v[178:181], v[226:229], v[84:87]
	v_mfma_f32_16x16x32_bf16 v[76:79], v[170:173], v[234:237], v[76:79]
	v_mfma_f32_16x16x32_bf16 v[68:71], v[178:181], v[234:237], v[68:71]
	s_setprio 0
	s_barrier
	s_add_i32 s54, s54, s39
	v_lshl_add_u64 v[144:145], s[24:25], 0, v[136:137]
	s_mov_b32 m0, s54
	ds_read_b128 v[182:185], v149 offset:16384
	ds_read_b128 v[186:189], v149 offset:17408
	ds_read_b128 v[190:193], v149 offset:18432
	ds_read_b128 v[194:197], v149 offset:19456
	ds_read_b128 v[210:213], v149 offset:20480
	ds_read_b128 v[226:229], v149 offset:21504
	ds_read_b128 v[230:233], v149 offset:22528
	ds_read_b128 v[234:237], v149 offset:23552
	global_load_lds_dwordx4 v[144:145], off
	s_add_i32 m0, s54, 0x2000
	s_add_u32 s54, s24, 0x40000
	v_lshl_add_u64 v[238:239], s[24:25], 0, v[132:133]
	s_addc_u32 s55, s25, 0
	s_add_i32 s56, s56, s39
	global_load_lds_dwordx4 v[238:239], off
	v_lshl_add_u64 v[240:241], s[54:55], 0, v[136:137]
	s_mov_b32 m0, s56
	v_lshl_add_u64 v[242:243], s[26:27], 0, v[134:135]
	global_load_lds_dwordx4 v[240:241], off
	v_lshl_add_u64 v[240:241], s[54:55], 0, v[132:133]
	s_add_i32 m0, s56, 0x2000
	s_nop 0
	global_load_lds_dwordx4 v[240:241], off
	v_lshl_add_u64 v[240:241], s[26:27], 0, v[138:139]
	s_mov_b32 m0, s41
	s_nop 0
	global_load_lds_dwordx4 v[240:241], off
	s_mov_b32 m0, s42
	s_nop 0
	global_load_lds_dwordx4 v[242:243], off
	s_waitcnt vmcnt(8)
	s_waitcnt lgkmcnt(0)
	s_barrier
; #define PG8_STAGE(bufoff, gbase, voff) do { _Pragma("unroll") for (int _i = 0; _i < 2; ++_i) \
;         __builtin_amdgcn_global_load_lds((const unsigned*)((const char*)(gbase) + (voff)[_i]), (PG8_LAS unsigned*)(lds + (bufoff) + ldsw + _i * 8192), 16, 0, 0); } while (0)
; #define PG8_LDA(dst, b, h) do { _Pragma("unroll") for (int m = 0; m < 4; ++m) _Pragma("unroll") for (int k = 0; k < 2; ++k) dst[m][k] = *(const PG8_LAS bf16x8*)(lds + PG8_SA(b, h) + aoff + m * 2048 + k * 1024); } while (0)
; #define PG8_LDB(dst, b, h) do { _Pragma("unroll") for (int n = 0; n < 2; ++n) _Pragma("unroll") for (int k = 0; k < 2; ++k) dst[n][k] = *(const PG8_LAS bf16x8*)(lds + PG8_SB(b, h) + boff + n * 2048 + k * 1024); } while (0)
; #define PG8_MMA(ai, bj, At, Bt) do { __builtin_amdgcn_s_setprio(1); _Pragma("unroll") for (int m = 0; m < 4; ++m) _Pragma("unroll") for (int n = 0; n < 2; ++n) _Pragma("unroll") for (int k = 0; k < 2; ++k) \
;         acc[ai][bj][m][n] = __builtin_amdgcn_mfma_f32_16x16x32_bf16(Bt[n][k], At[m][k], acc[ai][bj][m][n], 0, 0, 0); __builtin_amdgcn_s_setprio(0); } while (0)
; #define PG8_WAIT_V(n) asm volatile("s_waitcnt vmcnt(" #n ")" ::: "memory")
; #define PG8_WAIT_L(n) asm volatile("s_waitcnt lgkmcnt(" #n ")" ::: "memory")
; #define PG8_BAR __builtin_amdgcn_s_barrier()
; #define PG8_SCHED __builtin_amdgcn_sched_barrier(0)
; template <class Epi, class Sched, bool ALIGN_EPI = false, bool SP2 = false>
; __device__ __forceinline__ void gemm_phase(PG8_LAS unsigned char* lds, const Gemm g, const Sched& S, const Epi& E) {
;     ...
;             PG8_WAIT_V(8); PG8_WAIT_L(0); PG8_BAR; PG8_MMA(1, 0, At, B0); PG8_MMA(1, 1, At, B1); PG8_BAR; PG8_SCHED;
;             PG8_LDB(B0, 1, 0); PG8_LDB(B1, 1, 1); PG8_SCHED; PG8_LDA(At, 1, 0); PG8_STAGE(PG8_SA(0, 1), a2 + hstepA, voffA);
;             PG8_WAIT_V(8); PG8_WAIT_L(0); PG8_BAR; PG8_MMA(0, 0, At, B0); PG8_MMA(0, 1, At, B1); PG8_BAR; PG8_SCHED;
	s_setprio 1
	s_waitcnt lgkmcnt(0)
	v_mfma_f32_16x16x32_bf16 v[64:67], v[150:153], v[182:185], 0
	v_mfma_f32_16x16x32_bf16 v[56:59], v[158:161], v[182:185], 0
	v_mfma_f32_16x16x32_bf16 v[48:51], v[150:153], v[190:193], 0
	v_mfma_f32_16x16x32_bf16 v[40:43], v[158:161], v[190:193], 0
	v_mfma_f32_16x16x32_bf16 v[32:35], v[150:153], v[210:213], 0
	v_mfma_f32_16x16x32_bf16 v[24:27], v[158:161], v[210:213], 0
	v_mfma_f32_16x16x32_bf16 v[16:19], v[150:153], v[230:233], 0
	v_mfma_f32_16x16x32_bf16 v[8:11], v[158:161], v[230:233], 0
	v_mfma_f32_16x16x32_bf16 v[64:67], v[154:157], v[186:189], v[64:67]
	v_mfma_f32_16x16x32_bf16 v[56:59], v[162:165], v[186:189], v[56:59]
	v_mfma_f32_16x16x32_bf16 v[48:51], v[154:157], v[194:197], v[48:51]
	v_mfma_f32_16x16x32_bf16 v[40:43], v[162:165], v[194:197], v[40:43]
	v_mfma_f32_16x16x32_bf16 v[32:35], v[154:157], v[226:229], v[32:35]
	v_mfma_f32_16x16x32_bf16 v[24:27], v[162:165], v[226:229], v[24:27]
	v_mfma_f32_16x16x32_bf16 v[16:19], v[154:157], v[234:237], v[16:19]
	v_mfma_f32_16x16x32_bf16 v[8:11], v[162:165], v[234:237], v[8:11]
	s_setprio 0
	s_setprio 1
	v_mfma_f32_16x16x32_bf16 v[60:63], v[166:169], v[182:185], 0
	v_mfma_f32_16x16x32_bf16 v[52:55], v[174:177], v[182:185], 0
	v_mfma_f32_16x16x32_bf16 v[44:47], v[166:169], v[190:193], 0
	v_mfma_f32_16x16x32_bf16 v[36:39], v[174:177], v[190:193], 0
	v_mfma_f32_16x16x32_bf16 v[28:31], v[166:169], v[210:213], 0
	v_mfma_f32_16x16x32_bf16 v[20:23], v[174:177], v[210:213], 0
	v_mfma_f32_16x16x32_bf16 v[12:15], v[166:169], v[230:233], 0
	v_mfma_f32_16x16x32_bf16 v[4:7], v[174:177], v[230:233], 0
	v_mfma_f32_16x16x32_bf16 v[60:63], v[170:173], v[186:189], v[60:63]
	v_mfma_f32_16x16x32_bf16 v[52:55], v[178:181], v[186:189], v[52:55]
	v_mfma_f32_16x16x32_bf16 v[44:47], v[170:173], v[194:197], v[44:47]
	v_mfma_f32_16x16x32_bf16 v[36:39], v[178:181], v[194:197], v[36:39]
	v_mfma_f32_16x16x32_bf16 v[28:31], v[170:173], v[226:229], v[28:31]
	v_mfma_f32_16x16x32_bf16 v[20:23], v[178:181], v[226:229], v[20:23]
	v_mfma_f32_16x16x32_bf16 v[12:15], v[170:173], v[234:237], v[12:15]
	v_mfma_f32_16x16x32_bf16 v[4:7], v[178:181], v[234:237], v[4:7]
	s_setprio 0
	s_barrier
	s_add_i32 s54, 0, 0x18000
	s_add_i32 s55, 0, 0x1c000
	v_add_u32_e32 v162, s54, v147
	v_add_u32_e32 v178, s55, v147
	ds_read_b128 v[150:153], v162
	ds_read_b128 v[154:157], v162 offset:1024
	ds_read_b128 v[158:161], v162 offset:2048
	ds_read_b128 v[162:165], v162 offset:3072
	ds_read_b128 v[166:169], v178
	ds_read_b128 v[170:173], v178 offset:1024
	ds_read_b128 v[174:177], v178 offset:2048
	ds_read_b128 v[178:181], v178 offset:3072
	s_add_u32 s26, s26, 0x40000
	s_addc_u32 s27, s27, 0
	s_mov_b32 m0, s43
	v_lshl_add_u64 v[244:245], s[26:27], 0, v[138:139]
	ds_read_b128 v[182:185], v149 offset:32768
	ds_read_b128 v[186:189], v149 offset:33792
	ds_read_b128 v[190:193], v149 offset:34816
	ds_read_b128 v[194:197], v149 offset:35840
	ds_read_b128 v[210:213], v149 offset:36864
	ds_read_b128 v[226:229], v149 offset:37888
	ds_read_b128 v[230:233], v149 offset:38912
	ds_read_b128 v[234:237], v149 offset:39936
	global_load_lds_dwordx4 v[244:245], off
	v_lshl_add_u64 v[244:245], s[26:27], 0, v[134:135]
	s_mov_b32 m0, s44
	s_nop 0
	global_load_lds_dwordx4 v[244:245], off
	s_waitcnt vmcnt(8)
	s_waitcnt lgkmcnt(0)
	s_barrier
	s_setprio 1
	s_waitcnt lgkmcnt(0)
	v_mfma_f32_16x16x32_bf16 v[128:131], v[150:153], v[182:185], v[128:131]
	v_mfma_f32_16x16x32_bf16 v[120:123], v[158:161], v[182:185], v[120:123]
	v_mfma_f32_16x16x32_bf16 v[112:115], v[150:153], v[190:193], v[112:115]
	v_mfma_f32_16x16x32_bf16 v[104:107], v[158:161], v[190:193], v[104:107]
	v_mfma_f32_16x16x32_bf16 v[96:99], v[150:153], v[210:213], v[96:99]
	v_mfma_f32_16x16x32_bf16 v[88:91], v[158:161], v[210:213], v[88:91]
	v_mfma_f32_16x16x32_bf16 v[80:83], v[150:153], v[230:233], v[80:83]
	v_mfma_f32_16x16x32_bf16 v[72:75], v[158:161], v[230:233], v[72:75]
	v_mfma_f32_16x16x32_bf16 v[128:131], v[154:157], v[186:189], v[128:131]
	v_mfma_f32_16x16x32_bf16 v[120:123], v[162:165], v[186:189], v[120:123]
	v_mfma_f32_16x16x32_bf16 v[112:115], v[154:157], v[194:197], v[112:115]
	v_mfma_f32_16x16x32_bf16 v[104:107], v[162:165], v[194:197], v[104:107]
	v_mfma_f32_16x16x32_bf16 v[96:99], v[154:157], v[226:229], v[96:99]
	v_mfma_f32_16x16x32_bf16 v[88:91], v[162:165], v[226:229], v[88:91]
	v_mfma_f32_16x16x32_bf16 v[80:83], v[154:157], v[234:237], v[80:83]
	v_mfma_f32_16x16x32_bf16 v[72:75], v[162:165], v[234:237], v[72:75]
	s_setprio 0
	s_setprio 1
	v_mfma_f32_16x16x32_bf16 v[124:127], v[166:169], v[182:185], v[124:127]
	v_mfma_f32_16x16x32_bf16 v[116:119], v[174:177], v[182:185], v[116:119]
	v_mfma_f32_16x16x32_bf16 v[108:111], v[166:169], v[190:193], v[108:111]
	v_mfma_f32_16x16x32_bf16 v[100:103], v[174:177], v[190:193], v[100:103]
	v_mfma_f32_16x16x32_bf16 v[92:95], v[166:169], v[210:213], v[92:95]
	v_mfma_f32_16x16x32_bf16 v[84:87], v[174:177], v[210:213], v[84:87]
	v_mfma_f32_16x16x32_bf16 v[76:79], v[166:169], v[230:233], v[76:79]
	v_mfma_f32_16x16x32_bf16 v[68:71], v[174:177], v[230:233], v[68:71]
	v_mfma_f32_16x16x32_bf16 v[124:127], v[170:173], v[186:189], v[124:127]
	v_mfma_f32_16x16x32_bf16 v[116:119], v[178:181], v[186:189], v[116:119]
	v_mfma_f32_16x16x32_bf16 v[108:111], v[170:173], v[194:197], v[108:111]
	v_mfma_f32_16x16x32_bf16 v[100:103], v[178:181], v[194:197], v[100:103]
	v_mfma_f32_16x16x32_bf16 v[92:95], v[170:173], v[226:229], v[92:95]
	v_mfma_f32_16x16x32_bf16 v[84:87], v[178:181], v[226:229], v[84:87]
	v_mfma_f32_16x16x32_bf16 v[76:79], v[170:173], v[234:237], v[76:79]
	v_mfma_f32_16x16x32_bf16 v[68:71], v[178:181], v[234:237], v[68:71]
	s_setprio 0
	s_barrier
; #define PG8_STR(x) PG8_STR2(x)
; #define PG8_STAGE(bufoff, gbase, voff) do { _Pragma("unroll") for (int _i = 0; _i < 2; ++_i) \
;         __builtin_amdgcn_global_load_lds((const unsigned*)((const char*)(gbase) + (voff)[_i]), (PG8_LAS unsigned*)(lds + (bufoff) + ldsw + _i * 8192), 16, 0, 0); } while (0)
; #define PG8_LDA(dst, b, h) do { _Pragma("unroll") for (int m = 0; m < 4; ++m) _Pragma("unroll") for (int k = 0; k < 2; ++k) dst[m][k] = *(const PG8_LAS bf16x8*)(lds + PG8_SA(b, h) + aoff + m * 2048 + k * 1024); } while (0)
; #define PG8_LDB(dst, b, h) do { _Pragma("unroll") for (int n = 0; n < 2; ++n) _Pragma("unroll") for (int k = 0; k < 2; ++k) dst[n][k] = *(const PG8_LAS bf16x8*)(lds + PG8_SB(b, h) + boff + n * 2048 + k * 1024); } while (0)
; #define PG8_MMA(ai, bj, At, Bt) do { __builtin_amdgcn_s_setprio(1); _Pragma("unroll") for (int m = 0; m < 4; ++m) _Pragma("unroll") for (int n = 0; n < 2; ++n) _Pragma("unroll") for (int k = 0; k < 2; ++k) \
;         acc[ai][bj][m][n] = __builtin_amdgcn_mfma_f32_16x16x32_bf16(Bt[n][k], At[m][k], acc[ai][bj][m][n], 0, 0, 0); __builtin_amdgcn_s_setprio(0); } while (0)
; #define PG8_WAIT_V(n) asm volatile("s_waitcnt vmcnt(" #n ")" ::: "memory")
; #define PG8_BAR __builtin_amdgcn_s_barrier()
; template <class Epi, class Sched, bool ALIGN_EPI = false, bool SP2 = false>
; __device__ __forceinline__ void gemm_phase(PG8_LAS unsigned char* lds, const Gemm g, const Sched& S, const Epi& E) {
;     ...
;         for (int t = 0; t < nt; t += 2) {
;     ...
;             asm volatile(".p2align 6\n\t.rept " PG8_STR(KLOOP_ALIGN) "\n\ts_nop 0\n\t.endr");
;     ...
;             const bool last = (t == nt - 2);
;             const char* a1 = cA + (size_t)(t + 1) * kstep;
;             const char* a2 = last ? nA : cA + (size_t)(t + 2) * kstep; const char* b2 = last ? nB : cB + (size_t)(t + 2) * kstep;
;             const char* a3 = a2 + kstep; const char* b3 = b2 + kstep;
;             if (last && has_next) S.a_ready(nxt);
;             if constexpr (SP2) {
;             PG8_LDB(B0, 0, 0); PG8_LDB(B1, 0, 1); PG8_SCHED; PG8_LDA(At, 0, 0); PG8_STAGE(PG8_SA(1, 1), a1 + hstepA, voffA);
;     ...
;             PG8_LDA(At, 1, 1); PG8_STAGE(PG8_SB(1, 0), b3, voffB); PG8_STAGE(PG8_SB(1, 1), b3 + hstepB, voffB); PG8_STAGE(PG8_SA(1, 0), a3, voffA);
;             PG8_WAIT_V(8); PG8_WAIT_L(0); PG8_BAR; PG8_MMA(1, 0, At, B0); PG8_MMA(1, 1, At, B1); PG8_BAR; PG8_SCHED;
	s_add_i32 s26, s54, s39
	v_lshl_add_u64 v[144:145], v[144:145], 0, s[64:65]
	s_mov_b32 m0, s26
	ds_read_b128 v[182:185], v149 offset:49152
	ds_read_b128 v[186:189], v149 offset:50176
	ds_read_b128 v[190:193], v149 offset:51200
	ds_read_b128 v[194:197], v149 offset:52224
	ds_read_b128 v[210:213], v149 offset:53248
	ds_read_b128 v[226:229], v149 offset:54272
	ds_read_b128 v[230:233], v149 offset:55296
	ds_read_b128 v[234:237], v149 offset:56320
	global_load_lds_dwordx4 v[144:145], off
	s_add_i32 m0, s26, 0x2000
	s_add_u32 s24, s24, 0x40080
	v_lshl_add_u64 v[144:145], v[238:239], 0, s[64:65]
	s_addc_u32 s25, s25, 0
	s_add_i32 s26, s55, s39
	global_load_lds_dwordx4 v[144:145], off
	v_lshl_add_u64 v[144:145], s[24:25], 0, v[136:137]
	s_mov_b32 m0, s26
	s_nop 0
	global_load_lds_dwordx4 v[144:145], off
	v_lshl_add_u64 v[144:145], s[24:25], 0, v[132:133]
	s_add_i32 m0, s26, 0x2000
	s_nop 0
	global_load_lds_dwordx4 v[144:145], off
	v_lshl_add_u64 v[144:145], v[240:241], 0, s[64:65]
	s_mov_b32 m0, s45
	s_nop 0
	global_load_lds_dwordx4 v[144:145], off
	v_lshl_add_u64 v[144:145], v[242:243], 0, s[64:65]
	s_mov_b32 m0, s46
	s_nop 0
	global_load_lds_dwordx4 v[144:145], off
	s_waitcnt vmcnt(8)
	s_waitcnt lgkmcnt(0)
	s_barrier
	s_setprio 1
	s_waitcnt lgkmcnt(0)
	v_mfma_f32_16x16x32_bf16 v[64:67], v[150:153], v[182:185], v[64:67]
	v_mfma_f32_16x16x32_bf16 v[56:59], v[158:161], v[182:185], v[56:59]
	v_mfma_f32_16x16x32_bf16 v[48:51], v[150:153], v[190:193], v[48:51]
	v_mfma_f32_16x16x32_bf16 v[40:43], v[158:161], v[190:193], v[40:43]
	v_mfma_f32_16x16x32_bf16 v[32:35], v[150:153], v[210:213], v[32:35]
	v_mfma_f32_16x16x32_bf16 v[24:27], v[158:161], v[210:213], v[24:27]
	v_mfma_f32_16x16x32_bf16 v[16:19], v[150:153], v[230:233], v[16:19]
	v_mfma_f32_16x16x32_bf16 v[8:11], v[158:161], v[230:233], v[8:11]
	v_mfma_f32_16x16x32_bf16 v[64:67], v[154:157], v[186:189], v[64:67]
	v_mfma_f32_16x16x32_bf16 v[56:59], v[162:165], v[186:189], v[56:59]
	v_mfma_f32_16x16x32_bf16 v[48:51], v[154:157], v[194:197], v[48:51]
	v_mfma_f32_16x16x32_bf16 v[40:43], v[162:165], v[194:197], v[40:43]
	v_mfma_f32_16x16x32_bf16 v[32:35], v[154:157], v[226:229], v[32:35]
	v_mfma_f32_16x16x32_bf16 v[24:27], v[162:165], v[226:229], v[24:27]
	v_mfma_f32_16x16x32_bf16 v[16:19], v[154:157], v[234:237], v[16:19]
	v_mfma_f32_16x16x32_bf16 v[8:11], v[162:165], v[234:237], v[8:11]
	s_setprio 0
	s_setprio 1
	v_mfma_f32_16x16x32_bf16 v[60:63], v[166:169], v[182:185], v[60:63]
	v_mfma_f32_16x16x32_bf16 v[52:55], v[174:177], v[182:185], v[52:55]
	v_mfma_f32_16x16x32_bf16 v[44:47], v[166:169], v[190:193], v[44:47]
	v_mfma_f32_16x16x32_bf16 v[36:39], v[174:177], v[190:193], v[36:39]
	v_mfma_f32_16x16x32_bf16 v[28:31], v[166:169], v[210:213], v[28:31]
	v_mfma_f32_16x16x32_bf16 v[20:23], v[174:177], v[210:213], v[20:23]
	v_mfma_f32_16x16x32_bf16 v[12:15], v[166:169], v[230:233], v[12:15]
	v_mfma_f32_16x16x32_bf16 v[4:7], v[174:177], v[230:233], v[4:7]
	v_mfma_f32_16x16x32_bf16 v[60:63], v[170:173], v[186:189], v[60:63]
	v_mfma_f32_16x16x32_bf16 v[52:55], v[178:181], v[186:189], v[52:55]
	v_mfma_f32_16x16x32_bf16 v[44:47], v[170:173], v[194:197], v[44:47]
	v_mfma_f32_16x16x32_bf16 v[36:39], v[178:181], v[194:197], v[36:39]
	v_mfma_f32_16x16x32_bf16 v[28:31], v[170:173], v[226:229], v[28:31]
	v_mfma_f32_16x16x32_bf16 v[20:23], v[178:181], v[226:229], v[20:23]
	v_mfma_f32_16x16x32_bf16 v[12:15], v[170:173], v[234:237], v[12:15]
	v_mfma_f32_16x16x32_bf16 v[4:7], v[178:181], v[234:237], v[4:7]
	s_setprio 0
	s_barrier
	s_add_i32 s53, s53, 2
	s_add_u32 s51, s51, 0x100
	s_addc_u32 s52, s52, 0
	s_add_u32 s22, s22, 0x100
	s_addc_u32 s23, s23, 0
	s_cmp_gt_u32 s53, 13
	s_cbranch_scc1 .Lpeel_exit_0
.LBB0_153:
	s_add_u32 s24, s22, 0xfffc0080
	s_addc_u32 s25, s23, -1
	s_add_i32 s54, 0, 0x10000
	s_cmp_eq_u32 s53, 12
	s_cselect_b32 s27, s15, s25
	s_cselect_b32 s26, s49, s24
	v_add_u32_e32 v144, s54, v147
	s_cselect_b32 s25, s13, s52
	s_cselect_b32 s24, s50, s51
	s_add_i32 s56, 0, 0x14000
	ds_read_b128 v[150:153], v144
	ds_read_b128 v[154:157], v144 offset:1024
	ds_read_b128 v[158:161], v144 offset:2048
	ds_read_b128 v[162:165], v144 offset:3072
	v_add_u32_e32 v144, s56, v147
	ds_read_b128 v[166:169], v144
	ds_read_b128 v[170:173], v144 offset:1024
	ds_read_b128 v[174:177], v144 offset:2048
	ds_read_b128 v[178:181], v144 offset:3072
	v_lshl_add_u64 v[144:145], s[22:23], 0, v[142:143]
	s_add_i32 m0, s41, 0xc000
	ds_read_b128 v[182:185], v149
	ds_read_b128 v[186:189], v149 offset:1024
	ds_read_b128 v[190:193], v149 offset:2048
	ds_read_b128 v[194:197], v149 offset:3072
	ds_read_b128 v[210:213], v149 offset:4096
	ds_read_b128 v[226:229], v149 offset:5120
	ds_read_b128 v[230:233], v149 offset:6144
	ds_read_b128 v[234:237], v149 offset:7168
	global_load_lds_dwordx4 v[144:145], off
	v_lshl_add_u64 v[144:145], s[22:23], 0, v[140:141]
	s_add_i32 m0, s41, 0xe000
	s_nop 0
	global_load_lds_dwordx4 v[144:145], off
	s_waitcnt vmcnt(8)
	s_waitcnt lgkmcnt(0)
	s_barrier
; #define PG8_STAGE(bufoff, gbase, voff) do { _Pragma("unroll") for (int _i = 0; _i < 2; ++_i) \
;         __builtin_amdgcn_global_load_lds((const unsigned*)((const char*)(gbase) + (voff)[_i]), (PG8_LAS unsigned*)(lds + (bufoff) + ldsw + _i * 8192), 16, 0, 0); } while (0)
; #define PG8_LDA(dst, b, h) do { _Pragma("unroll") for (int m = 0; m < 4; ++m) _Pragma("unroll") for (int k = 0; k < 2; ++k) dst[m][k] = *(const PG8_LAS bf16x8*)(lds + PG8_SA(b, h) + aoff + m * 2048 + k * 1024); } while (0)
; #define PG8_MMA(ai, bj, At, Bt) do { __builtin_amdgcn_s_setprio(1); _Pragma("unroll") for (int m = 0; m < 4; ++m) _Pragma("unroll") for (int n = 0; n < 2; ++n) _Pragma("unroll") for (int k = 0; k < 2; ++k) \
;         acc[ai][bj][m][n] = __builtin_amdgcn_mfma_f32_16x16x32_bf16(Bt[n][k], At[m][k], acc[ai][bj][m][n], 0, 0, 0); __builtin_amdgcn_s_setprio(0); } while (0)
; #define PG8_WAIT_V(n) asm volatile("s_waitcnt vmcnt(" #n ")" ::: "memory")
; #define PG8_WAIT_L(n) asm volatile("s_waitcnt lgkmcnt(" #n ")" ::: "memory")
; #define PG8_BAR __builtin_amdgcn_s_barrier()
; #define PG8_SCHED __builtin_amdgcn_sched_barrier(0)
; template <class Epi, class Sched, bool ALIGN_EPI = false, bool SP2 = false>
; __device__ __forceinline__ void gemm_phase(PG8_LAS unsigned char* lds, const Gemm g, const Sched& S, const Epi& E) {
;     ...
;             PG8_WAIT_V(8); PG8_WAIT_L(0); PG8_BAR; PG8_MMA(0, 0, At, B0); PG8_MMA(0, 1, At, B1); PG8_BAR; PG8_SCHED;
;             PG8_LDA(At, 0, 1); PG8_STAGE(PG8_SB(0, 0), b2, voffB); PG8_STAGE(PG8_SB(0, 1), b2 + hstepB, voffB); PG8_STAGE(PG8_SA(0, 0), a2, voffA);
;             PG8_WAIT_V(8); PG8_WAIT_L(0); PG8_BAR; PG8_MMA(1, 0, At, B0); PG8_MMA(1, 1, At, B1); PG8_BAR; PG8_SCHED;
	s_setprio 1
	s_waitcnt lgkmcnt(0)
	v_mfma_f32_16x16x32_bf16 v[128:131], v[150:153], v[182:185], v[128:131]
	v_mfma_f32_16x16x32_bf16 v[120:123], v[158:161], v[182:185], v[120:123]
	v_mfma_f32_16x16x32_bf16 v[112:115], v[150:153], v[190:193], v[112:115]
	v_mfma_f32_16x16x32_bf16 v[104:107], v[158:161], v[190:193], v[104:107]
	v_mfma_f32_16x16x32_bf16 v[96:99], v[150:153], v[210:213], v[96:99]
	v_mfma_f32_16x16x32_bf16 v[88:91], v[158:161], v[210:213], v[88:91]
	v_mfma_f32_16x16x32_bf16 v[80:83], v[150:153], v[230:233], v[80:83]
	v_mfma_f32_16x16x32_bf16 v[72:75], v[158:161], v[230:233], v[72:75]
	v_mfma_f32_16x16x32_bf16 v[128:131], v[154:157], v[186:189], v[128:131]
	v_mfma_f32_16x16x32_bf16 v[120:123], v[162:165], v[186:189], v[120:123]
	v_mfma_f32_16x16x32_bf16 v[112:115], v[154:157], v[194:197], v[112:115]
	v_mfma_f32_16x16x32_bf16 v[104:107], v[162:165], v[194:197], v[104:107]
	v_mfma_f32_16x16x32_bf16 v[96:99], v[154:157], v[226:229], v[96:99]
	v_mfma_f32_16x16x32_bf16 v[88:91], v[162:165], v[226:229], v[88:91]
	v_mfma_f32_16x16x32_bf16 v[80:83], v[154:157], v[234:237], v[80:83]
	v_mfma_f32_16x16x32_bf16 v[72:75], v[162:165], v[234:237], v[72:75]
	s_setprio 0
	s_setprio 1
	v_mfma_f32_16x16x32_bf16 v[124:127], v[166:169], v[182:185], v[124:127]
	v_mfma_f32_16x16x32_bf16 v[116:119], v[174:177], v[182:185], v[116:119]
	v_mfma_f32_16x16x32_bf16 v[108:111], v[166:169], v[190:193], v[108:111]
	v_mfma_f32_16x16x32_bf16 v[100:103], v[174:177], v[190:193], v[100:103]
	v_mfma_f32_16x16x32_bf16 v[92:95], v[166:169], v[210:213], v[92:95]
	v_mfma_f32_16x16x32_bf16 v[84:87], v[174:177], v[210:213], v[84:87]
	v_mfma_f32_16x16x32_bf16 v[76:79], v[166:169], v[230:233], v[76:79]
	v_mfma_f32_16x16x32_bf16 v[68:71], v[174:177], v[230:233], v[68:71]
	v_mfma_f32_16x16x32_bf16 v[124:127], v[170:173], v[186:189], v[124:127]
	v_mfma_f32_16x16x32_bf16 v[116:119], v[178:181], v[186:189], v[116:119]
	v_mfma_f32_16x16x32_bf16 v[108:111], v[170:173], v[194:197], v[108:111]
	v_mfma_f32_16x16x32_bf16 v[100:103], v[178:181], v[194:197], v[100:103]
	v_mfma_f32_16x16x32_bf16 v[92:95], v[170:173], v[226:229], v[92:95]
	v_mfma_f32_16x16x32_bf16 v[84:87], v[178:181], v[226:229], v[84:87]
	v_mfma_f32_16x16x32_bf16 v[76:79], v[170:173], v[234:237], v[76:79]
	v_mfma_f32_16x16x32_bf16 v[68:71], v[178:181], v[234:237], v[68:71]
	s_setprio 0
	s_barrier
	s_add_i32 s54, s54, s39
	v_lshl_add_u64 v[144:145], s[24:25], 0, v[136:137]
	s_mov_b32 m0, s54
	ds_read_b128 v[182:185], v149 offset:16384
	ds_read_b128 v[186:189], v149 offset:17408
	ds_read_b128 v[190:193], v149 offset:18432
	ds_read_b128 v[194:197], v149 offset:19456
	ds_read_b128 v[210:213], v149 offset:20480
	ds_read_b128 v[226:229], v149 offset:21504
	ds_read_b128 v[230:233], v149 offset:22528
	ds_read_b128 v[234:237], v149 offset:23552
	global_load_lds_dwordx4 v[144:145], off
	s_add_i32 m0, s54, 0x2000
	s_add_u32 s54, s24, 0x40000
	v_lshl_add_u64 v[238:239], s[24:25], 0, v[132:133]
	s_addc_u32 s55, s25, 0
	s_add_i32 s56, s56, s39
	global_load_lds_dwordx4 v[238:239], off
	v_lshl_add_u64 v[240:241], s[54:55], 0, v[136:137]
	s_mov_b32 m0, s56
	v_lshl_add_u64 v[242:243], s[26:27], 0, v[134:135]
	global_load_lds_dwordx4 v[240:241], off
	v_lshl_add_u64 v[240:241], s[54:55], 0, v[132:133]
	s_add_i32 m0, s56, 0x2000
	s_nop 0
	global_load_lds_dwordx4 v[240:241], off
	v_lshl_add_u64 v[240:241], s[26:27], 0, v[138:139]
	s_mov_b32 m0, s41
	s_nop 0
	global_load_lds_dwordx4 v[240:241], off
	s_mov_b32 m0, s42
	s_nop 0
	global_load_lds_dwordx4 v[242:243], off
	s_waitcnt vmcnt(8)
	s_waitcnt lgkmcnt(0)
	s_barrier
	s_setprio 1
	s_waitcnt lgkmcnt(0)
	v_mfma_f32_16x16x32_bf16 v[64:67], v[150:153], v[182:185], v[64:67]
	v_mfma_f32_16x16x32_bf16 v[56:59], v[158:161], v[182:185], v[56:59]
	v_mfma_f32_16x16x32_bf16 v[48:51], v[150:153], v[190:193], v[48:51]
	v_mfma_f32_16x16x32_bf16 v[40:43], v[158:161], v[190:193], v[40:43]
	v_mfma_f32_16x16x32_bf16 v[32:35], v[150:153], v[210:213], v[32:35]
	v_mfma_f32_16x16x32_bf16 v[24:27], v[158:161], v[210:213], v[24:27]
	v_mfma_f32_16x16x32_bf16 v[16:19], v[150:153], v[230:233], v[16:19]
	v_mfma_f32_16x16x32_bf16 v[8:11], v[158:161], v[230:233], v[8:11]
	v_mfma_f32_16x16x32_bf16 v[64:67], v[154:157], v[186:189], v[64:67]
	v_mfma_f32_16x16x32_bf16 v[56:59], v[162:165], v[186:189], v[56:59]
	v_mfma_f32_16x16x32_bf16 v[48:51], v[154:157], v[194:197], v[48:51]
	v_mfma_f32_16x16x32_bf16 v[40:43], v[162:165], v[194:197], v[40:43]
	v_mfma_f32_16x16x32_bf16 v[32:35], v[154:157], v[226:229], v[32:35]
	v_mfma_f32_16x16x32_bf16 v[24:27], v[162:165], v[226:229], v[24:27]
	v_mfma_f32_16x16x32_bf16 v[16:19], v[154:157], v[234:237], v[16:19]
	v_mfma_f32_16x16x32_bf16 v[8:11], v[162:165], v[234:237], v[8:11]
	s_setprio 0
	s_setprio 1
	v_mfma_f32_16x16x32_bf16 v[60:63], v[166:169], v[182:185], v[60:63]
	v_mfma_f32_16x16x32_bf16 v[52:55], v[174:177], v[182:185], v[52:55]
	v_mfma_f32_16x16x32_bf16 v[44:47], v[166:169], v[190:193], v[44:47]
	v_mfma_f32_16x16x32_bf16 v[36:39], v[174:177], v[190:193], v[36:39]
	v_mfma_f32_16x16x32_bf16 v[28:31], v[166:169], v[210:213], v[28:31]
	v_mfma_f32_16x16x32_bf16 v[20:23], v[174:177], v[210:213], v[20:23]
	v_mfma_f32_16x16x32_bf16 v[12:15], v[166:169], v[230:233], v[12:15]
	v_mfma_f32_16x16x32_bf16 v[4:7], v[174:177], v[230:233], v[4:7]
	v_mfma_f32_16x16x32_bf16 v[60:63], v[170:173], v[186:189], v[60:63]
	v_mfma_f32_16x16x32_bf16 v[52:55], v[178:181], v[186:189], v[52:55]
	v_mfma_f32_16x16x32_bf16 v[44:47], v[170:173], v[194:197], v[44:47]
	v_mfma_f32_16x16x32_bf16 v[36:39], v[178:181], v[194:197], v[36:39]
	v_mfma_f32_16x16x32_bf16 v[28:31], v[170:173], v[226:229], v[28:31]
	v_mfma_f32_16x16x32_bf16 v[20:23], v[178:181], v[226:229], v[20:23]
	v_mfma_f32_16x16x32_bf16 v[12:15], v[170:173], v[234:237], v[12:15]
	v_mfma_f32_16x16x32_bf16 v[4:7], v[178:181], v[234:237], v[4:7]
	s_setprio 0
	s_barrier
; #define PG8_STAGE(bufoff, gbase, voff) do { _Pragma("unroll") for (int _i = 0; _i < 2; ++_i) \
;         __builtin_amdgcn_global_load_lds((const unsigned*)((const char*)(gbase) + (voff)[_i]), (PG8_LAS unsigned*)(lds + (bufoff) + ldsw + _i * 8192), 16, 0, 0); } while (0)
; #define PG8_LDA(dst, b, h) do { _Pragma("unroll") for (int m = 0; m < 4; ++m) _Pragma("unroll") for (int k = 0; k < 2; ++k) dst[m][k] = *(const PG8_LAS bf16x8*)(lds + PG8_SA(b, h) + aoff + m * 2048 + k * 1024); } while (0)
; #define PG8_LDB(dst, b, h) do { _Pragma("unroll") for (int n = 0; n < 2; ++n) _Pragma("unroll") for (int k = 0; k < 2; ++k) dst[n][k] = *(const PG8_LAS bf16x8*)(lds + PG8_SB(b, h) + boff + n * 2048 + k * 1024); } while (0)
; #define PG8_MMA(ai, bj, At, Bt) do { __builtin_amdgcn_s_setprio(1); _Pragma("unroll") for (int m = 0; m < 4; ++m) _Pragma("unroll") for (int n = 0; n < 2; ++n) _Pragma("unroll") for (int k = 0; k < 2; ++k) \
;         acc[ai][bj][m][n] = __builtin_amdgcn_mfma_f32_16x16x32_bf16(Bt[n][k], At[m][k], acc[ai][bj][m][n], 0, 0, 0); __builtin_amdgcn_s_setprio(0); } while (0)
; #define PG8_WAIT_V(n) asm volatile("s_waitcnt vmcnt(" #n ")" ::: "memory")
; #define PG8_WAIT_L(n) asm volatile("s_waitcnt lgkmcnt(" #n ")" ::: "memory")
; #define PG8_BAR __builtin_amdgcn_s_barrier()
; #define PG8_SCHED __builtin_amdgcn_sched_barrier(0)
; template <class Epi, class Sched, bool ALIGN_EPI = false, bool SP2 = false>
; __device__ __forceinline__ void gemm_phase(PG8_LAS unsigned char* lds, const Gemm g, const Sched& S, const Epi& E) {
;     ...
;             PG8_LDB(B0, 1, 0); PG8_LDB(B1, 1, 1); PG8_SCHED; PG8_LDA(At, 1, 0); PG8_STAGE(PG8_SA(0, 1), a2 + hstepA, voffA);
;             PG8_WAIT_V(8); PG8_WAIT_L(0); PG8_BAR; PG8_MMA(0, 0, At, B0); PG8_MMA(0, 1, At, B1); PG8_BAR; PG8_SCHED;
;             PG8_LDA(At, 1, 1); PG8_STAGE(PG8_SB(1, 0), b3, voffB); PG8_STAGE(PG8_SB(1, 1), b3 + hstepB, voffB); PG8_STAGE(PG8_SA(1, 0), a3, voffA);
;             PG8_WAIT_V(8); PG8_WAIT_L(0); PG8_BAR; PG8_MMA(1, 0, At, B0); PG8_MMA(1, 1, At, B1); PG8_BAR; PG8_SCHED;
	s_add_i32 s54, 0, 0x18000
	s_add_i32 s55, 0, 0x1c000
	v_add_u32_e32 v162, s54, v147
	v_add_u32_e32 v178, s55, v147
	ds_read_b128 v[150:153], v162
	ds_read_b128 v[154:157], v162 offset:1024
	ds_read_b128 v[158:161], v162 offset:2048
	ds_read_b128 v[162:165], v162 offset:3072
	ds_read_b128 v[166:169], v178
	ds_read_b128 v[170:173], v178 offset:1024
	ds_read_b128 v[174:177], v178 offset:2048
	ds_read_b128 v[178:181], v178 offset:3072
	s_add_u32 s26, s26, 0x40000
	s_addc_u32 s27, s27, 0
	s_mov_b32 m0, s43
	v_lshl_add_u64 v[244:245], s[26:27], 0, v[138:139]
	ds_read_b128 v[182:185], v149 offset:32768
	ds_read_b128 v[186:189], v149 offset:33792
	ds_read_b128 v[190:193], v149 offset:34816
	ds_read_b128 v[194:197], v149 offset:35840
	ds_read_b128 v[210:213], v149 offset:36864
	ds_read_b128 v[226:229], v149 offset:37888
	ds_read_b128 v[230:233], v149 offset:38912
	ds_read_b128 v[234:237], v149 offset:39936
	global_load_lds_dwordx4 v[244:245], off
	v_lshl_add_u64 v[244:245], s[26:27], 0, v[134:135]
	s_mov_b32 m0, s44
	s_nop 0
	global_load_lds_dwordx4 v[244:245], off
	s_waitcnt vmcnt(8)
	s_waitcnt lgkmcnt(0)
	s_barrier
	s_setprio 1
	s_waitcnt lgkmcnt(0)
	v_mfma_f32_16x16x32_bf16 v[128:131], v[150:153], v[182:185], v[128:131]
	v_mfma_f32_16x16x32_bf16 v[120:123], v[158:161], v[182:185], v[120:123]
	v_mfma_f32_16x16x32_bf16 v[112:115], v[150:153], v[190:193], v[112:115]
	v_mfma_f32_16x16x32_bf16 v[104:107], v[158:161], v[190:193], v[104:107]
	v_mfma_f32_16x16x32_bf16 v[96:99], v[150:153], v[210:213], v[96:99]
	v_mfma_f32_16x16x32_bf16 v[88:91], v[158:161], v[210:213], v[88:91]
	v_mfma_f32_16x16x32_bf16 v[80:83], v[150:153], v[230:233], v[80:83]
	v_mfma_f32_16x16x32_bf16 v[72:75], v[158:161], v[230:233], v[72:75]
	v_mfma_f32_16x16x32_bf16 v[128:131], v[154:157], v[186:189], v[128:131]
	v_mfma_f32_16x16x32_bf16 v[120:123], v[162:165], v[186:189], v[120:123]
	v_mfma_f32_16x16x32_bf16 v[112:115], v[154:157], v[194:197], v[112:115]
	v_mfma_f32_16x16x32_bf16 v[104:107], v[162:165], v[194:197], v[104:107]
	v_mfma_f32_16x16x32_bf16 v[96:99], v[154:157], v[226:229], v[96:99]
	v_mfma_f32_16x16x32_bf16 v[88:91], v[162:165], v[226:229], v[88:91]
	v_mfma_f32_16x16x32_bf16 v[80:83], v[154:157], v[234:237], v[80:83]
	v_mfma_f32_16x16x32_bf16 v[72:75], v[162:165], v[234:237], v[72:75]
	s_setprio 0
	s_setprio 1
	v_mfma_f32_16x16x32_bf16 v[124:127], v[166:169], v[182:185], v[124:127]
	v_mfma_f32_16x16x32_bf16 v[116:119], v[174:177], v[182:185], v[116:119]
	v_mfma_f32_16x16x32_bf16 v[108:111], v[166:169], v[190:193], v[108:111]
	v_mfma_f32_16x16x32_bf16 v[100:103], v[174:177], v[190:193], v[100:103]
	v_mfma_f32_16x16x32_bf16 v[92:95], v[166:169], v[210:213], v[92:95]
	v_mfma_f32_16x16x32_bf16 v[84:87], v[174:177], v[210:213], v[84:87]
	v_mfma_f32_16x16x32_bf16 v[76:79], v[166:169], v[230:233], v[76:79]
	v_mfma_f32_16x16x32_bf16 v[68:71], v[174:177], v[230:233], v[68:71]
	v_mfma_f32_16x16x32_bf16 v[124:127], v[170:173], v[186:189], v[124:127]
	v_mfma_f32_16x16x32_bf16 v[116:119], v[178:181], v[186:189], v[116:119]
	v_mfma_f32_16x16x32_bf16 v[108:111], v[170:173], v[194:197], v[108:111]
	v_mfma_f32_16x16x32_bf16 v[100:103], v[178:181], v[194:197], v[100:103]
	v_mfma_f32_16x16x32_bf16 v[92:95], v[170:173], v[226:229], v[92:95]
	v_mfma_f32_16x16x32_bf16 v[84:87], v[178:181], v[226:229], v[84:87]
	v_mfma_f32_16x16x32_bf16 v[76:79], v[170:173], v[234:237], v[76:79]
	v_mfma_f32_16x16x32_bf16 v[68:71], v[178:181], v[234:237], v[68:71]
	s_setprio 0
	s_barrier
	s_add_i32 s26, s54, s39
	v_lshl_add_u64 v[144:145], v[144:145], 0, s[64:65]
	s_mov_b32 m0, s26
	ds_read_b128 v[182:185], v149 offset:49152
	ds_read_b128 v[186:189], v149 offset:50176
	ds_read_b128 v[190:193], v149 offset:51200
	ds_read_b128 v[194:197], v149 offset:52224
	ds_read_b128 v[210:213], v149 offset:53248
	ds_read_b128 v[226:229], v149 offset:54272
	ds_read_b128 v[230:233], v149 offset:55296
	ds_read_b128 v[234:237], v149 offset:56320
	global_load_lds_dwordx4 v[144:145], off
	s_add_i32 m0, s26, 0x2000
	s_add_u32 s24, s24, 0x40080
	v_lshl_add_u64 v[144:145], v[238:239], 0, s[64:65]
	s_addc_u32 s25, s25, 0
	s_add_i32 s26, s55, s39
	global_load_lds_dwordx4 v[144:145], off
	v_lshl_add_u64 v[144:145], s[24:25], 0, v[136:137]
	s_mov_b32 m0, s26
	s_nop 0
	global_load_lds_dwordx4 v[144:145], off
	v_lshl_add_u64 v[144:145], s[24:25], 0, v[132:133]
	s_add_i32 m0, s26, 0x2000
	s_nop 0
	global_load_lds_dwordx4 v[144:145], off
	v_lshl_add_u64 v[144:145], v[240:241], 0, s[64:65]
	s_mov_b32 m0, s45
	s_nop 0
	global_load_lds_dwordx4 v[144:145], off
	v_lshl_add_u64 v[144:145], v[242:243], 0, s[64:65]
	s_mov_b32 m0, s46
	s_nop 0
	global_load_lds_dwordx4 v[144:145], off
	s_waitcnt vmcnt(8)
	s_waitcnt lgkmcnt(0)
	s_barrier
; #define PG8_STAGE(bufoff, gbase, voff) do { _Pragma("unroll") for (int _i = 0; _i < 2; ++_i) \
;         __builtin_amdgcn_global_load_lds((const unsigned*)((const char*)(gbase) + (voff)[_i]), (PG8_LAS unsigned*)(lds + (bufoff) + ldsw + _i * 8192), 16, 0, 0); } while (0)
; #define PG8_LDA(dst, b, h) do { _Pragma("unroll") for (int m = 0; m < 4; ++m) _Pragma("unroll") for (int k = 0; k < 2; ++k) dst[m][k] = *(const PG8_LAS bf16x8*)(lds + PG8_SA(b, h) + aoff + m * 2048 + k * 1024); } while (0)
; #define PG8_MMA(ai, bj, At, Bt) do { __builtin_amdgcn_s_setprio(1); _Pragma("unroll") for (int m = 0; m < 4; ++m) _Pragma("unroll") for (int n = 0; n < 2; ++n) _Pragma("unroll") for (int k = 0; k < 2; ++k) \
;         acc[ai][bj][m][n] = __builtin_amdgcn_mfma_f32_16x16x32_bf16(Bt[n][k], At[m][k], acc[ai][bj][m][n], 0, 0, 0); __builtin_amdgcn_s_setprio(0); } while (0)
; #define PG8_WAIT_V(n) asm volatile("s_waitcnt vmcnt(" #n ")" ::: "memory")
; #define PG8_WAIT_L(n) asm volatile("s_waitcnt lgkmcnt(" #n ")" ::: "memory")
; template <class Epi, class Sched, bool ALIGN_EPI = false, bool SP2 = false>
; __device__ __forceinline__ void gemm_phase(PG8_LAS unsigned char* lds, const Gemm g, const Sched& S, const Epi& E) {
;     ...
;             PG8_WAIT_V(8); PG8_WAIT_L(0); PG8_BAR; PG8_MMA(0, 0, At, B0); PG8_MMA(0, 1, At, B1); PG8_BAR; PG8_SCHED;
;             PG8_LDA(At, 1, 1); PG8_STAGE(PG8_SB(1, 0), b3, voffB); PG8_STAGE(PG8_SB(1, 1), b3 + hstepB, voffB); PG8_STAGE(PG8_SA(1, 0), a3, voffA);
;             PG8_WAIT_V(8); PG8_WAIT_L(0); PG8_BAR; PG8_MMA(1, 0, At, B0); PG8_MMA(1, 1, At, B1); PG8_BAR; PG8_SCHED;
;     __device__ __forceinline__ void operator()(const f32x4 (&acc)[2][2][4][2], const Unit& u, int wr, int wc, int fr, int fq) const {
;         const int row0 = u.pm * BM + wr * 64 + fr, col0 = u.pn * HALF + wc * 32 + 8 * fq;
; #pragma unroll
;         for (int ai = 0; ai < 2; ++ai)
; #pragma unroll
;             for (int m = 0; m < 4; ++m) {
;                 bf16_t* rowp = O + (size_t)(row0 + ai * HALF + m * 16) * ldc + col0;
;                 f32x4 h[2];
; #pragma unroll
;                 for (int n = 0; n < 2; ++n) { const f32x4 gt = acc[ai][0][m][n], up = acc[ai][1][m][n];
; #pragma unroll
;                     for (int e = 0; e < 4; ++e) h[n][e] = gt[e] * sigm(gt[e]) * up[e]; }
;                 *(u32x4*)rowp = pack8(h[0], h[1]);
	s_setprio 1
	s_waitcnt lgkmcnt(0)
	v_mfma_f32_16x16x32_bf16 v[64:67], v[150:153], v[182:185], v[64:67]
	v_mfma_f32_16x16x32_bf16 v[56:59], v[158:161], v[182:185], v[56:59]
	v_mfma_f32_16x16x32_bf16 v[48:51], v[150:153], v[190:193], v[48:51]
	v_mfma_f32_16x16x32_bf16 v[40:43], v[158:161], v[190:193], v[40:43]
	v_mfma_f32_16x16x32_bf16 v[32:35], v[150:153], v[210:213], v[32:35]
	v_mfma_f32_16x16x32_bf16 v[24:27], v[158:161], v[210:213], v[24:27]
	v_mfma_f32_16x16x32_bf16 v[16:19], v[150:153], v[230:233], v[16:19]
	v_mfma_f32_16x16x32_bf16 v[8:11], v[158:161], v[230:233], v[8:11]
	v_mfma_f32_16x16x32_bf16 v[64:67], v[154:157], v[186:189], v[64:67]
	v_mfma_f32_16x16x32_bf16 v[56:59], v[162:165], v[186:189], v[56:59]
	v_mfma_f32_16x16x32_bf16 v[48:51], v[154:157], v[194:197], v[48:51]
	v_mfma_f32_16x16x32_bf16 v[40:43], v[162:165], v[194:197], v[40:43]
	v_mfma_f32_16x16x32_bf16 v[32:35], v[154:157], v[226:229], v[32:35]
	v_mfma_f32_16x16x32_bf16 v[24:27], v[162:165], v[226:229], v[24:27]
	v_mfma_f32_16x16x32_bf16 v[16:19], v[154:157], v[234:237], v[16:19]
	v_mfma_f32_16x16x32_bf16 v[8:11], v[162:165], v[234:237], v[8:11]
	s_setprio 0
	s_setprio 1
	v_mfma_f32_16x16x32_bf16 v[60:63], v[166:169], v[182:185], v[60:63]
	v_mfma_f32_16x16x32_bf16 v[52:55], v[174:177], v[182:185], v[52:55]
	v_mfma_f32_16x16x32_bf16 v[44:47], v[166:169], v[190:193], v[44:47]
	v_mfma_f32_16x16x32_bf16 v[36:39], v[174:177], v[190:193], v[36:39]
	v_mfma_f32_16x16x32_bf16 v[28:31], v[166:169], v[210:213], v[28:31]
	v_mfma_f32_16x16x32_bf16 v[20:23], v[174:177], v[210:213], v[20:23]
	v_mfma_f32_16x16x32_bf16 v[12:15], v[166:169], v[230:233], v[12:15]
	v_mfma_f32_16x16x32_bf16 v[4:7], v[174:177], v[230:233], v[4:7]
	v_mfma_f32_16x16x32_bf16 v[60:63], v[170:173], v[186:189], v[60:63]
	v_mfma_f32_16x16x32_bf16 v[52:55], v[178:181], v[186:189], v[52:55]
	v_mfma_f32_16x16x32_bf16 v[44:47], v[170:173], v[194:197], v[44:47]
	v_mfma_f32_16x16x32_bf16 v[36:39], v[178:181], v[194:197], v[36:39]
	v_mfma_f32_16x16x32_bf16 v[28:31], v[170:173], v[226:229], v[28:31]
	v_mfma_f32_16x16x32_bf16 v[20:23], v[178:181], v[226:229], v[20:23]
	v_mfma_f32_16x16x32_bf16 v[12:15], v[170:173], v[234:237], v[12:15]
	v_mfma_f32_16x16x32_bf16 v[4:7], v[178:181], v[234:237], v[4:7]
	s_setprio 0
	s_barrier
	s_add_i32 s53, s53, 2
	s_add_u32 s51, s51, 0x100
	s_addc_u32 s52, s52, 0
	s_add_u32 s22, s22, 0x100
	s_addc_u32 s23, s23, 0
	s_cmp_gt_u32 s53, 13
	s_cbranch_scc0 .LBB0_153
.Lpeel_exit_0:
	s_and_b64 vcc, exec, s[10:11]
	s_cbranch_vccz .LBB0_156
	s_barrier
.LBB0_156:
	v_pk_mul_f32 v[160:161], v[128:129], s[82:83] op_sel:[0,1] op_sel_hi:[1,1]
	v_pk_mul_f32 v[162:163], v[130:131], s[82:83] op_sel:[0,1] op_sel_hi:[1,1]
	v_pk_mul_f32 v[164:165], v[120:121], s[82:83] op_sel:[0,1] op_sel_hi:[1,1]
	v_pk_mul_f32 v[166:167], v[122:123], s[82:83] op_sel:[0,1] op_sel_hi:[1,1]
	v_exp_f32_e32 v160, v160
	v_exp_f32_e32 v161, v161
	v_exp_f32_e32 v162, v162
	v_exp_f32_e32 v163, v163
	v_exp_f32_e32 v164, v164
	v_exp_f32_e32 v165, v165
	v_exp_f32_e32 v166, v166
	v_exp_f32_e32 v167, v167
	v_pk_add_f32 v[160:161], v[160:161], 1.0 op_sel_hi:[1,0]
	v_pk_add_f32 v[162:163], v[162:163], 1.0 op_sel_hi:[1,0]
	v_pk_add_f32 v[164:165], v[164:165], 1.0 op_sel_hi:[1,0]
	v_pk_add_f32 v[166:167], v[166:167], 1.0 op_sel_hi:[1,0]
	v_rcp_f32_e32 v160, v160
	v_rcp_f32_e32 v161, v161
	v_rcp_f32_e32 v162, v162
	v_rcp_f32_e32 v163, v163
	v_rcp_f32_e32 v164, v164
	v_rcp_f32_e32 v165, v165
	v_rcp_f32_e32 v166, v166
	v_rcp_f32_e32 v167, v167
	v_pk_mul_f32 v[160:161], v[128:129], v[160:161]
	v_pk_mul_f32 v[162:163], v[130:131], v[162:163]
	v_pk_mul_f32 v[164:165], v[120:121], v[164:165]
	v_pk_mul_f32 v[166:167], v[122:123], v[166:167]
	v_pk_mul_f32 v[124:125], v[160:161], v[124:125]
	v_pk_mul_f32 v[126:127], v[162:163], v[126:127]
	v_pk_mul_f32 v[120:121], v[164:165], v[116:117]
	v_pk_mul_f32 v[128:129], v[166:167], v[118:119]
	v_lshl_or_b32 v152, s21, 7, v148
	v_lshl_add_u32 v150, s20, 8, v2
	v_ashrrev_i32_e32 v153, 31, v152
	v_mov_b64_e32 v[144:145], s[8:9]
	v_mad_i64_i32 v[154:155], s[20:21], v150, s82, v[144:145]
	s_andn2_b64 vcc, exec, s[2:3]
	v_lshlrev_b64 v[116:117], 1, v[152:153]
	v_lshl_add_u64 v[122:123], v[154:155], 0, v[116:117]
	v_cvt_pk_bf16_f32 v118, v124, v125
	v_cvt_pk_bf16_f32 v119, v126, v127
	v_cvt_pk_bf16_f32 v120, v120, v121
	v_cvt_pk_bf16_f32 v121, v128, v129
	flat_store_dwordx4 v[122:123], v[118:121] sc1
	s_nop 1
	v_pk_mul_f32 v[160:161], v[112:113], s[82:83] op_sel:[0,1] op_sel_hi:[1,1]
	v_pk_mul_f32 v[162:163], v[114:115], s[82:83] op_sel:[0,1] op_sel_hi:[1,1]
	v_pk_mul_f32 v[164:165], v[104:105], s[82:83] op_sel:[0,1] op_sel_hi:[1,1]
	v_pk_mul_f32 v[166:167], v[106:107], s[82:83] op_sel:[0,1] op_sel_hi:[1,1]
	v_exp_f32_e32 v160, v160
	v_exp_f32_e32 v161, v161
	v_exp_f32_e32 v162, v162
	v_exp_f32_e32 v163, v163
	v_exp_f32_e32 v164, v164
	v_exp_f32_e32 v165, v165
	v_exp_f32_e32 v166, v166
	v_exp_f32_e32 v167, v167
	v_pk_add_f32 v[160:161], v[160:161], 1.0 op_sel_hi:[1,0]
	v_pk_add_f32 v[162:163], v[162:163], 1.0 op_sel_hi:[1,0]
	v_pk_add_f32 v[164:165], v[164:165], 1.0 op_sel_hi:[1,0]
	v_pk_add_f32 v[166:167], v[166:167], 1.0 op_sel_hi:[1,0]
	v_rcp_f32_e32 v160, v160
	v_rcp_f32_e32 v161, v161
	v_rcp_f32_e32 v162, v162
	v_rcp_f32_e32 v163, v163
	v_rcp_f32_e32 v164, v164
	v_rcp_f32_e32 v165, v165
	v_rcp_f32_e32 v166, v166
	v_rcp_f32_e32 v167, v167
	v_pk_mul_f32 v[160:161], v[112:113], v[160:161]
	v_pk_mul_f32 v[162:163], v[114:115], v[162:163]
	v_pk_mul_f32 v[164:165], v[104:105], v[164:165]
	v_pk_mul_f32 v[166:167], v[106:107], v[166:167]
	v_pk_mul_f32 v[108:109], v[160:161], v[108:109]
	v_pk_mul_f32 v[110:111], v[162:163], v[110:111]
; __device__ __forceinline__ float sigm(float x) { return __builtin_amdgcn_rcpf(1.0f + __builtin_amdgcn_exp2f(-1.4426950408889634f * x)); }
; __device__ __forceinline__ u32x4 pack8(const f32x4 a, const f32x4 b) { u32x4 w; w.x = cvt_pk_bf16(a[0], a[1]); w.y = cvt_pk_bf16(a[2], a[3]); w.z = cvt_pk_bf16(b[0], b[1]); w.w = cvt_pk_bf16(b[2], b[3]); return w; }
;     __device__ __forceinline__ void operator()(const f32x4 (&acc)[2][2][4][2], const Unit& u, int wr, int wc, int fr, int fq) const {
;     ...
;             for (int m = 0; m < 4; ++m) {
;                 bf16_t* rowp = O + (size_t)(row0 + ai * HALF + m * 16) * ldc + col0;
;                 f32x4 h[2];
; #pragma unroll
;                 for (int n = 0; n < 2; ++n) { const f32x4 gt = acc[ai][0][m][n], up = acc[ai][1][m][n];
; #pragma unroll
;                     for (int e = 0; e < 4; ++e) h[n][e] = gt[e] * sigm(gt[e]) * up[e]; }
;                 *(u32x4*)rowp = pack8(h[0], h[1]);
	v_pk_mul_f32 v[112:113], v[164:165], v[100:101]
	v_mul_f32_e32 v106, v166, v102
	v_mul_f32_e32 v103, v167, v103
	v_or_b32_e32 v118, 16, v150
	v_mad_i64_i32 v[118:119], s[20:21], v118, s82, v[144:145]
	v_lshl_add_u64 v[104:105], v[118:119], 0, v[116:117]
	v_cvt_pk_bf16_f32 v100, v108, v109
	v_cvt_pk_bf16_f32 v101, v110, v111
	v_cvt_pk_bf16_f32 v102, v112, v113
	v_cvt_pk_bf16_f32 v103, v106, v103
	flat_store_dwordx4 v[104:105], v[100:103] sc1
	s_nop 1
	v_pk_mul_f32 v[160:161], v[96:97], s[82:83] op_sel:[0,1] op_sel_hi:[1,1]
	v_pk_mul_f32 v[162:163], v[98:99], s[82:83] op_sel:[0,1] op_sel_hi:[1,1]
	v_pk_mul_f32 v[164:165], v[88:89], s[82:83] op_sel:[0,1] op_sel_hi:[1,1]
	v_pk_mul_f32 v[166:167], v[90:91], s[82:83] op_sel:[0,1] op_sel_hi:[1,1]
	v_exp_f32_e32 v160, v160
	v_exp_f32_e32 v161, v161
	v_exp_f32_e32 v162, v162
	v_exp_f32_e32 v163, v163
	v_exp_f32_e32 v164, v164
	v_exp_f32_e32 v165, v165
	v_exp_f32_e32 v166, v166
	v_exp_f32_e32 v167, v167
	v_pk_add_f32 v[160:161], v[160:161], 1.0 op_sel_hi:[1,0]
	v_pk_add_f32 v[162:163], v[162:163], 1.0 op_sel_hi:[1,0]
	v_pk_add_f32 v[164:165], v[164:165], 1.0 op_sel_hi:[1,0]
	v_pk_add_f32 v[166:167], v[166:167], 1.0 op_sel_hi:[1,0]
	v_rcp_f32_e32 v160, v160
	v_rcp_f32_e32 v161, v161
	v_rcp_f32_e32 v162, v162
	v_rcp_f32_e32 v163, v163
	v_rcp_f32_e32 v164, v164
	v_rcp_f32_e32 v165, v165
	v_rcp_f32_e32 v166, v166
	v_rcp_f32_e32 v167, v167
	v_pk_mul_f32 v[160:161], v[96:97], v[160:161]
	v_pk_mul_f32 v[162:163], v[98:99], v[162:163]
	v_pk_mul_f32 v[164:165], v[88:89], v[164:165]
	v_pk_mul_f32 v[166:167], v[90:91], v[166:167]
	v_pk_mul_f32 v[92:93], v[160:161], v[92:93]
	v_pk_mul_f32 v[94:95], v[162:163], v[94:95]
	v_pk_mul_f32 v[96:97], v[164:165], v[84:85]
	v_mul_f32_e32 v90, v166, v86
	v_mul_f32_e32 v87, v167, v87
	v_or_b32_e32 v100, 32, v150
	v_mad_i64_i32 v[100:101], s[20:21], v100, s82, v[144:145]
	v_lshl_add_u64 v[88:89], v[100:101], 0, v[116:117]
	v_cvt_pk_bf16_f32 v84, v92, v93
	v_cvt_pk_bf16_f32 v85, v94, v95
	v_cvt_pk_bf16_f32 v86, v96, v97
	v_cvt_pk_bf16_f32 v87, v90, v87
	flat_store_dwordx4 v[88:89], v[84:87] sc1
	s_nop 1
	v_pk_mul_f32 v[160:161], v[80:81], s[82:83] op_sel:[0,1] op_sel_hi:[1,1]
	v_pk_mul_f32 v[162:163], v[82:83], s[82:83] op_sel:[0,1] op_sel_hi:[1,1]
	v_pk_mul_f32 v[164:165], v[72:73], s[82:83] op_sel:[0,1] op_sel_hi:[1,1]
	v_pk_mul_f32 v[166:167], v[74:75], s[82:83] op_sel:[0,1] op_sel_hi:[1,1]
	v_exp_f32_e32 v160, v160
	v_exp_f32_e32 v161, v161
	v_exp_f32_e32 v162, v162
	v_exp_f32_e32 v163, v163
	v_exp_f32_e32 v164, v164
	v_exp_f32_e32 v165, v165
	v_exp_f32_e32 v166, v166
	v_exp_f32_e32 v167, v167
	v_pk_add_f32 v[160:161], v[160:161], 1.0 op_sel_hi:[1,0]
	v_pk_add_f32 v[162:163], v[162:163], 1.0 op_sel_hi:[1,0]
	v_pk_add_f32 v[164:165], v[164:165], 1.0 op_sel_hi:[1,0]
	v_pk_add_f32 v[166:167], v[166:167], 1.0 op_sel_hi:[1,0]
	v_rcp_f32_e32 v160, v160
	v_rcp_f32_e32 v161, v161
	v_rcp_f32_e32 v162, v162
	v_rcp_f32_e32 v163, v163
	v_rcp_f32_e32 v164, v164
	v_rcp_f32_e32 v165, v165
	v_rcp_f32_e32 v166, v166
	v_rcp_f32_e32 v167, v167
	v_pk_mul_f32 v[160:161], v[80:81], v[160:161]
	v_pk_mul_f32 v[162:163], v[82:83], v[162:163]
	v_pk_mul_f32 v[164:165], v[72:73], v[164:165]
	v_pk_mul_f32 v[166:167], v[74:75], v[166:167]
	v_pk_mul_f32 v[76:77], v[160:161], v[76:77]
	v_pk_mul_f32 v[78:79], v[162:163], v[78:79]
	v_pk_mul_f32 v[80:81], v[164:165], v[68:69]
	v_mul_f32_e32 v74, v166, v70
	v_mul_f32_e32 v71, v167, v71
	v_or_b32_e32 v84, 48, v150
	v_mad_i64_i32 v[84:85], s[20:21], v84, s82, v[144:145]
	v_lshl_add_u64 v[72:73], v[84:85], 0, v[116:117]
	v_cvt_pk_bf16_f32 v68, v76, v77
	v_cvt_pk_bf16_f32 v69, v78, v79
	v_cvt_pk_bf16_f32 v70, v80, v81
	v_cvt_pk_bf16_f32 v71, v74, v71
	flat_store_dwordx4 v[72:73], v[68:71] sc1
	s_nop 1
	v_pk_mul_f32 v[160:161], v[64:65], s[82:83] op_sel:[0,1] op_sel_hi:[1,1]
	v_pk_mul_f32 v[162:163], v[66:67], s[82:83] op_sel:[0,1] op_sel_hi:[1,1]
	v_pk_mul_f32 v[164:165], v[56:57], s[82:83] op_sel:[0,1] op_sel_hi:[1,1]
	v_pk_mul_f32 v[166:167], v[58:59], s[82:83] op_sel:[0,1] op_sel_hi:[1,1]
	v_exp_f32_e32 v160, v160
	v_exp_f32_e32 v161, v161
	v_exp_f32_e32 v162, v162
	v_exp_f32_e32 v163, v163
	v_exp_f32_e32 v164, v164
	v_exp_f32_e32 v165, v165
	v_exp_f32_e32 v166, v166
	v_exp_f32_e32 v167, v167
	v_pk_add_f32 v[160:161], v[160:161], 1.0 op_sel_hi:[1,0]
	v_pk_add_f32 v[162:163], v[162:163], 1.0 op_sel_hi:[1,0]
	v_pk_add_f32 v[164:165], v[164:165], 1.0 op_sel_hi:[1,0]
	v_pk_add_f32 v[166:167], v[166:167], 1.0 op_sel_hi:[1,0]
	v_rcp_f32_e32 v160, v160
	v_rcp_f32_e32 v161, v161
	v_rcp_f32_e32 v162, v162
	v_rcp_f32_e32 v163, v163
	v_rcp_f32_e32 v164, v164
	v_rcp_f32_e32 v165, v165
	v_rcp_f32_e32 v166, v166
	v_rcp_f32_e32 v167, v167
	v_pk_mul_f32 v[160:161], v[64:65], v[160:161]
	v_pk_mul_f32 v[162:163], v[66:67], v[162:163]
	v_pk_mul_f32 v[164:165], v[56:57], v[164:165]
	v_pk_mul_f32 v[166:167], v[58:59], v[166:167]
	v_pk_mul_f32 v[60:61], v[160:161], v[60:61]
	v_pk_mul_f32 v[62:63], v[162:163], v[62:63]
	v_pk_mul_f32 v[64:65], v[164:165], v[52:53]
	v_mul_f32_e32 v58, v166, v54
	v_mul_f32_e32 v55, v167, v55
	v_add_u32_e32 v68, 0x80, v150
	v_mad_i64_i32 v[68:69], s[20:21], v68, s82, v[144:145]
	v_lshl_add_u64 v[56:57], v[68:69], 0, v[116:117]
; __device__ __forceinline__ float sigm(float x) { return __builtin_amdgcn_rcpf(1.0f + __builtin_amdgcn_exp2f(-1.4426950408889634f * x)); }
; __device__ __forceinline__ u32x4 pack8(const f32x4 a, const f32x4 b) { u32x4 w; w.x = cvt_pk_bf16(a[0], a[1]); w.y = cvt_pk_bf16(a[2], a[3]); w.z = cvt_pk_bf16(b[0], b[1]); w.w = cvt_pk_bf16(b[2], b[3]); return w; }
;     __device__ __forceinline__ void operator()(const f32x4 (&acc)[2][2][4][2], const Unit& u, int wr, int wc, int fr, int fq) const {
;     ...
;         for (int ai = 0; ai < 2; ++ai)
; #pragma unroll
;             for (int m = 0; m < 4; ++m) {
;                 bf16_t* rowp = O + (size_t)(row0 + ai * HALF + m * 16) * ldc + col0;
;                 f32x4 h[2];
; #pragma unroll
;                 for (int n = 0; n < 2; ++n) { const f32x4 gt = acc[ai][0][m][n], up = acc[ai][1][m][n];
; #pragma unroll
;                     for (int e = 0; e < 4; ++e) h[n][e] = gt[e] * sigm(gt[e]) * up[e]; }
;                 *(u32x4*)rowp = pack8(h[0], h[1]);
	v_cvt_pk_bf16_f32 v52, v60, v61
	v_cvt_pk_bf16_f32 v53, v62, v63
	v_cvt_pk_bf16_f32 v54, v64, v65
	v_cvt_pk_bf16_f32 v55, v58, v55
	flat_store_dwordx4 v[56:57], v[52:55] sc1
	s_nop 1
	v_pk_mul_f32 v[160:161], v[48:49], s[82:83] op_sel:[0,1] op_sel_hi:[1,1]
	v_pk_mul_f32 v[162:163], v[50:51], s[82:83] op_sel:[0,1] op_sel_hi:[1,1]
	v_pk_mul_f32 v[164:165], v[40:41], s[82:83] op_sel:[0,1] op_sel_hi:[1,1]
	v_pk_mul_f32 v[166:167], v[42:43], s[82:83] op_sel:[0,1] op_sel_hi:[1,1]
	v_exp_f32_e32 v160, v160
	v_exp_f32_e32 v161, v161
	v_exp_f32_e32 v162, v162
	v_exp_f32_e32 v163, v163
	v_exp_f32_e32 v164, v164
	v_exp_f32_e32 v165, v165
	v_exp_f32_e32 v166, v166
	v_exp_f32_e32 v167, v167
	v_pk_add_f32 v[160:161], v[160:161], 1.0 op_sel_hi:[1,0]
	v_pk_add_f32 v[162:163], v[162:163], 1.0 op_sel_hi:[1,0]
	v_pk_add_f32 v[164:165], v[164:165], 1.0 op_sel_hi:[1,0]
	v_pk_add_f32 v[166:167], v[166:167], 1.0 op_sel_hi:[1,0]
	v_rcp_f32_e32 v160, v160
	v_rcp_f32_e32 v161, v161
	v_rcp_f32_e32 v162, v162
	v_rcp_f32_e32 v163, v163
	v_rcp_f32_e32 v164, v164
	v_rcp_f32_e32 v165, v165
	v_rcp_f32_e32 v166, v166
	v_rcp_f32_e32 v167, v167
	v_pk_mul_f32 v[160:161], v[48:49], v[160:161]
	v_pk_mul_f32 v[162:163], v[50:51], v[162:163]
	v_pk_mul_f32 v[164:165], v[40:41], v[164:165]
	v_pk_mul_f32 v[166:167], v[42:43], v[166:167]
	v_pk_mul_f32 v[44:45], v[160:161], v[44:45]
	v_pk_mul_f32 v[46:47], v[162:163], v[46:47]
	v_pk_mul_f32 v[48:49], v[164:165], v[36:37]
	v_mul_f32_e32 v42, v166, v38
	v_mul_f32_e32 v39, v167, v39
	v_add_u32_e32 v52, 0x90, v150
	v_mad_i64_i32 v[52:53], s[20:21], v52, s82, v[144:145]
	v_lshl_add_u64 v[40:41], v[52:53], 0, v[116:117]
	v_cvt_pk_bf16_f32 v36, v44, v45
	v_cvt_pk_bf16_f32 v37, v46, v47
	v_cvt_pk_bf16_f32 v38, v48, v49
	v_cvt_pk_bf16_f32 v39, v42, v39
	flat_store_dwordx4 v[40:41], v[36:39] sc1
	s_nop 1
	v_pk_mul_f32 v[160:161], v[32:33], s[82:83] op_sel:[0,1] op_sel_hi:[1,1]
	v_pk_mul_f32 v[162:163], v[34:35], s[82:83] op_sel:[0,1] op_sel_hi:[1,1]
	v_pk_mul_f32 v[164:165], v[24:25], s[82:83] op_sel:[0,1] op_sel_hi:[1,1]
	v_pk_mul_f32 v[166:167], v[26:27], s[82:83] op_sel:[0,1] op_sel_hi:[1,1]
	v_exp_f32_e32 v160, v160
	v_exp_f32_e32 v161, v161
	v_exp_f32_e32 v162, v162
	v_exp_f32_e32 v163, v163
	v_exp_f32_e32 v164, v164
	v_exp_f32_e32 v165, v165
	v_exp_f32_e32 v166, v166
	v_exp_f32_e32 v167, v167
	v_pk_add_f32 v[160:161], v[160:161], 1.0 op_sel_hi:[1,0]
	v_pk_add_f32 v[162:163], v[162:163], 1.0 op_sel_hi:[1,0]
	v_pk_add_f32 v[164:165], v[164:165], 1.0 op_sel_hi:[1,0]
	v_pk_add_f32 v[166:167], v[166:167], 1.0 op_sel_hi:[1,0]
	v_rcp_f32_e32 v160, v160
	v_rcp_f32_e32 v161, v161
	v_rcp_f32_e32 v162, v162
	v_rcp_f32_e32 v163, v163
	v_rcp_f32_e32 v164, v164
	v_rcp_f32_e32 v165, v165
	v_rcp_f32_e32 v166, v166
	v_rcp_f32_e32 v167, v167
	v_pk_mul_f32 v[160:161], v[32:33], v[160:161]
	v_pk_mul_f32 v[162:163], v[34:35], v[162:163]
	v_pk_mul_f32 v[164:165], v[24:25], v[164:165]
	v_pk_mul_f32 v[166:167], v[26:27], v[166:167]
	v_pk_mul_f32 v[28:29], v[160:161], v[28:29]
	v_pk_mul_f32 v[30:31], v[162:163], v[30:31]
	v_pk_mul_f32 v[32:33], v[164:165], v[20:21]
	v_mul_f32_e32 v26, v166, v22
	v_mul_f32_e32 v23, v167, v23
	v_add_u32_e32 v36, 0xa0, v150
	v_mad_i64_i32 v[36:37], s[20:21], v36, s82, v[144:145]
	v_lshl_add_u64 v[24:25], v[36:37], 0, v[116:117]
	v_cvt_pk_bf16_f32 v20, v28, v29
	v_cvt_pk_bf16_f32 v21, v30, v31
	v_cvt_pk_bf16_f32 v22, v32, v33
	v_cvt_pk_bf16_f32 v23, v26, v23
	flat_store_dwordx4 v[24:25], v[20:23] sc1
	s_nop 1
	v_pk_mul_f32 v[160:161], v[16:17], s[82:83] op_sel:[0,1] op_sel_hi:[1,1]
	v_pk_mul_f32 v[162:163], v[18:19], s[82:83] op_sel:[0,1] op_sel_hi:[1,1]
	v_pk_mul_f32 v[164:165], v[8:9], s[82:83] op_sel:[0,1] op_sel_hi:[1,1]
	v_pk_mul_f32 v[166:167], v[10:11], s[82:83] op_sel:[0,1] op_sel_hi:[1,1]
	v_exp_f32_e32 v160, v160
	v_exp_f32_e32 v161, v161
	v_exp_f32_e32 v162, v162
	v_exp_f32_e32 v163, v163
	v_exp_f32_e32 v164, v164
	v_exp_f32_e32 v165, v165
	v_exp_f32_e32 v166, v166
	v_exp_f32_e32 v167, v167
	v_pk_add_f32 v[160:161], v[160:161], 1.0 op_sel_hi:[1,0]
	v_pk_add_f32 v[162:163], v[162:163], 1.0 op_sel_hi:[1,0]
	v_pk_add_f32 v[164:165], v[164:165], 1.0 op_sel_hi:[1,0]
	v_pk_add_f32 v[166:167], v[166:167], 1.0 op_sel_hi:[1,0]
	v_rcp_f32_e32 v160, v160
	v_rcp_f32_e32 v161, v161
	v_rcp_f32_e32 v162, v162
	v_rcp_f32_e32 v163, v163
	v_rcp_f32_e32 v164, v164
	v_rcp_f32_e32 v165, v165
	v_rcp_f32_e32 v166, v166
	v_rcp_f32_e32 v167, v167
	v_pk_mul_f32 v[160:161], v[16:17], v[160:161]
	v_pk_mul_f32 v[162:163], v[18:19], v[162:163]
	v_pk_mul_f32 v[164:165], v[8:9], v[164:165]
	v_pk_mul_f32 v[166:167], v[10:11], v[166:167]
	v_pk_mul_f32 v[12:13], v[160:161], v[12:13]
	v_pk_mul_f32 v[14:15], v[162:163], v[14:15]
	v_pk_mul_f32 v[16:17], v[164:165], v[4:5]
	v_mul_f32_e32 v10, v166, v6
	v_mul_f32_e32 v7, v167, v7
	v_add_u32_e32 v20, 0xb0, v150
	v_mad_i64_i32 v[20:21], s[20:21], v20, s82, v[144:145]
	s_mov_b64 s[20:21], -1
	v_lshl_add_u64 v[8:9], v[20:21], 0, v[116:117]
	v_cvt_pk_bf16_f32 v4, v12, v13
	v_cvt_pk_bf16_f32 v5, v14, v15
	v_cvt_pk_bf16_f32 v6, v16, v17
	v_cvt_pk_bf16_f32 v7, v10, v7
	flat_store_dwordx4 v[8:9], v[4:7] sc1
	s_cbranch_vccnz .LBB0_149
	s_andn2_b64 vcc, exec, s[6:7]
	s_cbranch_vccnz .LBB0_148
	s_barrier
	s_branch .LBB0_148

; #define GAS __attribute__((address_space(1)))
; #define LAS __attribute__((address_space(3)))
; #define LDS_WAIT() asm volatile("s_waitcnt lgkmcnt(0)" ::: "memory")
; __device__ __forceinline__ unsigned pk2(float lo, float hi) { unsigned r; asm("v_cvt_pk_bf16_f32 %0, %1, %2" : "=v"(r) : "v"(lo), "v"(hi)); return r; }
; __device__ __forceinline__ void transpose_item(const float* W, int K, int N, bf16* WT, int drow0, int kb, int n0, LAS float* scr, int lane) {
;     const int k0 = 64 * kb; const int c4 = 4 * (lane & 7); const bool ok = (n0 + c4) < N;
;     f32x4 v[8];
; #pragma unroll
;     for (int i = 0; i < 8; ++i) { const int kk = 8 * i + (lane >> 3); v[i] = ok ? *(const f32x4*)(W + (size_t)(k0 + kk) * N + n0 + c4) : (f32x4){0.f, 0.f, 0.f, 0.f}; }
; #pragma unroll
;     for (int i = 0; i < 8; ++i) { const int kk = 8 * i + (lane >> 3); LAS float* d = scr + kk * 33 + c4; d[0] = v[i][0]; d[1] = v[i][1]; d[2] = v[i][2]; d[3] = v[i][3]; }
;     LDS_WAIT(); asm volatile("" ::: "memory");
;     const int c = lane & 7;
; #pragma unroll
;     for (int j = 0; j < 4; ++j) { const int n = (lane >> 3) + 8 * j; const LAS float* s = scr + (8 * c) * 33 + n;
;         v4u o; o.x = pk2(s[0 * 33], s[1 * 33]); o.y = pk2(s[2 * 33], s[3 * 33]); o.z = pk2(s[4 * 33], s[5 * 33]); o.w = pk2(s[6 * 33], s[7 * 33]);
;         *(GAS v4u*)(WT + (size_t)(drow0 + n) * K + k0 + 8 * c) = o; }
;     LDS_WAIT(); asm volatile("" ::: "memory");
; }
; __device__ __forceinline__ void convert_item(const In& I, unsigned char* ws, int it, LAS float* scr, int lane) {
;     ...
;     { const int jk = r >> 3; r &= 7; const int kb = r >> 1, nb = r & 1;
;         transpose_item(I.nsa_w2 + (size_t)jk * 256 * 64, 256, 64, W2t + (size_t)jk * 64 * 256, 32 * nb, kb, 32 * nb, scr, lane); }
.LBB0_167:
	s_add_i32 s45, s40, 0xa800
	s_cmp_gt_i32 s45, 0x83ff
	s_mov_b64 s[2:3], -1
	s_cbranch_scc0 .LBB0_221
	s_cmpk_gt_u32 s45, 0x8eff
	s_cbranch_scc0 .LBB0_202
	s_cmpk_gt_u32 s45, 0x92ff
	s_cbranch_scc0 .LBB0_199
	s_cmpk_gt_u32 s45, 0x9fff
	s_cbranch_scc0 .LBB0_180
	s_cmpk_gt_u32 s45, 0xa3ff
	s_cbranch_scc0 .LBB0_177
	s_cmpk_gt_u32 s45, 0xa7ff
	s_cbranch_scc0 .LBB0_174
	s_lshr_b32 s68, s40, 3
	v_readlane_b32 s48, v253, 16
	s_lshl_b64 s[2:3], s[68:69], 16
	v_readlane_b32 s52, v253, 20
	v_readlane_b32 s53, v253, 21
	s_add_u32 s6, s52, s2
	s_addc_u32 s7, s53, s3
	s_lshl_b64 s[2:3], s[68:69], 15
	s_add_u32 s8, s35, s2
	s_addc_u32 s3, s39, s3
	s_and_b32 s2, s42, 32
	s_and_b32 s9, s42, 0xc0
	s_lshl_b32 s10, s2, 2
	s_add_u32 s6, s6, s10
	v_or_b32_e32 v6, s9, v39
	s_addc_u32 s7, s7, 0
	v_lshlrev_b32_e32 v2, 2, v36
	v_lshl_add_u64 v[4:5], s[6:7], 0, v[2:3]
	v_lshlrev_b32_e32 v2, 8, v6
	v_lshl_add_u64 v[28:29], v[4:5], 0, v[2:3]
	global_load_dwordx4 v[4:7], v[28:29], off
	global_load_dwordx4 v[8:11], v[28:29], off offset:2048
	v_add_co_u32_e32 v16, vcc, s84, v28
	s_movk_i32 s6, 0x3000
	s_nop 0
	v_addc_co_u32_e32 v17, vcc, 0, v29, vcc
	v_add_co_u32_e32 v24, vcc, s74, v28
	v_add_u32_e32 v2, v44, v45
	s_nop 0
	v_addc_co_u32_e32 v25, vcc, 0, v29, vcc
	global_load_dwordx4 v[12:15], v[24:25], off offset:-4096
	s_nop 0
	global_load_dwordx4 v[16:19], v[16:17], off offset:2048
	s_nop 0
	global_load_dwordx4 v[20:23], v[24:25], off
	s_nop 0
	global_load_dwordx4 v[24:27], v[24:25], off offset:2048
	v_add_co_u32_e32 v32, vcc, s6, v28
	s_lshl_b32 s6, s9, 1
	s_nop 0
	v_addc_co_u32_e32 v33, vcc, 0, v29, vcc
	global_load_dwordx4 v[28:31], v[32:33], off
	s_nop 0
	global_load_dwordx4 v[32:35], v[32:33], off offset:2048
	s_add_u32 s6, s8, s6
	s_addc_u32 s7, s3, 0
	v_readlane_b32 s49, v253, 17
	v_readlane_b32 s50, v253, 18
	v_readlane_b32 s51, v253, 19
	v_readlane_b32 s54, v253, 22
	v_readlane_b32 s55, v253, 23
	v_readlane_b32 s56, v253, 24
	v_readlane_b32 s57, v253, 25
	v_readlane_b32 s58, v253, 26
	v_readlane_b32 s59, v253, 27
	v_readlane_b32 s60, v253, 28
	v_readlane_b32 s61, v253, 29
	v_readlane_b32 s62, v253, 30
	v_readlane_b32 s63, v253, 31
	s_waitcnt vmcnt(0)
	ds_write2_b32 v2, v4, v5 offset1:1
	ds_write2_b32 v2, v6, v7 offset0:2 offset1:3
	v_add_u32_e32 v4, 0x420, v2
	ds_write2_b32 v4, v8, v9 offset1:1
	v_add_u32_e32 v4, 0x428, v2
	ds_write2_b32 v4, v10, v11 offset1:1
	v_add_u32_e32 v4, 0x840, v2
	ds_write2_b32 v4, v12, v13 offset1:1
	v_add_u32_e32 v4, 0x848, v2
	ds_write2_b32 v4, v14, v15 offset1:1
	v_add_u32_e32 v4, 0xc60, v2
	ds_write2_b32 v4, v16, v17 offset1:1
	v_add_u32_e32 v4, 0xc68, v2
	ds_write2_b32 v4, v18, v19 offset1:1
	v_add_u32_e32 v4, 0x1080, v2
	ds_write2_b32 v4, v20, v21 offset1:1
	v_add_u32_e32 v4, 0x1088, v2
	ds_write2_b32 v4, v22, v23 offset1:1
	v_add_u32_e32 v4, 0x14a0, v2
	ds_write2_b32 v4, v24, v25 offset1:1
	v_add_u32_e32 v4, 0x14a8, v2
	ds_write2_b32 v4, v26, v27 offset1:1
	v_add_u32_e32 v4, 0x18c0, v2
	ds_write2_b32 v4, v28, v29 offset1:1
	v_add_u32_e32 v4, 0x18c8, v2
	ds_write2_b32 v4, v30, v31 offset1:1
	v_add_u32_e32 v4, 0x1ce0, v2
	v_add_u32_e32 v2, 0x1ce8, v2
	ds_write2_b32 v4, v32, v33 offset1:1
	ds_write2_b32 v2, v34, v35 offset1:1
	s_waitcnt lgkmcnt(0)
	ds_read2_b32 v[10:11], v49 offset0:33 offset1:41
	ds_read2_b32 v[12:13], v49 offset1:8
	v_lshlrev_b32_e32 v2, 1, v38
	ds_read2_b32 v[14:15], v49 offset0:66 offset1:74
	ds_read2_b32 v[16:17], v49 offset0:99 offset1:107
	ds_read2_b32 v[18:19], v49 offset0:132 offset1:140
	ds_read2_b32 v[20:21], v49 offset0:165 offset1:173
	ds_read2_b32 v[22:23], v49 offset0:198 offset1:206
	ds_read2_b32 v[24:25], v49 offset0:231 offset1:239
	v_lshl_add_u64 v[4:5], s[6:7], 0, v[2:3]
	v_or_b32_e32 v2, s2, v39
	v_lshlrev_b32_e32 v2, 9, v2
	v_lshl_add_u64 v[26:27], v[4:5], 0, v[2:3]
	v_or_b32_e32 v2, s2, v46
	s_waitcnt lgkmcnt(0)
	v_cvt_pk_bf16_f32 v6, v12, v10
	v_lshlrev_b32_e32 v2, 9, v2
	v_cvt_pk_bf16_f32 v7, v14, v16
	v_cvt_pk_bf16_f32 v8, v18, v20
	v_cvt_pk_bf16_f32 v9, v22, v24
	global_store_dwordx4 v[26:27], v[6:9], off sc1
	s_nop 1
	v_cvt_pk_bf16_f32 v6, v13, v11
	v_lshl_add_u64 v[10:11], v[4:5], 0, v[2:3]
	v_cvt_pk_bf16_f32 v7, v15, v17
	v_cvt_pk_bf16_f32 v8, v19, v21
	v_cvt_pk_bf16_f32 v9, v23, v25
	global_store_dwordx4 v[10:11], v[6:9], off sc1
	ds_read2_b32 v[10:11], v49 offset0:16 offset1:24
	ds_read2_b32 v[12:13], v49 offset0:49 offset1:57
	ds_read2_b32 v[14:15], v49 offset0:82 offset1:90
	ds_read2_b32 v[16:17], v49 offset0:115 offset1:123
	ds_read2_b32 v[18:19], v49 offset0:148 offset1:156
	ds_read2_b32 v[20:21], v49 offset0:181 offset1:189
	ds_read2_b32 v[22:23], v49 offset0:214 offset1:222
	ds_read2_b32 v[24:25], v49 offset0:247 offset1:255
	v_or_b32_e32 v2, s2, v47
	v_lshlrev_b32_e32 v2, 9, v2
	v_lshl_add_u64 v[26:27], v[4:5], 0, v[2:3]
	v_or_b32_e32 v2, s2, v48
	v_lshlrev_b32_e32 v2, 9, v2
	s_waitcnt lgkmcnt(6)
	v_cvt_pk_bf16_f32 v6, v10, v12
	s_waitcnt lgkmcnt(4)
	v_cvt_pk_bf16_f32 v7, v14, v16
	s_waitcnt lgkmcnt(2)
	v_cvt_pk_bf16_f32 v8, v18, v20
	s_waitcnt lgkmcnt(0)
	v_cvt_pk_bf16_f32 v9, v22, v24
	v_lshl_add_u64 v[4:5], v[4:5], 0, v[2:3]
	global_store_dwordx4 v[26:27], v[6:9], off sc1
	s_mov_b64 s[2:3], 0
	s_nop 0
	v_cvt_pk_bf16_f32 v6, v11, v13
	v_cvt_pk_bf16_f32 v7, v15, v17
	v_cvt_pk_bf16_f32 v8, v19, v21
	v_cvt_pk_bf16_f32 v9, v23, v25
	global_store_dwordx4 v[4:5], v[6:9], off sc1
	s_waitcnt lgkmcnt(0)
; #define GAS __attribute__((address_space(1)))
; #define LAS __attribute__((address_space(3)))
; #define LDS_WAIT() asm volatile("s_waitcnt lgkmcnt(0)" ::: "memory")
; __device__ __forceinline__ unsigned pk2(float lo, float hi) { unsigned r; asm("v_cvt_pk_bf16_f32 %0, %1, %2" : "=v"(r) : "v"(lo), "v"(hi)); return r; }
; __device__ __forceinline__ void transpose_item(const float* W, int K, int N, bf16* WT, int drow0, int kb, int n0, LAS float* scr, int lane) {
;     const int k0 = 64 * kb; const int c4 = 4 * (lane & 7); const bool ok = (n0 + c4) < N;
;     f32x4 v[8];
; #pragma unroll
;     for (int i = 0; i < 8; ++i) { const int kk = 8 * i + (lane >> 3); v[i] = ok ? *(const f32x4*)(W + (size_t)(k0 + kk) * N + n0 + c4) : (f32x4){0.f, 0.f, 0.f, 0.f}; }
; #pragma unroll
;     for (int i = 0; i < 8; ++i) { const int kk = 8 * i + (lane >> 3); LAS float* d = scr + kk * 33 + c4; d[0] = v[i][0]; d[1] = v[i][1]; d[2] = v[i][2]; d[3] = v[i][3]; }
;     LDS_WAIT(); asm volatile("" ::: "memory");
;     const int c = lane & 7;
; #pragma unroll
;     for (int j = 0; j < 4; ++j) { const int n = (lane >> 3) + 8 * j; const LAS float* s = scr + (8 * c) * 33 + n;
;         v4u o; o.x = pk2(s[0 * 33], s[1 * 33]); o.y = pk2(s[2 * 33], s[3 * 33]); o.z = pk2(s[4 * 33], s[5 * 33]); o.w = pk2(s[6 * 33], s[7 * 33]);
;         *(GAS v4u*)(WT + (size_t)(drow0 + n) * K + k0 + 8 * c) = o; }
;     LDS_WAIT(); asm volatile("" ::: "memory");
; }
; __device__ __forceinline__ void convert_item(const In& I, unsigned char* ws, int it, LAS float* scr, int lane) {
;     ...
;     if (r < 4 * I_W1) { const int jk = r / I_W1; r -= jk * I_W1; const int kb = r / 8, nb = r % 8;
;         transpose_item(I.nsa_w1 + (size_t)jk * 2048 * 256, 2048, 256, W1t + (size_t)jk * 256 * 2048, 32 * nb, kb, 32 * nb, scr, lane); return; }
.LBB0_174:
	s_andn2_b64 vcc, exec, s[2:3]
	s_cbranch_vccnz .LBB0_176
	s_add_i32 s2, s40, 0x400
	s_lshr_b32 s68, s2, 8
	s_lshl_b64 s[2:3], s[68:69], 21
	v_readlane_b32 s48, v253, 16
	v_readlane_b32 s49, v253, 17
	s_add_u32 s6, s48, s2
	s_addc_u32 s7, s49, s3
	s_lshl_b64 s[2:3], s[68:69], 20
	s_add_u32 s8, s33, s2
	s_addc_u32 s3, s34, s3
	s_and_b32 s2, s42, 0xe0
	s_and_b32 s9, s41, 0x7c0
	s_lshl_b32 s10, s2, 2
	s_add_u32 s6, s6, s10
	v_or_b32_e32 v6, s9, v39
	s_addc_u32 s7, s7, 0
	v_lshlrev_b32_e32 v2, 2, v36
	v_lshl_add_u64 v[4:5], s[6:7], 0, v[2:3]
	v_lshlrev_b32_e32 v2, 10, v6
	v_lshl_add_u64 v[32:33], v[4:5], 0, v[2:3]
	v_add_co_u32_e32 v8, vcc, s74, v32
	global_load_dwordx4 v[4:7], v[32:33], off
	s_nop 0
	v_addc_co_u32_e32 v9, vcc, 0, v33, vcc
	s_movk_i32 s6, 0x4000
	global_load_dwordx4 v[8:11], v[8:9], off
	v_add_co_u32_e32 v12, vcc, s6, v32
	s_movk_i32 s6, 0x6000
	s_nop 0
	v_addc_co_u32_e32 v13, vcc, 0, v33, vcc
	global_load_dwordx4 v[12:15], v[12:13], off
	v_add_co_u32_e32 v16, vcc, s6, v32
	s_mov_b32 s6, 0xa000
	s_nop 0
	v_addc_co_u32_e32 v17, vcc, 0, v33, vcc
	global_load_dwordx4 v[16:19], v[16:17], off
	v_add_co_u32_e32 v20, vcc, s81, v32
	v_add_u32_e32 v2, v44, v45
	s_nop 0
	v_addc_co_u32_e32 v21, vcc, 0, v33, vcc
	global_load_dwordx4 v[20:23], v[20:21], off
	v_add_co_u32_e32 v24, vcc, s6, v32
	s_mov_b32 s6, 0xc000
	s_nop 0
	v_addc_co_u32_e32 v25, vcc, 0, v33, vcc
	global_load_dwordx4 v[24:27], v[24:25], off
	v_add_co_u32_e32 v28, vcc, s6, v32
	s_mov_b32 s6, 0xe000
	s_nop 0
	v_addc_co_u32_e32 v29, vcc, 0, v33, vcc
	global_load_dwordx4 v[28:31], v[28:29], off
	v_add_co_u32_e32 v32, vcc, s6, v32
	s_lshl_b32 s6, s9, 1
	s_nop 0
	v_addc_co_u32_e32 v33, vcc, 0, v33, vcc
	global_load_dwordx4 v[32:35], v[32:33], off
	s_add_u32 s6, s8, s6
	s_addc_u32 s7, s3, 0
	v_readlane_b32 s50, v253, 18
	v_readlane_b32 s51, v253, 19
	v_readlane_b32 s52, v253, 20
	v_readlane_b32 s53, v253, 21
	v_readlane_b32 s54, v253, 22
	v_readlane_b32 s55, v253, 23
	v_readlane_b32 s56, v253, 24
	v_readlane_b32 s57, v253, 25
	v_readlane_b32 s58, v253, 26
	v_readlane_b32 s59, v253, 27
	v_readlane_b32 s60, v253, 28
	v_readlane_b32 s61, v253, 29
	v_readlane_b32 s62, v253, 30
	v_readlane_b32 s63, v253, 31
	s_waitcnt vmcnt(0)
	ds_write2_b32 v2, v4, v5 offset1:1
	ds_write2_b32 v2, v6, v7 offset0:2 offset1:3
	v_add_u32_e32 v4, 0x420, v2
	ds_write2_b32 v4, v8, v9 offset1:1
	v_add_u32_e32 v4, 0x428, v2
	ds_write2_b32 v4, v10, v11 offset1:1
	v_add_u32_e32 v4, 0x840, v2
	ds_write2_b32 v4, v12, v13 offset1:1
	v_add_u32_e32 v4, 0x848, v2
	ds_write2_b32 v4, v14, v15 offset1:1
	v_add_u32_e32 v4, 0xc60, v2
	ds_write2_b32 v4, v16, v17 offset1:1
	v_add_u32_e32 v4, 0xc68, v2
	ds_write2_b32 v4, v18, v19 offset1:1
	v_add_u32_e32 v4, 0x1080, v2
	ds_write2_b32 v4, v20, v21 offset1:1
	v_add_u32_e32 v4, 0x1088, v2
	ds_write2_b32 v4, v22, v23 offset1:1
	v_add_u32_e32 v4, 0x14a0, v2
	ds_write2_b32 v4, v24, v25 offset1:1
	v_add_u32_e32 v4, 0x14a8, v2
	ds_write2_b32 v4, v26, v27 offset1:1
	v_add_u32_e32 v4, 0x18c0, v2
	ds_write2_b32 v4, v28, v29 offset1:1
	v_add_u32_e32 v4, 0x18c8, v2
	ds_write2_b32 v4, v30, v31 offset1:1
	v_add_u32_e32 v4, 0x1ce0, v2
	v_add_u32_e32 v2, 0x1ce8, v2
	ds_write2_b32 v4, v32, v33 offset1:1
	ds_write2_b32 v2, v34, v35 offset1:1
	s_waitcnt lgkmcnt(0)
	ds_read2_b32 v[10:11], v49 offset0:33 offset1:41
	ds_read2_b32 v[12:13], v49 offset1:8
	v_lshlrev_b32_e32 v2, 1, v38
	ds_read2_b32 v[14:15], v49 offset0:66 offset1:74
	ds_read2_b32 v[16:17], v49 offset0:99 offset1:107
	ds_read2_b32 v[18:19], v49 offset0:132 offset1:140
	ds_read2_b32 v[20:21], v49 offset0:165 offset1:173
	ds_read2_b32 v[22:23], v49 offset0:198 offset1:206
	ds_read2_b32 v[24:25], v49 offset0:231 offset1:239
	v_lshl_add_u64 v[8:9], s[6:7], 0, v[2:3]
	v_or_b32_e32 v2, s2, v39
	v_lshlrev_b32_e32 v2, 12, v2
	v_lshl_add_u64 v[26:27], v[8:9], 0, v[2:3]
	v_or_b32_e32 v2, s2, v46
	s_waitcnt lgkmcnt(0)
	v_cvt_pk_bf16_f32 v4, v12, v10
	v_lshlrev_b32_e32 v2, 12, v2
	v_cvt_pk_bf16_f32 v5, v14, v16
	v_cvt_pk_bf16_f32 v6, v18, v20
	v_cvt_pk_bf16_f32 v7, v22, v24
	global_store_dwordx4 v[26:27], v[4:7], off sc1
	s_nop 1
	v_cvt_pk_bf16_f32 v4, v13, v11
	v_lshl_add_u64 v[10:11], v[8:9], 0, v[2:3]
	v_cvt_pk_bf16_f32 v5, v15, v17
	v_cvt_pk_bf16_f32 v6, v19, v21
	v_cvt_pk_bf16_f32 v7, v23, v25
	global_store_dwordx4 v[10:11], v[4:7], off sc1
	ds_read2_b32 v[10:11], v49 offset0:16 offset1:24
	ds_read2_b32 v[12:13], v49 offset0:49 offset1:57
	ds_read2_b32 v[14:15], v49 offset0:82 offset1:90
	ds_read2_b32 v[16:17], v49 offset0:115 offset1:123
	ds_read2_b32 v[18:19], v49 offset0:148 offset1:156
	ds_read2_b32 v[20:21], v49 offset0:181 offset1:189
	ds_read2_b32 v[22:23], v49 offset0:214 offset1:222
	ds_read2_b32 v[24:25], v49 offset0:247 offset1:255
	v_or_b32_e32 v2, s2, v47
	v_lshlrev_b32_e32 v2, 12, v2
	v_lshl_add_u64 v[26:27], v[8:9], 0, v[2:3]
	v_or_b32_e32 v2, s2, v48
	v_lshlrev_b32_e32 v2, 12, v2
	s_waitcnt lgkmcnt(6)
	v_cvt_pk_bf16_f32 v4, v10, v12
	s_waitcnt lgkmcnt(4)
	v_cvt_pk_bf16_f32 v5, v14, v16
	s_waitcnt lgkmcnt(2)
	v_cvt_pk_bf16_f32 v6, v18, v20
	s_waitcnt lgkmcnt(0)
	v_cvt_pk_bf16_f32 v7, v22, v24
	v_lshl_add_u64 v[8:9], v[8:9], 0, v[2:3]
	global_store_dwordx4 v[26:27], v[4:7], off
	s_nop 1
	v_cvt_pk_bf16_f32 v4, v11, v13
	v_cvt_pk_bf16_f32 v5, v15, v17
	v_cvt_pk_bf16_f32 v6, v19, v21
	v_cvt_pk_bf16_f32 v7, v23, v25
	global_store_dwordx4 v[8:9], v[4:7], off
	s_waitcnt lgkmcnt(0)

; __device__ __forceinline__ u32x4 pack8(const f32x4 a, const f32x4 b) { u32x4 w; w.x = cvt_pk_bf16(a[0], a[1]); w.y = cvt_pk_bf16(a[2], a[3]); w.z = cvt_pk_bf16(b[0], b[1]); w.w = cvt_pk_bf16(b[2], b[3]); return w; }
;     __device__ __forceinline__ void operator()(const f32x4 (&acc)[2][2][4][2], const Unit& u, int wr, int wc, int fr, int fq) const {
;         const int row0 = u.pm * BM + wr * 64 + fr, col0 = u.pn * BM + wc * 32 + 8 * fq;
; #pragma unroll
;         for (int ai = 0; ai < 2; ++ai)
; #pragma unroll
;             for (int m = 0; m < 4; ++m) {
;                 bf16_t* rowp = O + (size_t)(row0 + ai * HALF + m * 16) * ldc + col0;
; #pragma unroll
;                 for (int bj = 0; bj < 2; ++bj) *(u32x4*)(rowp + bj * HALF) = pack8(acc[ai][bj][m][0], acc[ai][bj][m][1]);
;             }
.LBB0_672:
	v_lshl_add_u32 v150, s42, 8, v2
	v_lshl_or_b32 v144, s43, 8, v147
	v_ashrrev_i32_e32 v151, 31, v150
	v_ashrrev_i32_e32 v145, 31, v144
	v_lshlrev_b64 v[152:153], 11, v[150:151]
	v_lshl_add_u64 v[152:153], s[8:9], 0, v[152:153]
	v_lshlrev_b64 v[154:155], 1, v[144:145]
	v_lshl_add_u64 v[144:145], v[152:153], 0, v[154:155]
	v_cvt_pk_bf16_f32 v128, v128, v129
	v_cvt_pk_bf16_f32 v129, v130, v131
	v_cvt_pk_bf16_f32 v130, v124, v125
	v_cvt_pk_bf16_f32 v131, v126, v127
	flat_store_dwordx4 v[144:145], v[128:131] sc1
	v_cvt_pk_bf16_f32 v116, v116, v117
	v_cvt_pk_bf16_f32 v117, v118, v119
	v_cvt_pk_bf16_f32 v118, v108, v109
	v_or_b32_e32 v108, 16, v150
	v_ashrrev_i32_e32 v109, 31, v108
	v_lshlrev_b64 v[108:109], 11, v[108:109]
	v_lshl_add_u64 v[108:109], s[8:9], 0, v[108:109]
	v_cvt_pk_bf16_f32 v119, v110, v111
	flat_store_dwordx4 v[144:145], v[116:119] offset:256 sc1
	s_mov_b64 s[14:15], 0x40000
	s_nop 0
	v_lshl_add_u64 v[116:117], v[108:109], 0, v[154:155]
	v_cvt_pk_bf16_f32 v108, v120, v121
	v_cvt_pk_bf16_f32 v109, v122, v123
	v_cvt_pk_bf16_f32 v110, v112, v113
	v_cvt_pk_bf16_f32 v111, v114, v115
	flat_store_dwordx4 v[116:117], v[108:111] sc1
	v_cvt_pk_bf16_f32 v100, v100, v101
	v_cvt_pk_bf16_f32 v101, v102, v103
	v_cvt_pk_bf16_f32 v102, v92, v93
	v_or_b32_e32 v92, 32, v150
	v_ashrrev_i32_e32 v93, 31, v92
	v_lshlrev_b64 v[92:93], 11, v[92:93]
	v_lshl_add_u64 v[92:93], s[8:9], 0, v[92:93]
	v_cvt_pk_bf16_f32 v103, v94, v95
	flat_store_dwordx4 v[116:117], v[100:103] offset:256 sc1
	s_nop 1
	v_lshl_add_u64 v[100:101], v[92:93], 0, v[154:155]
	v_cvt_pk_bf16_f32 v92, v104, v105
	v_cvt_pk_bf16_f32 v93, v106, v107
	v_cvt_pk_bf16_f32 v94, v96, v97
	v_cvt_pk_bf16_f32 v95, v98, v99
	flat_store_dwordx4 v[100:101], v[92:95] sc1
	v_cvt_pk_bf16_f32 v84, v84, v85
	v_cvt_pk_bf16_f32 v85, v86, v87
	v_cvt_pk_bf16_f32 v86, v76, v77
	v_or_b32_e32 v76, 48, v150
	v_ashrrev_i32_e32 v77, 31, v76
	v_lshlrev_b64 v[76:77], 11, v[76:77]
	v_lshl_add_u64 v[76:77], s[8:9], 0, v[76:77]
	v_cvt_pk_bf16_f32 v87, v78, v79
	flat_store_dwordx4 v[100:101], v[84:87] offset:256 sc1
	s_nop 1
	v_lshl_add_u64 v[84:85], v[76:77], 0, v[154:155]
	v_cvt_pk_bf16_f32 v76, v88, v89
	v_cvt_pk_bf16_f32 v77, v90, v91
	v_cvt_pk_bf16_f32 v78, v80, v81
	v_cvt_pk_bf16_f32 v79, v82, v83
	flat_store_dwordx4 v[84:85], v[76:79] sc1
	v_cvt_pk_bf16_f32 v72, v72, v73
	v_cvt_pk_bf16_f32 v73, v74, v75
	v_cvt_pk_bf16_f32 v74, v68, v69
	v_lshl_add_u64 v[68:69], v[144:145], 0, s[14:15]
	s_mov_b32 s14, 0x40000
	v_cvt_pk_bf16_f32 v75, v70, v71
	flat_store_dwordx4 v[84:85], v[72:75] offset:256 sc1
	v_cvt_pk_bf16_f32 v64, v64, v65
	v_cvt_pk_bf16_f32 v65, v66, v67
	v_cvt_pk_bf16_f32 v66, v60, v61
	v_add_co_u32_e32 v60, vcc, s14, v144
	v_cvt_pk_bf16_f32 v67, v62, v63
	s_mov_b64 s[14:15], 0x48000
	s_nop 0
	v_addc_co_u32_e32 v61, vcc, 0, v145, vcc
	flat_store_dwordx4 v[60:61], v[64:67] sc1
	v_cvt_pk_bf16_f32 v52, v52, v53
	v_cvt_pk_bf16_f32 v53, v54, v55
	v_cvt_pk_bf16_f32 v54, v44, v45
	v_cvt_pk_bf16_f32 v55, v46, v47
	flat_store_dwordx4 v[68:69], v[52:55] offset:256 sc1
	v_cvt_pk_bf16_f32 v44, v56, v57
	v_cvt_pk_bf16_f32 v45, v58, v59
	v_cvt_pk_bf16_f32 v46, v48, v49
	v_cvt_pk_bf16_f32 v47, v50, v51
	s_nop 1
	v_lshl_add_u64 v[52:53], v[144:145], 0, s[14:15]
	s_mov_b32 s14, 0x48000
	v_add_co_u32_e32 v48, vcc, s14, v144
	s_mov_b64 s[14:15], 0x50000
	s_nop 0
	v_addc_co_u32_e32 v49, vcc, 0, v145, vcc
	flat_store_dwordx4 v[48:49], v[44:47] sc1
	v_cvt_pk_bf16_f32 v36, v36, v37
	v_cvt_pk_bf16_f32 v37, v38, v39
	v_cvt_pk_bf16_f32 v38, v28, v29
	v_cvt_pk_bf16_f32 v39, v30, v31
	flat_store_dwordx4 v[52:53], v[36:39] offset:256 sc1
	v_cvt_pk_bf16_f32 v28, v40, v41
	v_cvt_pk_bf16_f32 v29, v42, v43
	v_cvt_pk_bf16_f32 v30, v32, v33
	v_cvt_pk_bf16_f32 v31, v34, v35
	s_nop 1
	v_lshl_add_u64 v[36:37], v[144:145], 0, s[14:15]
	s_mov_b32 s14, 0x50000
	v_add_co_u32_e32 v32, vcc, s14, v144
	s_mov_b64 s[14:15], 0x58000
	s_nop 0
	v_addc_co_u32_e32 v33, vcc, 0, v145, vcc
	flat_store_dwordx4 v[32:33], v[28:31] sc1
	v_cvt_pk_bf16_f32 v20, v20, v21
	v_cvt_pk_bf16_f32 v21, v22, v23
	v_cvt_pk_bf16_f32 v22, v12, v13
	v_cvt_pk_bf16_f32 v23, v14, v15
	flat_store_dwordx4 v[36:37], v[20:23] offset:256 sc1
	v_cvt_pk_bf16_f32 v12, v24, v25
	v_cvt_pk_bf16_f32 v13, v26, v27
	v_cvt_pk_bf16_f32 v14, v16, v17
	v_cvt_pk_bf16_f32 v15, v18, v19
	s_nop 1
	v_lshl_add_u64 v[20:21], v[144:145], 0, s[14:15]
	s_mov_b32 s14, 0x58000
	v_add_co_u32_e32 v16, vcc, s14, v144
	s_nop 1
	v_addc_co_u32_e32 v17, vcc, 0, v145, vcc
	s_and_b64 vcc, exec, s[2:3]
	s_mov_b64 s[2:3], -1
	flat_store_dwordx4 v[16:17], v[12:15] sc1
	v_cvt_pk_bf16_f32 v8, v8, v9
	v_cvt_pk_bf16_f32 v9, v10, v11
	v_cvt_pk_bf16_f32 v10, v4, v5
	v_cvt_pk_bf16_f32 v11, v6, v7
	flat_store_dwordx4 v[20:21], v[8:11] offset:256 sc1
	s_cbranch_vccnz .LBB0_657
	s_andn2_b64 vcc, exec, s[6:7]
	s_cbranch_vccnz .LBB0_656
	s_barrier
	s_branch .LBB0_656

;     __device__ __forceinline__ void operator()(const f32x4 (&acc)[2][2][4][2], const Unit& u, int wr, int wc, int fr, int fq) const {
;     ...
;         } else {
;             if (ct0 < 16) {
; #pragma unroll
;                 for (int ai = 0; ai < 2; ++ai)
; #pragma unroll
;                     for (int m = 0; m < 4; ++m) { float* fp = flog + (size_t)(row0 + ai * HALF + m * 16) * 16 + ct0;
; #pragma unroll
;                         for (int n = 0; n < 2; ++n) *(f32x4*)(fp + 4 * n) = acc[ai][0][m][n]; }
;             }
.LBB0_822:
	s_and_saveexec_b64 s[24:25], s[4:5]
	s_cbranch_execz .LBB0_824
	v_or_b32_e32 v156, 16, v150
	v_ashrrev_i32_e32 v151, 31, v150
	v_ashrrev_i32_e32 v157, 31, v156
	v_lshlrev_b64 v[148:149], 6, v[150:151]
	v_lshlrev_b64 v[156:157], 6, v[156:157]
	v_lshl_add_u64 v[148:149], v[140:141], 0, v[148:149]
	v_lshl_add_u64 v[156:157], v[140:141], 0, v[156:157]
	flat_store_dwordx4 v[148:149], v[128:131] sc1
	flat_store_dwordx4 v[148:149], v[124:127] offset:16 sc1
	flat_store_dwordx4 v[156:157], v[116:119] sc1
	flat_store_dwordx4 v[156:157], v[108:111] offset:16 sc1
	v_or_b32_e32 v156, 32, v150
	v_ashrrev_i32_e32 v157, 31, v156
	v_lshlrev_b64 v[156:157], 6, v[156:157]
	v_lshl_add_u64 v[156:157], v[140:141], 0, v[156:157]
	flat_store_dwordx4 v[156:157], v[100:103] sc1
	flat_store_dwordx4 v[156:157], v[92:95] offset:16 sc1
	v_or_b32_e32 v156, 48, v150
	v_ashrrev_i32_e32 v157, 31, v156
	v_lshlrev_b64 v[156:157], 6, v[156:157]
	v_lshl_add_u64 v[156:157], v[140:141], 0, v[156:157]
	s_mov_b64 s[26:27], 0x2000
	v_add_co_u32_e32 v158, vcc, 0x2000, v148
	flat_store_dwordx4 v[156:157], v[84:87] sc1
	flat_store_dwordx4 v[156:157], v[76:79] offset:16 sc1
	v_lshl_add_u64 v[156:157], v[148:149], 0, s[26:27]
	v_addc_co_u32_e32 v159, vcc, 0, v149, vcc
	s_mov_b64 s[26:27], 0x2400
	flat_store_dwordx4 v[158:159], v[64:67] sc1
	flat_store_dwordx4 v[156:157], v[60:63] offset:16 sc1
	v_lshl_add_u64 v[156:157], v[148:149], 0, s[26:27]
	s_mov_b64 s[26:27], 0x2800
	flat_store_dwordx4 v[158:159], v[52:55] offset:1024 sc1
	flat_store_dwordx4 v[156:157], v[44:47] offset:16 sc1
	v_lshl_add_u64 v[156:157], v[148:149], 0, s[26:27]
	s_mov_b64 s[26:27], 0x2c00
	flat_store_dwordx4 v[158:159], v[36:39] offset:2048 sc1
	flat_store_dwordx4 v[156:157], v[28:31] offset:16 sc1
	v_lshl_add_u64 v[148:149], v[148:149], 0, s[26:27]
	flat_store_dwordx4 v[158:159], v[20:23] offset:3072 sc1
	flat_store_dwordx4 v[148:149], v[12:15] offset:16 sc1

; __device__ __forceinline__ u32x4 pack8(const f32x4 a, const f32x4 b) { u32x4 w; w.x = cvt_pk_bf16(a[0], a[1]); w.y = cvt_pk_bf16(a[2], a[3]); w.z = cvt_pk_bf16(b[0], b[1]); w.w = cvt_pk_bf16(b[2], b[3]); return w; }
;     __device__ __forceinline__ void operator()(const f32x4 (&acc)[2][2][4][2], const Unit& u, int wr, int wc, int fr, int fq) const {
;         const int row0 = u.pm * BM + wr * 64 + fr, ct0 = wc * 32 + 8 * fq;
;         if (u.pn < 12) {
;             const int t = u.pn >> 2; const float sc = (t == 0) ? qscale : 1.0f;
;             bf16_t* base = QKV + (size_t)t * tstride + (u.pn & 3) * BM + ct0;
; #pragma unroll
;             for (int ai = 0; ai < 2; ++ai)
; #pragma unroll
;                 for (int m = 0; m < 4; ++m) { bf16_t* rowp = base + (size_t)(row0 + ai * HALF + m * 16) * 1024;
; #pragma unroll
;                     for (int bj = 0; bj < 2; ++bj) *(u32x4*)(rowp + bj * HALF) = pack8(acc[ai][bj][m][0] * sc, acc[ai][bj][m][1] * sc); }
.LBB0_825:
	s_ashr_i32 s24, s47, 2
	s_cmp_lt_u32 s47, 4
	s_cselect_b64 vcc, -1, 0
	s_ashr_i32 s25, s24, 31
	s_lshl_b64 s[24:25], s[24:25], 25
	s_add_u32 s17, s41, s24
	s_addc_u32 s19, s42, s25
	s_lshl_b32 s24, s47, 9
	s_and_b32 s24, s24, 0x600
	s_add_u32 s24, s17, s24
	s_addc_u32 s25, s19, 0
	v_mov_b32_e32 v147, v3
	v_ashrrev_i32_e32 v151, 31, v150
	v_cndmask_b32_e32 v2, 1.0, v220, vcc
	v_lshl_add_u64 v[156:157], s[24:25], 0, v[146:147]
	v_lshlrev_b64 v[148:149], 11, v[150:151]
	v_lshl_add_u64 v[148:149], v[156:157], 0, v[148:149]
	v_pk_mul_f32 v[130:131], v[2:3], v[130:131] op_sel_hi:[0,1]
	v_pk_mul_f32 v[128:129], v[2:3], v[128:129] op_sel_hi:[0,1]
	v_pk_mul_f32 v[158:159], v[2:3], v[126:127] op_sel_hi:[0,1]
	v_pk_mul_f32 v[126:127], v[2:3], v[124:125] op_sel_hi:[0,1]
	v_cvt_pk_bf16_f32 v124, v128, v129
	v_cvt_pk_bf16_f32 v125, v130, v131
	v_cvt_pk_bf16_f32 v126, v126, v127
	v_cvt_pk_bf16_f32 v127, v158, v159
	flat_store_dwordx4 v[148:149], v[124:127] sc1
	v_pk_mul_f32 v[120:121], v[2:3], v[120:121] op_sel_hi:[0,1]
	v_pk_mul_f32 v[122:123], v[2:3], v[122:123] op_sel_hi:[0,1]
	v_pk_mul_f32 v[124:125], v[2:3], v[114:115] op_sel_hi:[0,1]
	v_pk_mul_f32 v[114:115], v[2:3], v[112:113] op_sel_hi:[0,1]
	v_cvt_pk_bf16_f32 v112, v120, v121
	v_cvt_pk_bf16_f32 v113, v122, v123
	v_cvt_pk_bf16_f32 v114, v114, v115
	v_cvt_pk_bf16_f32 v115, v124, v125
	flat_store_dwordx4 v[148:149], v[112:115] offset:256 sc1
	v_pk_mul_f32 v[116:117], v[2:3], v[116:117] op_sel_hi:[0,1]
	v_pk_mul_f32 v[104:105], v[2:3], v[104:105] op_sel_hi:[0,1]
	v_or_b32_e32 v112, 16, v150
	v_ashrrev_i32_e32 v113, 31, v112
	v_lshlrev_b64 v[112:113], 11, v[112:113]
	v_lshl_add_u64 v[112:113], v[156:157], 0, v[112:113]
	v_pk_mul_f32 v[114:115], v[2:3], v[118:119] op_sel_hi:[0,1]
	v_pk_mul_f32 v[118:119], v[2:3], v[110:111] op_sel_hi:[0,1]
	v_pk_mul_f32 v[110:111], v[2:3], v[108:109] op_sel_hi:[0,1]
	v_cvt_pk_bf16_f32 v108, v116, v117
	v_cvt_pk_bf16_f32 v109, v114, v115
	v_cvt_pk_bf16_f32 v110, v110, v111
	v_cvt_pk_bf16_f32 v111, v118, v119
	flat_store_dwordx4 v[112:113], v[108:111] sc1
	v_pk_mul_f32 v[106:107], v[2:3], v[106:107] op_sel_hi:[0,1]
	v_pk_mul_f32 v[100:101], v[2:3], v[100:101] op_sel_hi:[0,1]
	v_pk_mul_f32 v[108:109], v[2:3], v[98:99] op_sel_hi:[0,1]
	v_pk_mul_f32 v[98:99], v[2:3], v[96:97] op_sel_hi:[0,1]
	v_cvt_pk_bf16_f32 v96, v104, v105
	v_cvt_pk_bf16_f32 v97, v106, v107
	v_cvt_pk_bf16_f32 v98, v98, v99
	v_cvt_pk_bf16_f32 v99, v108, v109
	flat_store_dwordx4 v[112:113], v[96:99] offset:256 sc1
	v_pk_mul_f32 v[88:89], v[2:3], v[88:89] op_sel_hi:[0,1]
	v_pk_mul_f32 v[90:91], v[2:3], v[90:91] op_sel_hi:[0,1]
	v_or_b32_e32 v96, 32, v150
	v_ashrrev_i32_e32 v97, 31, v96
	v_lshlrev_b64 v[96:97], 11, v[96:97]
	v_lshl_add_u64 v[96:97], v[156:157], 0, v[96:97]
	v_pk_mul_f32 v[98:99], v[2:3], v[102:103] op_sel_hi:[0,1]
	v_pk_mul_f32 v[102:103], v[2:3], v[94:95] op_sel_hi:[0,1]
	v_pk_mul_f32 v[94:95], v[2:3], v[92:93] op_sel_hi:[0,1]
	v_cvt_pk_bf16_f32 v92, v100, v101
	v_cvt_pk_bf16_f32 v93, v98, v99
	v_cvt_pk_bf16_f32 v94, v94, v95
	v_cvt_pk_bf16_f32 v95, v102, v103
	flat_store_dwordx4 v[96:97], v[92:95] sc1
	v_pk_mul_f32 v[84:85], v[2:3], v[84:85] op_sel_hi:[0,1]
	v_pk_mul_f32 v[74:75], v[2:3], v[74:75] op_sel_hi:[0,1]
	v_pk_mul_f32 v[92:93], v[2:3], v[82:83] op_sel_hi:[0,1]
	v_pk_mul_f32 v[82:83], v[2:3], v[80:81] op_sel_hi:[0,1]
	v_cvt_pk_bf16_f32 v80, v88, v89
	v_cvt_pk_bf16_f32 v81, v90, v91
	v_cvt_pk_bf16_f32 v82, v82, v83
	v_cvt_pk_bf16_f32 v83, v92, v93
	flat_store_dwordx4 v[96:97], v[80:83] offset:256 sc1
	v_pk_mul_f32 v[72:73], v[2:3], v[72:73] op_sel_hi:[0,1]
	v_pk_mul_f32 v[64:65], v[2:3], v[64:65] op_sel_hi:[0,1]
	v_or_b32_e32 v80, 48, v150
	v_ashrrev_i32_e32 v81, 31, v80
	v_lshlrev_b64 v[80:81], 11, v[80:81]
	v_lshl_add_u64 v[80:81], v[156:157], 0, v[80:81]
	v_pk_mul_f32 v[82:83], v[2:3], v[86:87] op_sel_hi:[0,1]
	v_pk_mul_f32 v[86:87], v[2:3], v[78:79] op_sel_hi:[0,1]
	v_pk_mul_f32 v[78:79], v[2:3], v[76:77] op_sel_hi:[0,1]
	v_cvt_pk_bf16_f32 v76, v84, v85
	v_cvt_pk_bf16_f32 v77, v82, v83
	v_cvt_pk_bf16_f32 v78, v78, v79
	v_cvt_pk_bf16_f32 v79, v86, v87
	flat_store_dwordx4 v[80:81], v[76:79] sc1
	s_mov_b32 s17, 0x40000
	v_pk_mul_f32 v[66:67], v[2:3], v[66:67] op_sel_hi:[0,1]
; __device__ __forceinline__ u32x4 pack8(const f32x4 a, const f32x4 b) { u32x4 w; w.x = cvt_pk_bf16(a[0], a[1]); w.y = cvt_pk_bf16(a[2], a[3]); w.z = cvt_pk_bf16(b[0], b[1]); w.w = cvt_pk_bf16(b[2], b[3]); return w; }
;     __device__ __forceinline__ void operator()(const f32x4 (&acc)[2][2][4][2], const Unit& u, int wr, int wc, int fr, int fq) const {
;     ...
; #pragma unroll
;             for (int ai = 0; ai < 2; ++ai)
; #pragma unroll
;                 for (int m = 0; m < 4; ++m) { bf16_t* rowp = base + (size_t)(row0 + ai * HALF + m * 16) * 1024;
; #pragma unroll
;                     for (int bj = 0; bj < 2; ++bj) *(u32x4*)(rowp + bj * HALF) = pack8(acc[ai][bj][m][0] * sc, acc[ai][bj][m][1] * sc); }
	v_pk_mul_f32 v[76:77], v[2:3], v[70:71] op_sel_hi:[0,1]
	v_pk_mul_f32 v[70:71], v[2:3], v[68:69] op_sel_hi:[0,1]
	v_cvt_pk_bf16_f32 v68, v72, v73
	v_cvt_pk_bf16_f32 v69, v74, v75
	v_cvt_pk_bf16_f32 v70, v70, v71
	v_cvt_pk_bf16_f32 v71, v76, v77
	flat_store_dwordx4 v[80:81], v[68:71] offset:256 sc1
	s_mov_b64 s[24:25], 0x40000
	v_pk_mul_f32 v[58:59], v[2:3], v[58:59] op_sel_hi:[0,1]
	v_pk_mul_f32 v[70:71], v[2:3], v[62:63] op_sel_hi:[0,1]
	v_pk_mul_f32 v[62:63], v[2:3], v[60:61] op_sel_hi:[0,1]
	v_cvt_pk_bf16_f32 v60, v64, v65
	v_add_co_u32_e32 v64, vcc, s17, v148
	v_cvt_pk_bf16_f32 v61, v66, v67
	v_cvt_pk_bf16_f32 v62, v62, v63
	v_cvt_pk_bf16_f32 v63, v70, v71
	v_lshl_add_u64 v[68:69], v[148:149], 0, s[24:25]
	s_nop 0
	v_addc_co_u32_e32 v65, vcc, 0, v149, vcc
	flat_store_dwordx4 v[64:65], v[60:63] sc1
	v_pk_mul_f32 v[56:57], v[2:3], v[56:57] op_sel_hi:[0,1]
	s_mov_b32 s17, 0x48000
	v_pk_mul_f32 v[60:61], v[2:3], v[50:51] op_sel_hi:[0,1]
	v_pk_mul_f32 v[50:51], v[2:3], v[48:49] op_sel_hi:[0,1]
	v_cvt_pk_bf16_f32 v48, v56, v57
	v_cvt_pk_bf16_f32 v49, v58, v59
	v_cvt_pk_bf16_f32 v50, v50, v51
	v_cvt_pk_bf16_f32 v51, v60, v61
	flat_store_dwordx4 v[68:69], v[48:51] offset:256 sc1
	v_pk_mul_f32 v[52:53], v[2:3], v[52:53] op_sel_hi:[0,1]
	s_mov_b64 s[24:25], 0x48000
	v_pk_mul_f32 v[50:51], v[2:3], v[54:55] op_sel_hi:[0,1]
	v_pk_mul_f32 v[54:55], v[2:3], v[46:47] op_sel_hi:[0,1]
	v_pk_mul_f32 v[46:47], v[2:3], v[44:45] op_sel_hi:[0,1]
	v_cvt_pk_bf16_f32 v44, v52, v53
	v_cvt_pk_bf16_f32 v45, v50, v51
	v_add_co_u32_e32 v50, vcc, s17, v148
	v_cvt_pk_bf16_f32 v46, v46, v47
	v_cvt_pk_bf16_f32 v47, v54, v55
	v_lshl_add_u64 v[48:49], v[148:149], 0, s[24:25]
	s_nop 0
	v_addc_co_u32_e32 v51, vcc, 0, v149, vcc
	flat_store_dwordx4 v[50:51], v[44:47] sc1
	v_pk_mul_f32 v[42:43], v[2:3], v[42:43] op_sel_hi:[0,1]
	v_pk_mul_f32 v[40:41], v[2:3], v[40:41] op_sel_hi:[0,1]
	v_pk_mul_f32 v[44:45], v[2:3], v[34:35] op_sel_hi:[0,1]
	v_pk_mul_f32 v[34:35], v[2:3], v[32:33] op_sel_hi:[0,1]
	v_cvt_pk_bf16_f32 v32, v40, v41
	v_cvt_pk_bf16_f32 v33, v42, v43
	v_cvt_pk_bf16_f32 v34, v34, v35
	v_cvt_pk_bf16_f32 v35, v44, v45
	flat_store_dwordx4 v[48:49], v[32:35] offset:256 sc1
	s_mov_b32 s17, 0x50000
	v_pk_mul_f32 v[36:37], v[2:3], v[36:37] op_sel_hi:[0,1]
	v_pk_mul_f32 v[34:35], v[2:3], v[38:39] op_sel_hi:[0,1]
	v_pk_mul_f32 v[38:39], v[2:3], v[30:31] op_sel_hi:[0,1]
	v_pk_mul_f32 v[30:31], v[2:3], v[28:29] op_sel_hi:[0,1]
	v_cvt_pk_bf16_f32 v28, v36, v37
	v_cvt_pk_bf16_f32 v29, v34, v35
	v_add_co_u32_e32 v34, vcc, s17, v148
	s_mov_b64 s[24:25], 0x50000
	s_nop 0
	v_addc_co_u32_e32 v35, vcc, 0, v149, vcc
	v_cvt_pk_bf16_f32 v30, v30, v31
	v_cvt_pk_bf16_f32 v31, v38, v39
	flat_store_dwordx4 v[34:35], v[28:31] sc1
	v_lshl_add_u64 v[32:33], v[148:149], 0, s[24:25]
	v_pk_mul_f32 v[26:27], v[2:3], v[26:27] op_sel_hi:[0,1]
	v_pk_mul_f32 v[28:29], v[2:3], v[18:19] op_sel_hi:[0,1]
	v_pk_mul_f32 v[18:19], v[2:3], v[16:17] op_sel_hi:[0,1]
	v_pk_mul_f32 v[24:25], v[2:3], v[24:25] op_sel_hi:[0,1]
	v_cvt_pk_bf16_f32 v16, v24, v25
	v_cvt_pk_bf16_f32 v17, v26, v27
	v_cvt_pk_bf16_f32 v18, v18, v19
	v_cvt_pk_bf16_f32 v19, v28, v29
	flat_store_dwordx4 v[32:33], v[16:19] offset:256 sc1
	s_mov_b32 s17, 0x58000
	v_pk_mul_f32 v[20:21], v[2:3], v[20:21] op_sel_hi:[0,1]
	v_pk_mul_f32 v[18:19], v[2:3], v[22:23] op_sel_hi:[0,1]
	v_pk_mul_f32 v[22:23], v[2:3], v[14:15] op_sel_hi:[0,1]
	v_pk_mul_f32 v[14:15], v[2:3], v[12:13] op_sel_hi:[0,1]
	v_cvt_pk_bf16_f32 v12, v20, v21
	v_cvt_pk_bf16_f32 v13, v18, v19
	v_add_co_u32_e32 v18, vcc, s17, v148
	s_mov_b64 s[24:25], 0x58000
	s_nop 0
	v_addc_co_u32_e32 v19, vcc, 0, v149, vcc
	v_lshl_add_u64 v[16:17], v[148:149], 0, s[24:25]
	v_cvt_pk_bf16_f32 v14, v14, v15
	v_cvt_pk_bf16_f32 v15, v22, v23
	flat_store_dwordx4 v[18:19], v[12:15] sc1
	v_pk_mul_f32 v[10:11], v[2:3], v[10:11] op_sel_hi:[0,1]
	v_pk_mul_f32 v[8:9], v[2:3], v[8:9] op_sel_hi:[0,1]
	v_pk_mul_f32 v[12:13], v[2:3], v[6:7] op_sel_hi:[0,1]
	v_pk_mul_f32 v[6:7], v[2:3], v[4:5] op_sel_hi:[0,1]
	v_cvt_pk_bf16_f32 v4, v8, v9
	v_cvt_pk_bf16_f32 v5, v10, v11
	v_cvt_pk_bf16_f32 v6, v6, v7
	v_cvt_pk_bf16_f32 v7, v12, v13
	flat_store_dwordx4 v[16:17], v[4:7] offset:256 sc1
	s_andn2_b64 vcc, exec, s[6:7]
	s_mov_b64 s[6:7], -1
	s_cbranch_vccnz .LBB0_812

; __device__ __forceinline__ u32x4 pack8(const f32x4 a, const f32x4 b) { u32x4 w; w.x = cvt_pk_bf16(a[0], a[1]); w.y = cvt_pk_bf16(a[2], a[3]); w.z = cvt_pk_bf16(b[0], b[1]); w.w = cvt_pk_bf16(b[2], b[3]); return w; }
;     __device__ __forceinline__ void operator()(const f32x4 (&acc)[2][2][4][2], const Unit& u, int wr, int wc, int fr, int fq) const {
;         const int row0 = u.pm * BM + wr * 64 + fr, col0 = u.pn * BM + wc * 32 + 8 * fq;
; #pragma unroll
;         for (int ai = 0; ai < 2; ++ai)
; #pragma unroll
;             for (int m = 0; m < 4; ++m) {
;                 bf16_t* rowp = O + (size_t)(row0 + ai * HALF + m * 16) * ldc + col0;
; #pragma unroll
;                 for (int bj = 0; bj < 2; ++bj) *(u32x4*)(rowp + bj * HALF) = pack8(acc[ai][bj][m][0], acc[ai][bj][m][1]);
;             }
.LBB0_1096:
	v_lshl_add_u32 v150, s16, 8, v2
	v_lshl_or_b32 v144, s43, 8, v147
	v_ashrrev_i32_e32 v151, 31, v150
	v_ashrrev_i32_e32 v145, 31, v144
	v_lshlrev_b64 v[152:153], 11, v[150:151]
	v_lshl_add_u64 v[152:153], s[8:9], 0, v[152:153]
	v_lshlrev_b64 v[154:155], 1, v[144:145]
	v_lshl_add_u64 v[144:145], v[152:153], 0, v[154:155]
	v_cvt_pk_bf16_f32 v128, v128, v129
	v_cvt_pk_bf16_f32 v129, v130, v131
	v_cvt_pk_bf16_f32 v130, v124, v125
	v_cvt_pk_bf16_f32 v131, v126, v127
	flat_store_dwordx4 v[144:145], v[128:131] sc1
	v_cvt_pk_bf16_f32 v116, v116, v117
	v_cvt_pk_bf16_f32 v117, v118, v119
	v_cvt_pk_bf16_f32 v118, v108, v109
	v_or_b32_e32 v108, 16, v150
	v_ashrrev_i32_e32 v109, 31, v108
	v_lshlrev_b64 v[108:109], 11, v[108:109]
	v_lshl_add_u64 v[108:109], s[8:9], 0, v[108:109]
	v_cvt_pk_bf16_f32 v119, v110, v111
	flat_store_dwordx4 v[144:145], v[116:119] offset:256 sc1
	s_mov_b32 s13, 0x40000
	s_mov_b64 s[22:23], 0x40000
	v_lshl_add_u64 v[116:117], v[108:109], 0, v[154:155]
	v_cvt_pk_bf16_f32 v108, v120, v121
	v_cvt_pk_bf16_f32 v109, v122, v123
	v_cvt_pk_bf16_f32 v110, v112, v113
	v_cvt_pk_bf16_f32 v111, v114, v115
	flat_store_dwordx4 v[116:117], v[108:111] sc1
	v_cvt_pk_bf16_f32 v100, v100, v101
	v_cvt_pk_bf16_f32 v101, v102, v103
	v_cvt_pk_bf16_f32 v102, v92, v93
	v_or_b32_e32 v92, 32, v150
	v_ashrrev_i32_e32 v93, 31, v92
	v_lshlrev_b64 v[92:93], 11, v[92:93]
	v_lshl_add_u64 v[92:93], s[8:9], 0, v[92:93]
	v_cvt_pk_bf16_f32 v103, v94, v95
	flat_store_dwordx4 v[116:117], v[100:103] offset:256 sc1
	s_nop 1
	v_lshl_add_u64 v[100:101], v[92:93], 0, v[154:155]
	v_cvt_pk_bf16_f32 v92, v104, v105
	v_cvt_pk_bf16_f32 v93, v106, v107
	v_cvt_pk_bf16_f32 v94, v96, v97
	v_cvt_pk_bf16_f32 v95, v98, v99
	flat_store_dwordx4 v[100:101], v[92:95] sc1
	v_cvt_pk_bf16_f32 v84, v84, v85
	v_cvt_pk_bf16_f32 v85, v86, v87
	v_cvt_pk_bf16_f32 v86, v76, v77
	v_or_b32_e32 v76, 48, v150
	v_ashrrev_i32_e32 v77, 31, v76
	v_lshlrev_b64 v[76:77], 11, v[76:77]
	v_lshl_add_u64 v[76:77], s[8:9], 0, v[76:77]
	v_cvt_pk_bf16_f32 v87, v78, v79
	flat_store_dwordx4 v[100:101], v[84:87] offset:256 sc1
	s_nop 1
	v_lshl_add_u64 v[84:85], v[76:77], 0, v[154:155]
	v_cvt_pk_bf16_f32 v76, v88, v89
	v_cvt_pk_bf16_f32 v77, v90, v91
	v_cvt_pk_bf16_f32 v78, v80, v81
	v_cvt_pk_bf16_f32 v79, v82, v83
	flat_store_dwordx4 v[84:85], v[76:79] sc1
	v_cvt_pk_bf16_f32 v72, v72, v73
	v_cvt_pk_bf16_f32 v73, v74, v75
	v_cvt_pk_bf16_f32 v74, v68, v69
	v_cvt_pk_bf16_f32 v75, v70, v71
	flat_store_dwordx4 v[84:85], v[72:75] offset:256 sc1
	v_cvt_pk_bf16_f32 v64, v64, v65
	v_cvt_pk_bf16_f32 v65, v66, v67
	v_cvt_pk_bf16_f32 v66, v60, v61
	v_add_co_u32_e32 v60, vcc, s13, v144
	v_lshl_add_u64 v[68:69], v[144:145], 0, s[22:23]
	s_nop 0
	v_addc_co_u32_e32 v61, vcc, 0, v145, vcc
	s_mov_b32 s13, 0x48000
	v_cvt_pk_bf16_f32 v67, v62, v63
	flat_store_dwordx4 v[60:61], v[64:67] sc1
	v_cvt_pk_bf16_f32 v52, v52, v53
	v_cvt_pk_bf16_f32 v53, v54, v55
	v_cvt_pk_bf16_f32 v54, v44, v45
	v_cvt_pk_bf16_f32 v55, v46, v47
	flat_store_dwordx4 v[68:69], v[52:55] offset:256 sc1
	s_mov_b64 s[22:23], 0x48000
	v_cvt_pk_bf16_f32 v44, v56, v57
	v_cvt_pk_bf16_f32 v45, v58, v59
	v_cvt_pk_bf16_f32 v46, v48, v49
	v_add_co_u32_e32 v48, vcc, s13, v144
	v_lshl_add_u64 v[52:53], v[144:145], 0, s[22:23]
	s_nop 0
	v_addc_co_u32_e32 v49, vcc, 0, v145, vcc
	s_mov_b32 s13, 0x50000
	v_cvt_pk_bf16_f32 v47, v50, v51
	flat_store_dwordx4 v[48:49], v[44:47] sc1
	v_cvt_pk_bf16_f32 v36, v36, v37
	v_cvt_pk_bf16_f32 v37, v38, v39
	v_cvt_pk_bf16_f32 v38, v28, v29
	v_cvt_pk_bf16_f32 v39, v30, v31
	flat_store_dwordx4 v[52:53], v[36:39] offset:256 sc1
	s_mov_b64 s[22:23], 0x50000
	v_cvt_pk_bf16_f32 v28, v40, v41
	v_cvt_pk_bf16_f32 v29, v42, v43
	v_cvt_pk_bf16_f32 v30, v32, v33
	v_add_co_u32_e32 v32, vcc, s13, v144
	v_lshl_add_u64 v[36:37], v[144:145], 0, s[22:23]
	s_nop 0
	v_addc_co_u32_e32 v33, vcc, 0, v145, vcc
	s_mov_b32 s13, 0x58000
	v_cvt_pk_bf16_f32 v31, v34, v35
	flat_store_dwordx4 v[32:33], v[28:31] sc1
	v_cvt_pk_bf16_f32 v20, v20, v21
	v_cvt_pk_bf16_f32 v21, v22, v23
	v_cvt_pk_bf16_f32 v22, v12, v13
	v_cvt_pk_bf16_f32 v23, v14, v15
	flat_store_dwordx4 v[36:37], v[20:23] offset:256 sc1
	v_cvt_pk_bf16_f32 v12, v24, v25
	v_cvt_pk_bf16_f32 v13, v26, v27
	v_cvt_pk_bf16_f32 v14, v16, v17
	v_add_co_u32_e32 v16, vcc, s13, v144
	s_mov_b64 s[22:23], 0x58000
	s_nop 0
	v_addc_co_u32_e32 v17, vcc, 0, v145, vcc
	v_lshl_add_u64 v[20:21], v[144:145], 0, s[22:23]
	s_andn2_b64 vcc, exec, s[4:5]
	s_mov_b64 s[4:5], -1
	v_cvt_pk_bf16_f32 v15, v18, v19
	flat_store_dwordx4 v[16:17], v[12:15] sc1
	v_cvt_pk_bf16_f32 v8, v8, v9
	v_cvt_pk_bf16_f32 v9, v10, v11
	v_cvt_pk_bf16_f32 v10, v4, v5
	v_cvt_pk_bf16_f32 v11, v6, v7
	flat_store_dwordx4 v[20:21], v[8:11] offset:256 sc1
	s_cbranch_vccnz .LBB0_1085
	s_andn2_b64 vcc, exec, s[6:7]
	s_cbranch_vccnz .LBB0_1084
	s_barrier
	s_branch .LBB0_1084

; __device__ __forceinline__ float sigm(float x) { return __builtin_amdgcn_rcpf(1.0f + __builtin_amdgcn_exp2f(-1.4426950408889634f * x)); }
;     __device__ __forceinline__ void operator()(const f32x4 (&acc)[2][2][4][2], const Unit& u, int wr, int wc, int fr, int fq) const {
;     ...
;         } else {
;             if (ct0 < 48) {
; #pragma unroll
;                 for (int ai = 0; ai < 2; ++ai)
; #pragma unroll
;                     for (int m = 0; m < 4; ++m) { float* gp = gates + (size_t)(row0 + ai * HALF + m * 16) * 48 + ct0;
; #pragma unroll
;                         for (int n = 0; n < 2; ++n) { const f32x4 v = acc[ai][0][m][n]; *(f32x4*)(gp + 4 * n) = (f32x4){sigm(v[0]), sigm(v[1]), sigm(v[2]), sigm(v[3])}; } }
;             }
.LBB0_1167:
	s_cmp_gt_u32 s18, 9
	s_cbranch_scc0 .LBB0_1171
	s_and_saveexec_b64 s[20:21], s[2:3]
	s_cbranch_execz .LBB0_1170
	v_mul_f32_e32 v149, 0xbfb8aa3b, v128
	v_exp_f32_e32 v149, v149
	s_movk_i32 s24, 0xc0
	v_mad_i64_i32 v[152:153], s[22:23], v150, s24, v[140:141]
	v_add_f32_e32 v149, 1.0, v149
	v_rcp_f32_e32 v156, v149
	v_mul_f32_e32 v149, 0xbfb8aa3b, v129
	v_exp_f32_e32 v149, v149
	s_nop 0
	v_add_f32_e32 v149, 1.0, v149
	v_rcp_f32_e32 v157, v149
	v_mul_f32_e32 v149, 0xbfb8aa3b, v130
	v_exp_f32_e32 v149, v149
	s_nop 0
	v_add_f32_e32 v149, 1.0, v149
	v_rcp_f32_e32 v158, v149
	v_mul_f32_e32 v149, 0xbfb8aa3b, v131
	v_exp_f32_e32 v149, v149
	s_nop 0
	v_add_f32_e32 v149, 1.0, v149
	v_rcp_f32_e32 v159, v149
	v_mul_f32_e32 v149, 0xbfb8aa3b, v124
	v_exp_f32_e32 v149, v149
	flat_store_dwordx4 v[152:153], v[156:159] sc1
	v_add_f32_e32 v149, 1.0, v149
	s_nop 0
	v_rcp_f32_e32 v156, v149
	v_mul_f32_e32 v149, 0xbfb8aa3b, v125
	v_exp_f32_e32 v149, v149
	s_nop 0
	v_add_f32_e32 v149, 1.0, v149
	v_rcp_f32_e32 v157, v149
	v_mul_f32_e32 v149, 0xbfb8aa3b, v126
	v_exp_f32_e32 v149, v149
	s_nop 0
	v_add_f32_e32 v149, 1.0, v149
	v_rcp_f32_e32 v158, v149
	v_mul_f32_e32 v149, 0xbfb8aa3b, v127
	v_exp_f32_e32 v149, v149
	s_nop 0
	v_add_f32_e32 v149, 1.0, v149
	v_rcp_f32_e32 v159, v149
	v_or_b32_e32 v149, 16, v150
	flat_store_dwordx4 v[152:153], v[156:159] offset:16 sc1
	v_mad_i64_i32 v[152:153], s[22:23], v149, s24, v[140:141]
	v_mul_f32_e32 v149, 0xbfb8aa3b, v112
	v_exp_f32_e32 v149, v149
	s_nop 0
	v_add_f32_e32 v149, 1.0, v149
	v_rcp_f32_e32 v156, v149
	v_mul_f32_e32 v149, 0xbfb8aa3b, v113
	v_exp_f32_e32 v149, v149
	s_nop 0
	v_add_f32_e32 v149, 1.0, v149
	v_rcp_f32_e32 v157, v149
	v_mul_f32_e32 v149, 0xbfb8aa3b, v114
	v_exp_f32_e32 v149, v149
	s_nop 0
	v_add_f32_e32 v149, 1.0, v149
	v_rcp_f32_e32 v158, v149
	v_mul_f32_e32 v149, 0xbfb8aa3b, v115
	v_exp_f32_e32 v149, v149
	s_nop 0
	v_add_f32_e32 v149, 1.0, v149
	v_rcp_f32_e32 v159, v149
	v_mul_f32_e32 v149, 0xbfb8aa3b, v108
	v_exp_f32_e32 v149, v149
	flat_store_dwordx4 v[152:153], v[156:159] sc1
	v_add_f32_e32 v149, 1.0, v149
	s_nop 0
	v_rcp_f32_e32 v156, v149
	v_mul_f32_e32 v149, 0xbfb8aa3b, v109
	v_exp_f32_e32 v149, v149
	s_nop 0
	v_add_f32_e32 v149, 1.0, v149
	v_rcp_f32_e32 v157, v149
	v_mul_f32_e32 v149, 0xbfb8aa3b, v110
	v_exp_f32_e32 v149, v149
	s_nop 0
	v_add_f32_e32 v149, 1.0, v149
	v_rcp_f32_e32 v158, v149
	v_mul_f32_e32 v149, 0xbfb8aa3b, v111
	v_exp_f32_e32 v149, v149
	s_nop 0
	v_add_f32_e32 v149, 1.0, v149
	v_rcp_f32_e32 v159, v149
	v_or_b32_e32 v149, 32, v150
	flat_store_dwordx4 v[152:153], v[156:159] offset:16 sc1
	v_mad_i64_i32 v[152:153], s[22:23], v149, s24, v[140:141]
	v_mul_f32_e32 v149, 0xbfb8aa3b, v96
	v_exp_f32_e32 v149, v149
	s_nop 0
	v_add_f32_e32 v149, 1.0, v149
	v_rcp_f32_e32 v156, v149
	v_mul_f32_e32 v149, 0xbfb8aa3b, v97
	v_exp_f32_e32 v149, v149
	s_nop 0
	v_add_f32_e32 v149, 1.0, v149
	v_rcp_f32_e32 v157, v149
	v_mul_f32_e32 v149, 0xbfb8aa3b, v98
	v_exp_f32_e32 v149, v149
	s_nop 0
	v_add_f32_e32 v149, 1.0, v149
	v_rcp_f32_e32 v158, v149
	v_mul_f32_e32 v149, 0xbfb8aa3b, v99
	v_exp_f32_e32 v149, v149
	s_nop 0
	v_add_f32_e32 v149, 1.0, v149
	v_rcp_f32_e32 v159, v149
	v_mul_f32_e32 v149, 0xbfb8aa3b, v92
	v_exp_f32_e32 v149, v149
	flat_store_dwordx4 v[152:153], v[156:159] sc1
	v_add_f32_e32 v149, 1.0, v149
	s_nop 0
	v_rcp_f32_e32 v156, v149
	v_mul_f32_e32 v149, 0xbfb8aa3b, v93
	v_exp_f32_e32 v149, v149
	s_nop 0
	v_add_f32_e32 v149, 1.0, v149
	v_rcp_f32_e32 v157, v149
	v_mul_f32_e32 v149, 0xbfb8aa3b, v94
	v_exp_f32_e32 v149, v149
	s_nop 0
	v_add_f32_e32 v149, 1.0, v149
	v_rcp_f32_e32 v158, v149
	v_mul_f32_e32 v149, 0xbfb8aa3b, v95
	v_exp_f32_e32 v149, v149
	s_nop 0
	v_add_f32_e32 v149, 1.0, v149
	v_rcp_f32_e32 v159, v149
	v_or_b32_e32 v149, 48, v150
	flat_store_dwordx4 v[152:153], v[156:159] offset:16 sc1
	v_mad_i64_i32 v[152:153], s[22:23], v149, s24, v[140:141]
	v_mul_f32_e32 v149, 0xbfb8aa3b, v80
	v_exp_f32_e32 v149, v149
	s_nop 0
	v_add_f32_e32 v149, 1.0, v149
	v_rcp_f32_e32 v156, v149
	v_mul_f32_e32 v149, 0xbfb8aa3b, v81
	v_exp_f32_e32 v149, v149
	s_nop 0
	v_add_f32_e32 v149, 1.0, v149
	v_rcp_f32_e32 v157, v149
	v_mul_f32_e32 v149, 0xbfb8aa3b, v82
	v_exp_f32_e32 v149, v149
	s_nop 0
	v_add_f32_e32 v149, 1.0, v149
	v_rcp_f32_e32 v158, v149
	v_mul_f32_e32 v149, 0xbfb8aa3b, v83
	v_exp_f32_e32 v149, v149
	s_nop 0
	v_add_f32_e32 v149, 1.0, v149
	v_rcp_f32_e32 v159, v149
	v_mul_f32_e32 v149, 0xbfb8aa3b, v76
	v_exp_f32_e32 v149, v149
	flat_store_dwordx4 v[152:153], v[156:159] sc1
	v_add_f32_e32 v149, 1.0, v149
	s_nop 0
	v_rcp_f32_e32 v156, v149
	v_mul_f32_e32 v149, 0xbfb8aa3b, v77
	v_exp_f32_e32 v149, v149
	s_nop 0
	v_add_f32_e32 v149, 1.0, v149
	v_rcp_f32_e32 v157, v149
	v_mul_f32_e32 v149, 0xbfb8aa3b, v78
	v_exp_f32_e32 v149, v149
	s_nop 0
	v_add_f32_e32 v149, 1.0, v149
	v_rcp_f32_e32 v158, v149
	v_mul_f32_e32 v149, 0xbfb8aa3b, v79
	v_exp_f32_e32 v149, v149
	s_nop 0
	v_add_f32_e32 v149, 1.0, v149
	v_rcp_f32_e32 v159, v149
; __device__ __forceinline__ float sigm(float x) { return __builtin_amdgcn_rcpf(1.0f + __builtin_amdgcn_exp2f(-1.4426950408889634f * x)); }
;     __device__ __forceinline__ void operator()(const f32x4 (&acc)[2][2][4][2], const Unit& u, int wr, int wc, int fr, int fq) const {
;     ...
;         } else {
;             if (ct0 < 48) {
; #pragma unroll
;                 for (int ai = 0; ai < 2; ++ai)
; #pragma unroll
;                     for (int m = 0; m < 4; ++m) { float* gp = gates + (size_t)(row0 + ai * HALF + m * 16) * 48 + ct0;
; #pragma unroll
;                         for (int n = 0; n < 2; ++n) { const f32x4 v = acc[ai][0][m][n]; *(f32x4*)(gp + 4 * n) = (f32x4){sigm(v[0]), sigm(v[1]), sigm(v[2]), sigm(v[3])}; } }
;             }
	v_add_u32_e32 v149, 0x80, v150
	flat_store_dwordx4 v[152:153], v[156:159] offset:16 sc1
	v_mad_i64_i32 v[152:153], s[22:23], v149, s24, v[140:141]
	v_mul_f32_e32 v149, 0xbfb8aa3b, v64
	v_exp_f32_e32 v149, v149
	s_nop 0
	v_add_f32_e32 v149, 1.0, v149
	v_rcp_f32_e32 v156, v149
	v_mul_f32_e32 v149, 0xbfb8aa3b, v65
	v_exp_f32_e32 v149, v149
	s_nop 0
	v_add_f32_e32 v149, 1.0, v149
	v_rcp_f32_e32 v157, v149
	v_mul_f32_e32 v149, 0xbfb8aa3b, v66
	v_exp_f32_e32 v149, v149
	s_nop 0
	v_add_f32_e32 v149, 1.0, v149
	v_rcp_f32_e32 v158, v149
	v_mul_f32_e32 v149, 0xbfb8aa3b, v67
	v_exp_f32_e32 v149, v149
	s_nop 0
	v_add_f32_e32 v149, 1.0, v149
	v_rcp_f32_e32 v159, v149
	v_mul_f32_e32 v149, 0xbfb8aa3b, v60
	v_exp_f32_e32 v149, v149
	flat_store_dwordx4 v[152:153], v[156:159] sc1
	v_add_f32_e32 v149, 1.0, v149
	s_nop 0
	v_rcp_f32_e32 v156, v149
	v_mul_f32_e32 v149, 0xbfb8aa3b, v61
	v_exp_f32_e32 v149, v149
	s_nop 0
	v_add_f32_e32 v149, 1.0, v149
	v_rcp_f32_e32 v157, v149
	v_mul_f32_e32 v149, 0xbfb8aa3b, v62
	v_exp_f32_e32 v149, v149
	s_nop 0
	v_add_f32_e32 v149, 1.0, v149
	v_rcp_f32_e32 v158, v149
	v_mul_f32_e32 v149, 0xbfb8aa3b, v63
	v_exp_f32_e32 v149, v149
	s_nop 0
	v_add_f32_e32 v149, 1.0, v149
	v_rcp_f32_e32 v159, v149
	v_add_u32_e32 v149, 0x90, v150
	flat_store_dwordx4 v[152:153], v[156:159] offset:16 sc1
	v_mad_i64_i32 v[152:153], s[22:23], v149, s24, v[140:141]
	v_mul_f32_e32 v149, 0xbfb8aa3b, v52
	v_exp_f32_e32 v149, v149
	s_nop 0
	v_add_f32_e32 v149, 1.0, v149
	v_rcp_f32_e32 v156, v149
	v_mul_f32_e32 v149, 0xbfb8aa3b, v53
	v_exp_f32_e32 v149, v149
	s_nop 0
	v_add_f32_e32 v149, 1.0, v149
	v_rcp_f32_e32 v157, v149
	v_mul_f32_e32 v149, 0xbfb8aa3b, v54
	v_exp_f32_e32 v149, v149
	s_nop 0
	v_add_f32_e32 v149, 1.0, v149
	v_rcp_f32_e32 v158, v149
	v_mul_f32_e32 v149, 0xbfb8aa3b, v55
	v_exp_f32_e32 v149, v149
	s_nop 0
	v_add_f32_e32 v149, 1.0, v149
	v_rcp_f32_e32 v159, v149
	v_mul_f32_e32 v149, 0xbfb8aa3b, v44
	v_exp_f32_e32 v149, v149
	flat_store_dwordx4 v[152:153], v[156:159] sc1
	v_add_f32_e32 v149, 1.0, v149
	s_nop 0
	v_rcp_f32_e32 v156, v149
	v_mul_f32_e32 v149, 0xbfb8aa3b, v45
	v_exp_f32_e32 v149, v149
	s_nop 0
	v_add_f32_e32 v149, 1.0, v149
	v_rcp_f32_e32 v157, v149
	v_mul_f32_e32 v149, 0xbfb8aa3b, v46
	v_exp_f32_e32 v149, v149
	s_nop 0
	v_add_f32_e32 v149, 1.0, v149
	v_rcp_f32_e32 v158, v149
	v_mul_f32_e32 v149, 0xbfb8aa3b, v47
	v_exp_f32_e32 v149, v149
	s_nop 0
	v_add_f32_e32 v149, 1.0, v149
	v_rcp_f32_e32 v159, v149
	v_add_u32_e32 v149, 0xa0, v150
	flat_store_dwordx4 v[152:153], v[156:159] offset:16 sc1
	v_mad_i64_i32 v[152:153], s[22:23], v149, s24, v[140:141]
	v_mul_f32_e32 v149, 0xbfb8aa3b, v36
	v_exp_f32_e32 v149, v149
	s_nop 0
	v_add_f32_e32 v149, 1.0, v149
	v_rcp_f32_e32 v156, v149
	v_mul_f32_e32 v149, 0xbfb8aa3b, v37
	v_exp_f32_e32 v149, v149
	s_nop 0
	v_add_f32_e32 v149, 1.0, v149
	v_rcp_f32_e32 v157, v149
	v_mul_f32_e32 v149, 0xbfb8aa3b, v38
	v_exp_f32_e32 v149, v149
	s_nop 0
	v_add_f32_e32 v149, 1.0, v149
	v_rcp_f32_e32 v158, v149
	v_mul_f32_e32 v149, 0xbfb8aa3b, v39
	v_exp_f32_e32 v149, v149
	s_nop 0
	v_add_f32_e32 v149, 1.0, v149
	v_rcp_f32_e32 v159, v149
	v_mul_f32_e32 v149, 0xbfb8aa3b, v28
	v_exp_f32_e32 v149, v149
	flat_store_dwordx4 v[152:153], v[156:159] sc1
	v_add_f32_e32 v149, 1.0, v149
	s_nop 0
	v_rcp_f32_e32 v156, v149
	v_mul_f32_e32 v149, 0xbfb8aa3b, v29
	v_exp_f32_e32 v149, v149
	s_nop 0
	v_add_f32_e32 v149, 1.0, v149
	v_rcp_f32_e32 v157, v149
	v_mul_f32_e32 v149, 0xbfb8aa3b, v30
	v_exp_f32_e32 v149, v149
	s_nop 0
	v_add_f32_e32 v149, 1.0, v149
	v_rcp_f32_e32 v158, v149
	v_mul_f32_e32 v149, 0xbfb8aa3b, v31
	v_exp_f32_e32 v149, v149
	s_nop 0
	v_add_f32_e32 v149, 1.0, v149
	v_rcp_f32_e32 v159, v149
	v_add_u32_e32 v149, 0xb0, v150
	flat_store_dwordx4 v[152:153], v[156:159] offset:16 sc1
	v_mad_i64_i32 v[152:153], s[22:23], v149, s24, v[140:141]
	v_mul_f32_e32 v149, 0xbfb8aa3b, v20
	v_exp_f32_e32 v149, v149
	s_nop 0
	v_add_f32_e32 v149, 1.0, v149
	v_rcp_f32_e32 v156, v149
	v_mul_f32_e32 v149, 0xbfb8aa3b, v21
	v_exp_f32_e32 v149, v149
	s_nop 0
	v_add_f32_e32 v149, 1.0, v149
	v_rcp_f32_e32 v157, v149
	v_mul_f32_e32 v149, 0xbfb8aa3b, v22
	v_exp_f32_e32 v149, v149
	s_nop 0
	v_add_f32_e32 v149, 1.0, v149
	v_rcp_f32_e32 v158, v149
	v_mul_f32_e32 v149, 0xbfb8aa3b, v23
	v_exp_f32_e32 v149, v149
	s_nop 0
	v_add_f32_e32 v149, 1.0, v149
	v_rcp_f32_e32 v159, v149
	v_mul_f32_e32 v149, 0xbfb8aa3b, v12
	v_exp_f32_e32 v149, v149
	flat_store_dwordx4 v[152:153], v[156:159] sc1
	v_add_f32_e32 v149, 1.0, v149
	s_nop 0
	v_rcp_f32_e32 v156, v149
	v_mul_f32_e32 v149, 0xbfb8aa3b, v13
	v_exp_f32_e32 v149, v149
	s_nop 0
	v_add_f32_e32 v149, 1.0, v149
	v_rcp_f32_e32 v157, v149
	v_mul_f32_e32 v149, 0xbfb8aa3b, v14
	v_exp_f32_e32 v149, v149
	s_nop 0
	v_add_f32_e32 v149, 1.0, v149
	v_rcp_f32_e32 v158, v149
	v_mul_f32_e32 v149, 0xbfb8aa3b, v15
	v_exp_f32_e32 v149, v149
	s_nop 0
	v_add_f32_e32 v149, 1.0, v149
	v_rcp_f32_e32 v159, v149
	flat_store_dwordx4 v[152:153], v[156:159] offset:16 sc1

; __device__ __forceinline__ u32x4 pack8(const f32x4 a, const f32x4 b) { u32x4 w; w.x = cvt_pk_bf16(a[0], a[1]); w.y = cvt_pk_bf16(a[2], a[3]); w.z = cvt_pk_bf16(b[0], b[1]); w.w = cvt_pk_bf16(b[2], b[3]); return w; }
;     __device__ __forceinline__ void operator()(const f32x4 (&acc)[2][2][4][2], const Unit& u, int wr, int wc, int fr, int fq) const {
;     ...
;         } else if (u.pn < 10) {
;             bf16_t* base = KV + (size_t)(u.pn - 4) * kvstride;
; #pragma unroll
;             for (int ai = 0; ai < 2; ++ai)
; #pragma unroll
;                 for (int m = 0; m < 4; ++m) { const int row = row0 + ai * HALF + m * 16, b = row >> 11, s = row & 2047;
; #pragma unroll
;                     for (int bj = 0; bj < 2; ++bj) { const int ct = bj * HALF + ct0, g = ct >> 6, d = ct & 63;
;                         *(u32x4*)(base + ((size_t)((b * 4 + g) * 2048 + s)) * 64 + d) = pack8(acc[ai][bj][m][0], acc[ai][bj][m][1]); } }
.LBB0_1171:
	s_andn2_b64 vcc, exec, s[20:21]
	s_cbranch_vccnz .LBB0_1173
	s_add_i32 s20, s18, -4
	s_ashr_i32 s19, s19, 9
	s_mul_hi_u32 s21, 0x400000, s20
	s_mul_i32 s20, s20, 0x400000
	s_and_b32 s19, s19, -4
	v_lshl_add_u64 v[152:153], s[20:21], 1, v[142:143]
	s_or_b32 s20, s19, s40
	v_and_b32_e32 v149, 0x7cf, v150
	s_lshl_b32 s20, s20, 11
	v_or_b32_e32 v160, s20, v149
	v_ashrrev_i32_e32 v161, 31, v160
	v_lshlrev_b64 v[160:161], 7, v[160:161]
	s_or_b32 s19, s19, s41
	v_lshl_add_u64 v[160:161], v[152:153], 0, v[160:161]
	s_lshl_b32 s19, s19, 11
	v_cvt_pk_bf16_f32 v156, v128, v129
	v_cvt_pk_bf16_f32 v157, v130, v131
	v_cvt_pk_bf16_f32 v158, v124, v125
	v_cvt_pk_bf16_f32 v159, v126, v127
	flat_store_dwordx4 v[160:161], v[156:159] sc1
	v_or_b32_e32 v160, s19, v149
	v_ashrrev_i32_e32 v161, 31, v160
	v_lshlrev_b64 v[160:161], 7, v[160:161]
	v_lshl_add_u64 v[160:161], v[152:153], 0, v[160:161]
	v_or_b32_e32 v151, 16, v149
	v_cvt_pk_bf16_f32 v156, v120, v121
	v_cvt_pk_bf16_f32 v157, v122, v123
	v_cvt_pk_bf16_f32 v158, v116, v117
	v_cvt_pk_bf16_f32 v159, v118, v119
	flat_store_dwordx4 v[160:161], v[156:159] sc1
	v_or_b32_e32 v160, s20, v151
	v_ashrrev_i32_e32 v161, 31, v160
	v_lshlrev_b64 v[160:161], 7, v[160:161]
	v_lshl_add_u64 v[160:161], v[152:153], 0, v[160:161]
	v_cvt_pk_bf16_f32 v156, v112, v113
	v_cvt_pk_bf16_f32 v157, v114, v115
	v_cvt_pk_bf16_f32 v158, v108, v109
	v_cvt_pk_bf16_f32 v159, v110, v111
	flat_store_dwordx4 v[160:161], v[156:159] sc1
	v_or_b32_e32 v160, s19, v151
	v_ashrrev_i32_e32 v161, 31, v160
	v_lshlrev_b64 v[160:161], 7, v[160:161]
	v_lshl_add_u64 v[160:161], v[152:153], 0, v[160:161]
	v_or_b32_e32 v151, 32, v149
	v_cvt_pk_bf16_f32 v156, v104, v105
	v_cvt_pk_bf16_f32 v157, v106, v107
	v_cvt_pk_bf16_f32 v158, v100, v101
	v_cvt_pk_bf16_f32 v159, v102, v103
	flat_store_dwordx4 v[160:161], v[156:159] sc1
	v_or_b32_e32 v160, s20, v151
	v_ashrrev_i32_e32 v161, 31, v160
	v_lshlrev_b64 v[160:161], 7, v[160:161]
	v_lshl_add_u64 v[160:161], v[152:153], 0, v[160:161]
	v_cvt_pk_bf16_f32 v156, v96, v97
	v_cvt_pk_bf16_f32 v157, v98, v99
	v_cvt_pk_bf16_f32 v158, v92, v93
	v_cvt_pk_bf16_f32 v159, v94, v95
	flat_store_dwordx4 v[160:161], v[156:159] sc1
	v_or_b32_e32 v160, s19, v151
	v_ashrrev_i32_e32 v161, 31, v160
	v_lshlrev_b64 v[160:161], 7, v[160:161]
	v_lshl_add_u64 v[160:161], v[152:153], 0, v[160:161]
	v_or_b32_e32 v149, 48, v149
	v_cvt_pk_bf16_f32 v156, v88, v89
	v_cvt_pk_bf16_f32 v157, v90, v91
	v_cvt_pk_bf16_f32 v158, v84, v85
	v_cvt_pk_bf16_f32 v159, v86, v87
	flat_store_dwordx4 v[160:161], v[156:159] sc1
	v_or_b32_e32 v160, s20, v149
	v_ashrrev_i32_e32 v161, 31, v160
	v_lshlrev_b64 v[160:161], 7, v[160:161]
	v_lshl_add_u64 v[160:161], v[152:153], 0, v[160:161]
	v_cvt_pk_bf16_f32 v156, v80, v81
	v_cvt_pk_bf16_f32 v157, v82, v83
	v_cvt_pk_bf16_f32 v158, v76, v77
	v_cvt_pk_bf16_f32 v159, v78, v79
	flat_store_dwordx4 v[160:161], v[156:159] sc1
	v_or_b32_e32 v160, s19, v149
	v_ashrrev_i32_e32 v161, 31, v160
	v_add_u32_e32 v149, 0x80, v150
	v_lshlrev_b64 v[160:161], 7, v[160:161]
	v_and_b32_e32 v151, 0x7cf, v149
	v_ashrrev_i32_e32 v149, 9, v149
	v_lshl_add_u64 v[160:161], v[152:153], 0, v[160:161]
	v_and_b32_e32 v149, -4, v149
	v_cvt_pk_bf16_f32 v156, v72, v73
	v_cvt_pk_bf16_f32 v157, v74, v75
	v_cvt_pk_bf16_f32 v158, v68, v69
	v_cvt_pk_bf16_f32 v159, v70, v71
	flat_store_dwordx4 v[160:161], v[156:159] sc1
	v_or_b32_e32 v160, s40, v149
	v_lshlrev_b32_e32 v162, 11, v160
	v_or_b32_e32 v160, v162, v151
	v_ashrrev_i32_e32 v161, 31, v160
	v_lshlrev_b64 v[160:161], 7, v[160:161]
	v_or_b32_e32 v149, s41, v149
	v_lshl_add_u64 v[160:161], v[152:153], 0, v[160:161]
	v_lshlrev_b32_e32 v149, 11, v149
	v_cvt_pk_bf16_f32 v156, v64, v65
	v_cvt_pk_bf16_f32 v157, v66, v67
	v_cvt_pk_bf16_f32 v158, v60, v61
	v_cvt_pk_bf16_f32 v159, v62, v63
	flat_store_dwordx4 v[160:161], v[156:159] sc1
	v_or_b32_e32 v160, v149, v151
	v_ashrrev_i32_e32 v161, 31, v160
	v_lshlrev_b64 v[160:161], 7, v[160:161]
	v_lshl_add_u64 v[160:161], v[152:153], 0, v[160:161]
	v_or_b32_e32 v163, 16, v151
	v_cvt_pk_bf16_f32 v156, v56, v57
	v_cvt_pk_bf16_f32 v157, v58, v59
	v_cvt_pk_bf16_f32 v158, v48, v49
	v_cvt_pk_bf16_f32 v159, v50, v51
	flat_store_dwordx4 v[160:161], v[156:159] sc1
	v_or_b32_e32 v160, v162, v163
	v_ashrrev_i32_e32 v161, 31, v160
	v_lshlrev_b64 v[160:161], 7, v[160:161]
	v_lshl_add_u64 v[160:161], v[152:153], 0, v[160:161]
	v_cvt_pk_bf16_f32 v156, v52, v53
	v_cvt_pk_bf16_f32 v157, v54, v55
	v_cvt_pk_bf16_f32 v158, v44, v45
	v_cvt_pk_bf16_f32 v159, v46, v47
	flat_store_dwordx4 v[160:161], v[156:159] sc1
	v_or_b32_e32 v160, v149, v163
	v_ashrrev_i32_e32 v161, 31, v160
	v_lshlrev_b64 v[160:161], 7, v[160:161]
	v_lshl_add_u64 v[160:161], v[152:153], 0, v[160:161]
	v_or_b32_e32 v163, 32, v151
	v_cvt_pk_bf16_f32 v156, v40, v41
	v_cvt_pk_bf16_f32 v157, v42, v43
	v_cvt_pk_bf16_f32 v158, v32, v33
	v_cvt_pk_bf16_f32 v159, v34, v35
	flat_store_dwordx4 v[160:161], v[156:159] sc1
	v_or_b32_e32 v160, v162, v163
	v_ashrrev_i32_e32 v161, 31, v160
	v_lshlrev_b64 v[160:161], 7, v[160:161]
	v_lshl_add_u64 v[160:161], v[152:153], 0, v[160:161]
	v_cvt_pk_bf16_f32 v156, v36, v37
	v_cvt_pk_bf16_f32 v157, v38, v39
	v_cvt_pk_bf16_f32 v158, v28, v29
	v_cvt_pk_bf16_f32 v159, v30, v31
	flat_store_dwordx4 v[160:161], v[156:159] sc1
	v_or_b32_e32 v160, v149, v163
	v_ashrrev_i32_e32 v161, 31, v160
	v_lshlrev_b64 v[160:161], 7, v[160:161]
	v_lshl_add_u64 v[160:161], v[152:153], 0, v[160:161]
	v_or_b32_e32 v151, 48, v151
	v_cvt_pk_bf16_f32 v156, v24, v25
	v_cvt_pk_bf16_f32 v157, v26, v27
	v_cvt_pk_bf16_f32 v158, v16, v17
	v_cvt_pk_bf16_f32 v159, v18, v19
	flat_store_dwordx4 v[160:161], v[156:159] sc1
	v_or_b32_e32 v160, v162, v151
	v_ashrrev_i32_e32 v161, 31, v160
	v_lshlrev_b64 v[160:161], 7, v[160:161]
	v_lshl_add_u64 v[160:161], v[152:153], 0, v[160:161]
	v_cvt_pk_bf16_f32 v156, v20, v21
	v_cvt_pk_bf16_f32 v157, v22, v23
	v_cvt_pk_bf16_f32 v158, v12, v13
	v_cvt_pk_bf16_f32 v159, v14, v15
	flat_store_dwordx4 v[160:161], v[156:159] sc1
	v_or_b32_e32 v160, v149, v151
	v_ashrrev_i32_e32 v161, 31, v160
	v_lshlrev_b64 v[160:161], 7, v[160:161]
	v_lshl_add_u64 v[152:153], v[152:153], 0, v[160:161]
	v_cvt_pk_bf16_f32 v156, v8, v9
	v_cvt_pk_bf16_f32 v157, v10, v11
	v_cvt_pk_bf16_f32 v158, v4, v5
	v_cvt_pk_bf16_f32 v159, v6, v7
	flat_store_dwordx4 v[152:153], v[156:159] sc1

; __device__ __forceinline__ u32x4 pack8(const f32x4 a, const f32x4 b) { u32x4 w; w.x = cvt_pk_bf16(a[0], a[1]); w.y = cvt_pk_bf16(a[2], a[3]); w.z = cvt_pk_bf16(b[0], b[1]); w.w = cvt_pk_bf16(b[2], b[3]); return w; }
;     __device__ __forceinline__ void operator()(const f32x4 (&acc)[2][2][4][2], const Unit& u, int wr, int wc, int fr, int fq) const {
;     ...
;         if (u.pn < 4) {
; #pragma unroll
;             for (int ai = 0; ai < 2; ++ai)
; #pragma unroll
;                 for (int m = 0; m < 4; ++m) { bf16_t* rowp = Q + (size_t)(row0 + ai * HALF + m * 16) * 1024 + u.pn * BM + ct0;
; #pragma unroll
;                     for (int bj = 0; bj < 2; ++bj) *(u32x4*)(rowp + bj * HALF) = pack8(acc[ai][bj][m][0] * qscale, acc[ai][bj][m][1] * qscale); }
.LBB0_1174:
	v_ashrrev_i32_e32 v151, 31, v150
	s_lshl_b32 s18, s18, 8
	v_lshlrev_b64 v[152:153], 11, v[150:151]
	s_ashr_i32 s19, s18, 31
	v_lshl_add_u64 v[152:153], s[10:11], 0, v[152:153]
	s_lshl_b64 s[18:19], s[18:19], 1
	v_readlane_b32 s20, v253, 57
	v_lshl_add_u64 v[152:153], v[152:153], 0, s[18:19]
	v_mov_b32_e32 v149, v3
	v_readlane_b32 s21, v253, 58
	v_lshl_add_u64 v[152:153], v[152:153], 0, v[148:149]
	v_pk_mul_f32 v[130:131], s[14:15], v[130:131]
	v_pk_mul_f32 v[128:129], s[20:21], v[128:129]
	v_pk_mul_f32 v[156:157], s[14:15], v[126:127]
	v_pk_mul_f32 v[126:127], s[20:21], v[124:125]
	v_cvt_pk_bf16_f32 v124, v128, v129
	v_cvt_pk_bf16_f32 v125, v130, v131
	v_pk_mul_f32 v[120:121], s[20:21], v[120:121]
	v_cvt_pk_bf16_f32 v126, v126, v127
	v_cvt_pk_bf16_f32 v127, v156, v157
	flat_store_dwordx4 v[152:153], v[124:127] sc1
	v_pk_mul_f32 v[122:123], s[14:15], v[122:123]
	v_pk_mul_f32 v[114:115], s[14:15], v[114:115]
	v_pk_mul_f32 v[124:125], s[14:15], v[118:119]
	v_pk_mul_f32 v[118:119], s[20:21], v[116:117]
	v_cvt_pk_bf16_f32 v116, v120, v121
	v_cvt_pk_bf16_f32 v117, v122, v123
	v_pk_mul_f32 v[112:113], s[20:21], v[112:113]
	v_cvt_pk_bf16_f32 v118, v118, v119
	v_cvt_pk_bf16_f32 v119, v124, v125
	flat_store_dwordx4 v[152:153], v[116:119] offset:256 sc1
	v_pk_mul_f32 v[104:105], s[20:21], v[104:105]
	v_pk_mul_f32 v[106:107], s[14:15], v[106:107]
	v_or_b32_e32 v116, 16, v150
	v_ashrrev_i32_e32 v117, 31, v116
	v_lshlrev_b64 v[116:117], 11, v[116:117]
	v_lshl_add_u64 v[116:117], s[10:11], 0, v[116:117]
	v_lshl_add_u64 v[116:117], v[116:117], 0, s[18:19]
	v_lshl_add_u64 v[116:117], v[116:117], 0, v[148:149]
	v_pk_mul_f32 v[118:119], s[14:15], v[110:111]
	v_pk_mul_f32 v[110:111], s[20:21], v[108:109]
	v_cvt_pk_bf16_f32 v108, v112, v113
	v_cvt_pk_bf16_f32 v109, v114, v115
	v_pk_mul_f32 v[98:99], s[14:15], v[98:99]
	v_cvt_pk_bf16_f32 v110, v110, v111
	v_cvt_pk_bf16_f32 v111, v118, v119
	flat_store_dwordx4 v[116:117], v[108:111] sc1
	v_pk_mul_f32 v[96:97], s[20:21], v[96:97]
	v_pk_mul_f32 v[88:89], s[20:21], v[88:89]
	v_pk_mul_f32 v[108:109], s[14:15], v[102:103]
	v_pk_mul_f32 v[102:103], s[20:21], v[100:101]
	v_cvt_pk_bf16_f32 v100, v104, v105
	v_cvt_pk_bf16_f32 v101, v106, v107
	v_pk_mul_f32 v[90:91], s[14:15], v[90:91]
	v_cvt_pk_bf16_f32 v102, v102, v103
	v_cvt_pk_bf16_f32 v103, v108, v109
	flat_store_dwordx4 v[116:117], v[100:103] offset:256 sc1
	v_pk_mul_f32 v[82:83], s[14:15], v[82:83]
	v_pk_mul_f32 v[80:81], s[20:21], v[80:81]
	v_or_b32_e32 v100, 32, v150
	v_ashrrev_i32_e32 v101, 31, v100
	v_lshlrev_b64 v[100:101], 11, v[100:101]
	v_lshl_add_u64 v[100:101], s[10:11], 0, v[100:101]
	v_lshl_add_u64 v[100:101], v[100:101], 0, s[18:19]
	v_lshl_add_u64 v[100:101], v[100:101], 0, v[148:149]
	v_pk_mul_f32 v[102:103], s[14:15], v[94:95]
	v_pk_mul_f32 v[94:95], s[20:21], v[92:93]
	v_cvt_pk_bf16_f32 v92, v96, v97
	v_cvt_pk_bf16_f32 v93, v98, v99
	v_pk_mul_f32 v[74:75], s[14:15], v[74:75]
	v_cvt_pk_bf16_f32 v94, v94, v95
	v_cvt_pk_bf16_f32 v95, v102, v103
	flat_store_dwordx4 v[100:101], v[92:95] sc1
	v_pk_mul_f32 v[72:73], s[20:21], v[72:73]
	v_pk_mul_f32 v[64:65], s[20:21], v[64:65]
	v_pk_mul_f32 v[92:93], s[14:15], v[86:87]
	v_pk_mul_f32 v[86:87], s[20:21], v[84:85]
	v_cvt_pk_bf16_f32 v84, v88, v89
	v_cvt_pk_bf16_f32 v85, v90, v91
	v_pk_mul_f32 v[66:67], s[14:15], v[66:67]
	v_cvt_pk_bf16_f32 v86, v86, v87
	v_cvt_pk_bf16_f32 v87, v92, v93
	flat_store_dwordx4 v[100:101], v[84:87] offset:256 sc1
	v_pk_mul_f32 v[58:59], s[14:15], v[58:59]
	v_pk_mul_f32 v[56:57], s[20:21], v[56:57]
	v_or_b32_e32 v84, 48, v150
	v_ashrrev_i32_e32 v85, 31, v84
	v_lshlrev_b64 v[84:85], 11, v[84:85]
	v_lshl_add_u64 v[84:85], s[10:11], 0, v[84:85]
	v_lshl_add_u64 v[84:85], v[84:85], 0, s[18:19]
	v_lshl_add_u64 v[84:85], v[84:85], 0, v[148:149]
	v_pk_mul_f32 v[86:87], s[14:15], v[78:79]
	v_pk_mul_f32 v[78:79], s[20:21], v[76:77]
	v_cvt_pk_bf16_f32 v76, v80, v81
	v_cvt_pk_bf16_f32 v77, v82, v83
; __device__ __forceinline__ u32x4 pack8(const f32x4 a, const f32x4 b) { u32x4 w; w.x = cvt_pk_bf16(a[0], a[1]); w.y = cvt_pk_bf16(a[2], a[3]); w.z = cvt_pk_bf16(b[0], b[1]); w.w = cvt_pk_bf16(b[2], b[3]); return w; }
;     __device__ __forceinline__ void operator()(const f32x4 (&acc)[2][2][4][2], const Unit& u, int wr, int wc, int fr, int fq) const {
;     ...
;         if (u.pn < 4) {
; #pragma unroll
;             for (int ai = 0; ai < 2; ++ai)
; #pragma unroll
;                 for (int m = 0; m < 4; ++m) { bf16_t* rowp = Q + (size_t)(row0 + ai * HALF + m * 16) * 1024 + u.pn * BM + ct0;
; #pragma unroll
;                     for (int bj = 0; bj < 2; ++bj) *(u32x4*)(rowp + bj * HALF) = pack8(acc[ai][bj][m][0] * qscale, acc[ai][bj][m][1] * qscale); }
	s_mov_b64 s[18:19], 0x40000
	v_cvt_pk_bf16_f32 v78, v78, v79
	v_cvt_pk_bf16_f32 v79, v86, v87
	flat_store_dwordx4 v[84:85], v[76:79] sc1
	v_pk_mul_f32 v[52:53], s[20:21], v[52:53]
	v_pk_mul_f32 v[42:43], s[14:15], v[42:43]
	v_pk_mul_f32 v[76:77], s[14:15], v[70:71]
	v_pk_mul_f32 v[70:71], s[20:21], v[68:69]
	v_cvt_pk_bf16_f32 v68, v72, v73
	v_cvt_pk_bf16_f32 v69, v74, v75
	v_pk_mul_f32 v[40:41], s[20:21], v[40:41]
	v_cvt_pk_bf16_f32 v70, v70, v71
	v_cvt_pk_bf16_f32 v71, v76, v77
	flat_store_dwordx4 v[84:85], v[68:71] offset:256 sc1
	v_pk_mul_f32 v[36:37], s[20:21], v[36:37]
	v_pk_mul_f32 v[26:27], s[14:15], v[26:27]
	v_lshl_add_u64 v[68:69], v[152:153], 0, s[18:19]
	s_mov_b32 s18, 0x40000
	v_pk_mul_f32 v[70:71], s[14:15], v[62:63]
	v_pk_mul_f32 v[62:63], s[20:21], v[60:61]
	v_cvt_pk_bf16_f32 v60, v64, v65
	v_add_co_u32_e32 v64, vcc, s18, v152
	v_cvt_pk_bf16_f32 v61, v66, v67
	v_cvt_pk_bf16_f32 v62, v62, v63
	v_cvt_pk_bf16_f32 v63, v70, v71
	s_mov_b64 s[18:19], 0x48000
	s_nop 0
	v_addc_co_u32_e32 v65, vcc, 0, v153, vcc
	flat_store_dwordx4 v[64:65], v[60:63] sc1
	v_pk_mul_f32 v[24:25], s[20:21], v[24:25]
	v_pk_mul_f32 v[20:21], s[20:21], v[20:21]
	v_pk_mul_f32 v[60:61], s[14:15], v[50:51]
	v_pk_mul_f32 v[50:51], s[20:21], v[48:49]
	v_cvt_pk_bf16_f32 v48, v56, v57
	v_cvt_pk_bf16_f32 v49, v58, v59
	v_pk_mul_f32 v[10:11], s[14:15], v[10:11]
	v_cvt_pk_bf16_f32 v50, v50, v51
	v_cvt_pk_bf16_f32 v51, v60, v61
	flat_store_dwordx4 v[68:69], v[48:51] offset:256 sc1
	v_pk_mul_f32 v[8:9], s[20:21], v[8:9]
	s_nop 0
	v_lshl_add_u64 v[48:49], v[152:153], 0, s[18:19]
	v_pk_mul_f32 v[50:51], s[14:15], v[54:55]
	s_mov_b32 s18, 0x48000
	v_pk_mul_f32 v[54:55], s[14:15], v[46:47]
	v_pk_mul_f32 v[46:47], s[20:21], v[44:45]
	v_cvt_pk_bf16_f32 v44, v52, v53
	v_cvt_pk_bf16_f32 v45, v50, v51
	v_add_co_u32_e32 v50, vcc, s18, v152
	v_cvt_pk_bf16_f32 v46, v46, v47
	v_cvt_pk_bf16_f32 v47, v54, v55
	s_mov_b64 s[18:19], 0x50000
	s_nop 0
	v_addc_co_u32_e32 v51, vcc, 0, v153, vcc
	flat_store_dwordx4 v[50:51], v[44:47]
	s_nop 1
	v_pk_mul_f32 v[44:45], s[14:15], v[34:35]
	v_pk_mul_f32 v[34:35], s[20:21], v[32:33]
	v_cvt_pk_bf16_f32 v32, v40, v41
	v_cvt_pk_bf16_f32 v33, v42, v43
	s_nop 0
	v_cvt_pk_bf16_f32 v34, v34, v35
	v_cvt_pk_bf16_f32 v35, v44, v45
	flat_store_dwordx4 v[48:49], v[32:35] offset:256
	s_nop 1
	v_lshl_add_u64 v[32:33], v[152:153], 0, s[18:19]
	v_pk_mul_f32 v[34:35], s[14:15], v[38:39]
	s_mov_b32 s18, 0x50000
	v_pk_mul_f32 v[38:39], s[14:15], v[30:31]
	v_pk_mul_f32 v[30:31], s[20:21], v[28:29]
	v_cvt_pk_bf16_f32 v28, v36, v37
	v_cvt_pk_bf16_f32 v29, v34, v35
	v_add_co_u32_e32 v34, vcc, s18, v152
	v_cvt_pk_bf16_f32 v30, v30, v31
	v_cvt_pk_bf16_f32 v31, v38, v39
	s_mov_b64 s[18:19], 0x58000
	s_nop 0
	v_addc_co_u32_e32 v35, vcc, 0, v153, vcc
	flat_store_dwordx4 v[34:35], v[28:31]
	s_nop 1
	v_pk_mul_f32 v[28:29], s[14:15], v[18:19]
	v_pk_mul_f32 v[18:19], s[20:21], v[16:17]
	v_cvt_pk_bf16_f32 v16, v24, v25
	v_cvt_pk_bf16_f32 v17, v26, v27
	s_nop 0
	v_cvt_pk_bf16_f32 v18, v18, v19
	v_cvt_pk_bf16_f32 v19, v28, v29
	flat_store_dwordx4 v[32:33], v[16:19] offset:256
	s_nop 1
	v_lshl_add_u64 v[16:17], v[152:153], 0, s[18:19]
	v_pk_mul_f32 v[18:19], s[14:15], v[22:23]
	s_mov_b32 s18, 0x58000
	v_pk_mul_f32 v[22:23], s[14:15], v[14:15]
	v_pk_mul_f32 v[14:15], s[20:21], v[12:13]
	v_cvt_pk_bf16_f32 v12, v20, v21
	v_cvt_pk_bf16_f32 v13, v18, v19
	v_add_co_u32_e32 v18, vcc, s18, v152
	v_cvt_pk_bf16_f32 v14, v14, v15
	v_cvt_pk_bf16_f32 v15, v22, v23
	s_nop 1
	v_addc_co_u32_e32 v19, vcc, 0, v153, vcc
	flat_store_dwordx4 v[18:19], v[12:15]
	s_nop 1
	v_pk_mul_f32 v[12:13], s[14:15], v[6:7]
	v_pk_mul_f32 v[6:7], s[20:21], v[4:5]
	v_cvt_pk_bf16_f32 v4, v8, v9
	v_cvt_pk_bf16_f32 v5, v10, v11
	s_nop 0
	v_cvt_pk_bf16_f32 v6, v6, v7
	v_cvt_pk_bf16_f32 v7, v12, v13
	flat_store_dwordx4 v[16:17], v[4:7] offset:256
	s_andn2_b64 vcc, exec, s[16:17]
	s_mov_b64 s[18:19], -1
	s_cbranch_vccnz .LBB0_1159

; __device__ __forceinline__ u32x4 pack8(const f32x4 a, const f32x4 b) { u32x4 w; w.x = cvt_pk_bf16(a[0], a[1]); w.y = cvt_pk_bf16(a[2], a[3]); w.z = cvt_pk_bf16(b[0], b[1]); w.w = cvt_pk_bf16(b[2], b[3]); return w; }
;     __device__ __forceinline__ void operator()(const f32x4 (&acc)[2][2][4][2], const Unit& u, int wr, int wc, int fr, int fq) const {
;         const int row0 = u.pm * BM + wr * 64 + fr, ct0 = wc * 32 + 8 * fq;
; #pragma unroll
;         for (int ai = 0; ai < 2; ++ai)
; #pragma unroll
;             for (int m = 0; m < 4; ++m) { bf16_t* rowp = S + (size_t)(row0 + ai * HALF + m * 16) * 256 + ct0;
; #pragma unroll
;                 for (int bj = 0; bj < 2; ++bj) *(u32x4*)(rowp + bj * HALF) = pack8(acc[ai][bj][m][0], acc[ai][bj][m][1]); }
;     }
.LBB0_1239:
	v_lshl_add_u32 v148, s42, 8, v2
	v_ashrrev_i32_e32 v149, 31, v148
	v_lshlrev_b64 v[150:151], 9, v[148:149]
	v_lshl_add_u64 v[150:151], v[140:141], 0, v[150:151]
	v_cvt_pk_bf16_f32 v124, v124, v125
	v_cvt_pk_bf16_f32 v125, v126, v127
	v_cvt_pk_bf16_f32 v126, v128, v129
	v_cvt_pk_bf16_f32 v127, v130, v131
	flat_store_dwordx4 v[150:151], v[124:127] sc1
	v_cvt_pk_bf16_f32 v120, v120, v121
	v_cvt_pk_bf16_f32 v121, v122, v123
	v_cvt_pk_bf16_f32 v122, v116, v117
	v_or_b32_e32 v116, 16, v148
	v_ashrrev_i32_e32 v117, 31, v116
	v_lshlrev_b64 v[116:117], 9, v[116:117]
	v_lshl_add_u64 v[116:117], v[140:141], 0, v[116:117]
	v_cvt_pk_bf16_f32 v123, v118, v119
	flat_store_dwordx4 v[150:151], v[120:123] offset:256 sc1
	v_cvt_pk_bf16_f32 v112, v112, v113
	v_cvt_pk_bf16_f32 v113, v114, v115
	v_cvt_pk_bf16_f32 v114, v108, v109
	v_cvt_pk_bf16_f32 v115, v110, v111
	flat_store_dwordx4 v[116:117], v[112:115] sc1
	v_cvt_pk_bf16_f32 v104, v104, v105
	v_cvt_pk_bf16_f32 v105, v106, v107
	v_cvt_pk_bf16_f32 v106, v100, v101
	v_or_b32_e32 v100, 32, v148
	v_ashrrev_i32_e32 v101, 31, v100
	v_lshlrev_b64 v[100:101], 9, v[100:101]
	v_lshl_add_u64 v[100:101], v[140:141], 0, v[100:101]
	v_cvt_pk_bf16_f32 v107, v102, v103
	flat_store_dwordx4 v[116:117], v[104:107] offset:256 sc1
	v_cvt_pk_bf16_f32 v96, v96, v97
	v_cvt_pk_bf16_f32 v97, v98, v99
	v_cvt_pk_bf16_f32 v98, v92, v93
	v_cvt_pk_bf16_f32 v99, v94, v95
	flat_store_dwordx4 v[100:101], v[96:99] sc1
	v_cvt_pk_bf16_f32 v88, v88, v89
	v_cvt_pk_bf16_f32 v89, v90, v91
	v_cvt_pk_bf16_f32 v90, v84, v85
	v_or_b32_e32 v84, 48, v148
	v_ashrrev_i32_e32 v85, 31, v84
	v_lshlrev_b64 v[84:85], 9, v[84:85]
	v_lshl_add_u64 v[84:85], v[140:141], 0, v[84:85]
	v_cvt_pk_bf16_f32 v91, v86, v87
	flat_store_dwordx4 v[100:101], v[88:91] offset:256 sc1
	v_cvt_pk_bf16_f32 v80, v80, v81
	v_cvt_pk_bf16_f32 v81, v82, v83
	v_cvt_pk_bf16_f32 v82, v76, v77
	v_cvt_pk_bf16_f32 v83, v78, v79
	flat_store_dwordx4 v[84:85], v[80:83] sc1
	v_cvt_pk_bf16_f32 v72, v72, v73
	v_cvt_pk_bf16_f32 v73, v74, v75
	v_cvt_pk_bf16_f32 v74, v68, v69
	v_cvt_pk_bf16_f32 v75, v70, v71
	flat_store_dwordx4 v[84:85], v[72:75] offset:256 sc1
	s_mov_b64 s[16:17], 0x10000
	v_cvt_pk_bf16_f32 v64, v64, v65
	v_cvt_pk_bf16_f32 v65, v66, v67
	v_cvt_pk_bf16_f32 v66, v60, v61
	v_add_co_u32_e32 v60, vcc, s79, v150
	v_lshl_add_u64 v[68:69], v[150:151], 0, s[16:17]
	s_nop 0
	v_addc_co_u32_e32 v61, vcc, 0, v151, vcc
	s_mov_b64 s[16:17], 0x12000
	v_cvt_pk_bf16_f32 v67, v62, v63
	flat_store_dwordx4 v[60:61], v[64:67] sc1
	v_cvt_pk_bf16_f32 v56, v56, v57
	v_cvt_pk_bf16_f32 v57, v58, v59
	v_cvt_pk_bf16_f32 v58, v52, v53
	v_lshl_add_u64 v[52:53], v[150:151], 0, s[16:17]
	s_mov_b32 s16, 0x12000
	v_cvt_pk_bf16_f32 v59, v54, v55
	flat_store_dwordx4 v[68:69], v[56:59] offset:256 sc1
	v_cvt_pk_bf16_f32 v48, v48, v49
	v_cvt_pk_bf16_f32 v49, v50, v51
	v_cvt_pk_bf16_f32 v50, v44, v45
	v_add_co_u32_e32 v44, vcc, s16, v150
	s_mov_b64 s[16:17], 0x14000
	s_nop 0
	v_addc_co_u32_e32 v45, vcc, 0, v151, vcc
	v_cvt_pk_bf16_f32 v51, v46, v47
	flat_store_dwordx4 v[44:45], v[48:51] sc1
	v_cvt_pk_bf16_f32 v40, v40, v41
	v_cvt_pk_bf16_f32 v41, v42, v43
	v_cvt_pk_bf16_f32 v42, v36, v37
	v_lshl_add_u64 v[36:37], v[150:151], 0, s[16:17]
	s_mov_b32 s16, 0x14000
	v_cvt_pk_bf16_f32 v43, v38, v39
	flat_store_dwordx4 v[52:53], v[40:43] offset:256 sc1
	v_cvt_pk_bf16_f32 v32, v32, v33
	v_cvt_pk_bf16_f32 v33, v34, v35
	v_cvt_pk_bf16_f32 v34, v28, v29
	v_add_co_u32_e32 v28, vcc, s16, v150
	v_cvt_pk_bf16_f32 v35, v30, v31
	s_mov_b64 s[16:17], 0x16000
	s_nop 0
	v_addc_co_u32_e32 v29, vcc, 0, v151, vcc
	flat_store_dwordx4 v[28:29], v[32:35] sc1
	v_cvt_pk_bf16_f32 v24, v24, v25
	v_cvt_pk_bf16_f32 v25, v26, v27
	v_cvt_pk_bf16_f32 v26, v20, v21
	v_cvt_pk_bf16_f32 v27, v22, v23
	flat_store_dwordx4 v[36:37], v[24:27] offset:256 sc1
	v_cvt_pk_bf16_f32 v16, v16, v17
	v_cvt_pk_bf16_f32 v17, v18, v19
	v_cvt_pk_bf16_f32 v18, v12, v13
	v_add_co_u32_e32 v12, vcc, 0x16000, v150
	v_lshl_add_u64 v[20:21], v[150:151], 0, s[16:17]
	s_nop 0
	v_addc_co_u32_e32 v13, vcc, 0, v151, vcc
	s_cmp_eq_u32 s41, 3
	s_mov_b64 s[16:17], -1
	v_cvt_pk_bf16_f32 v19, v14, v15
	flat_store_dwordx4 v[12:13], v[16:19] sc1
	v_cvt_pk_bf16_f32 v8, v8, v9
	v_cvt_pk_bf16_f32 v9, v10, v11
	v_cvt_pk_bf16_f32 v10, v4, v5
	v_cvt_pk_bf16_f32 v11, v6, v7
	flat_store_dwordx4 v[20:21], v[8:11] offset:256 sc1
	s_cbranch_scc1 .LBB0_1233
	s_andn2_b64 vcc, exec, s[6:7]
	s_cbranch_vccnz .LBB0_1232
	s_barrier
	s_branch .LBB0_1232

; __device__ __forceinline__ float sigm(float x) { return __builtin_amdgcn_rcpf(1.0f + __builtin_amdgcn_exp2f(-1.4426950408889634f * x)); }
;     __device__ __forceinline__ void operator()(const f32x4 (&acc)[2][2][4][2], const Unit& u, int wr, int wc, int fr, int fq) const {
;     ...
;         } else {
;             if (ct0 < 48) {
; #pragma unroll
;                 for (int ai = 0; ai < 2; ++ai)
; #pragma unroll
;                     for (int m = 0; m < 4; ++m) { float* gp = gates + (size_t)(row0 + ai * HALF + m * 16) * 48 + ct0;
; #pragma unroll
;                         for (int n = 0; n < 2; ++n) { const f32x4 v = acc[ai][0][m][n]; *(f32x4*)(gp + 4 * n) = (f32x4){sigm(v[0]), sigm(v[1]), sigm(v[2]), sigm(v[3])}; } }
;             }
.LBB0_1250:
	s_lshl_b32 s4, s17, 8
	s_add_i32 s6, s25, s4
	v_lshl_or_b32 v136, s15, 5, v144
	v_or_b32_e32 v2, s6, v2
	s_cmp_gt_u32 s22, 15
	s_mov_b64 s[4:5], -1
	s_cbranch_scc0 .LBB0_1254
	v_cmp_gt_u32_e32 vcc, 48, v136
	s_and_saveexec_b64 s[4:5], vcc
	s_cbranch_execz .LBB0_1253
	v_mul_f32_e32 v137, 0xbfb8aa3b, v128
	v_exp_f32_e32 v137, v137
	s_add_u32 s2, s2, 0x400000
	s_addc_u32 s3, s3, 0
	v_mov_b64_e32 v[132:133], s[2:3]
	s_movk_i32 s7, 0xc0
	v_mad_i64_i32 v[138:139], s[2:3], v2, s7, v[132:133]
	v_lshlrev_b32_e32 v134, 2, v136
	v_mov_b32_e32 v135, v3
	v_add_f32_e32 v137, 1.0, v137
	v_lshl_add_u64 v[142:143], v[138:139], 0, v[134:135]
	v_rcp_f32_e32 v138, v137
	v_mul_f32_e32 v137, 0xbfb8aa3b, v129
	v_exp_f32_e32 v137, v137
	s_nop 0
	v_add_f32_e32 v137, 1.0, v137
	v_rcp_f32_e32 v139, v137
	v_mul_f32_e32 v137, 0xbfb8aa3b, v130
	v_exp_f32_e32 v137, v137
	s_nop 0
	v_add_f32_e32 v137, 1.0, v137
	v_rcp_f32_e32 v140, v137
	v_mul_f32_e32 v137, 0xbfb8aa3b, v131
	v_exp_f32_e32 v137, v137
	s_nop 0
	v_add_f32_e32 v137, 1.0, v137
	v_rcp_f32_e32 v141, v137
	v_mul_f32_e32 v137, 0xbfb8aa3b, v124
	v_exp_f32_e32 v137, v137
	flat_store_dwordx4 v[142:143], v[138:141] sc1
	v_add_f32_e32 v137, 1.0, v137
	s_nop 0
	v_rcp_f32_e32 v138, v137
	v_mul_f32_e32 v137, 0xbfb8aa3b, v125
	v_exp_f32_e32 v137, v137
	s_nop 0
	v_add_f32_e32 v137, 1.0, v137
	v_rcp_f32_e32 v139, v137
	v_mul_f32_e32 v137, 0xbfb8aa3b, v126
	v_exp_f32_e32 v137, v137
	s_nop 0
	v_add_f32_e32 v137, 1.0, v137
	v_rcp_f32_e32 v140, v137
	v_mul_f32_e32 v137, 0xbfb8aa3b, v127
	v_exp_f32_e32 v137, v137
	s_nop 0
	v_add_f32_e32 v137, 1.0, v137
	v_rcp_f32_e32 v141, v137
	v_or_b32_e32 v137, 16, v2
	flat_store_dwordx4 v[142:143], v[138:141] offset:16 sc1
	s_nop 1
	v_mad_i64_i32 v[138:139], s[2:3], v137, s7, v[132:133]
	v_mul_f32_e32 v137, 0xbfb8aa3b, v116
	v_exp_f32_e32 v137, v137
	v_lshl_add_u64 v[142:143], v[138:139], 0, v[134:135]
	v_add_f32_e32 v137, 1.0, v137
	v_rcp_f32_e32 v138, v137
	v_mul_f32_e32 v137, 0xbfb8aa3b, v117
	v_exp_f32_e32 v137, v137
	s_nop 0
	v_add_f32_e32 v137, 1.0, v137
	v_rcp_f32_e32 v139, v137
	v_mul_f32_e32 v137, 0xbfb8aa3b, v118
	v_exp_f32_e32 v137, v137
	s_nop 0
	v_add_f32_e32 v137, 1.0, v137
	v_rcp_f32_e32 v140, v137
	v_mul_f32_e32 v137, 0xbfb8aa3b, v119
	v_exp_f32_e32 v137, v137
	s_nop 0
	v_add_f32_e32 v137, 1.0, v137
	v_rcp_f32_e32 v141, v137
	v_mul_f32_e32 v137, 0xbfb8aa3b, v108
	v_exp_f32_e32 v137, v137
	flat_store_dwordx4 v[142:143], v[138:141] sc1
	v_add_f32_e32 v137, 1.0, v137
	s_nop 0
	v_rcp_f32_e32 v138, v137
	v_mul_f32_e32 v137, 0xbfb8aa3b, v109
	v_exp_f32_e32 v137, v137
	s_nop 0
	v_add_f32_e32 v137, 1.0, v137
	v_rcp_f32_e32 v139, v137
	v_mul_f32_e32 v137, 0xbfb8aa3b, v110
	v_exp_f32_e32 v137, v137
	s_nop 0
	v_add_f32_e32 v137, 1.0, v137
	v_rcp_f32_e32 v140, v137
	v_mul_f32_e32 v137, 0xbfb8aa3b, v111
	v_exp_f32_e32 v137, v137
	s_nop 0
	v_add_f32_e32 v137, 1.0, v137
	v_rcp_f32_e32 v141, v137
	v_or_b32_e32 v137, 32, v2
	flat_store_dwordx4 v[142:143], v[138:141] offset:16 sc1
	s_nop 1
	v_mad_i64_i32 v[138:139], s[2:3], v137, s7, v[132:133]
	v_mul_f32_e32 v137, 0xbfb8aa3b, v104
	v_exp_f32_e32 v137, v137
	v_lshl_add_u64 v[142:143], v[138:139], 0, v[134:135]
	v_add_f32_e32 v137, 1.0, v137
	v_rcp_f32_e32 v138, v137
	v_mul_f32_e32 v137, 0xbfb8aa3b, v105
	v_exp_f32_e32 v137, v137
	s_nop 0
	v_add_f32_e32 v137, 1.0, v137
	v_rcp_f32_e32 v139, v137
	v_mul_f32_e32 v137, 0xbfb8aa3b, v106
	v_exp_f32_e32 v137, v137
	s_nop 0
	v_add_f32_e32 v137, 1.0, v137
	v_rcp_f32_e32 v140, v137
	v_mul_f32_e32 v137, 0xbfb8aa3b, v107
	v_exp_f32_e32 v137, v137
	s_nop 0
	v_add_f32_e32 v137, 1.0, v137
	v_rcp_f32_e32 v141, v137
	v_mul_f32_e32 v137, 0xbfb8aa3b, v96
	v_exp_f32_e32 v137, v137
	flat_store_dwordx4 v[142:143], v[138:141] sc1
	v_add_f32_e32 v137, 1.0, v137
	s_nop 0
	v_rcp_f32_e32 v138, v137
	v_mul_f32_e32 v137, 0xbfb8aa3b, v97
	v_exp_f32_e32 v137, v137
	s_nop 0
	v_add_f32_e32 v137, 1.0, v137
	v_rcp_f32_e32 v139, v137
	v_mul_f32_e32 v137, 0xbfb8aa3b, v98
	v_exp_f32_e32 v137, v137
	s_nop 0
	v_add_f32_e32 v137, 1.0, v137
	v_rcp_f32_e32 v140, v137
	v_mul_f32_e32 v137, 0xbfb8aa3b, v99
	v_exp_f32_e32 v137, v137
	s_nop 0
	v_add_f32_e32 v137, 1.0, v137
	v_rcp_f32_e32 v141, v137
	v_or_b32_e32 v137, 48, v2
	flat_store_dwordx4 v[142:143], v[138:141] offset:16 sc1
	s_nop 1
	v_mad_i64_i32 v[138:139], s[2:3], v137, s7, v[132:133]
	v_mul_f32_e32 v137, 0xbfb8aa3b, v88
	v_exp_f32_e32 v137, v137
	v_lshl_add_u64 v[142:143], v[138:139], 0, v[134:135]
	v_add_f32_e32 v137, 1.0, v137
	v_rcp_f32_e32 v138, v137
	v_mul_f32_e32 v137, 0xbfb8aa3b, v89
	v_exp_f32_e32 v137, v137
	s_nop 0
	v_add_f32_e32 v137, 1.0, v137
	v_rcp_f32_e32 v139, v137
	v_mul_f32_e32 v137, 0xbfb8aa3b, v90
	v_exp_f32_e32 v137, v137
	s_nop 0
	v_add_f32_e32 v137, 1.0, v137
	v_rcp_f32_e32 v140, v137
	v_mul_f32_e32 v137, 0xbfb8aa3b, v91
	v_exp_f32_e32 v137, v137
	s_nop 0
	v_add_f32_e32 v137, 1.0, v137
	v_rcp_f32_e32 v141, v137
	v_mul_f32_e32 v137, 0xbfb8aa3b, v80
	v_exp_f32_e32 v137, v137
	flat_store_dwordx4 v[142:143], v[138:141] sc1
	v_add_f32_e32 v137, 1.0, v137
	s_nop 0
	v_rcp_f32_e32 v138, v137
	v_mul_f32_e32 v137, 0xbfb8aa3b, v81
	v_exp_f32_e32 v137, v137
	s_nop 0
	v_add_f32_e32 v137, 1.0, v137
	v_rcp_f32_e32 v139, v137
	v_mul_f32_e32 v137, 0xbfb8aa3b, v82
	v_exp_f32_e32 v137, v137
	s_nop 0
; __device__ __forceinline__ float sigm(float x) { return __builtin_amdgcn_rcpf(1.0f + __builtin_amdgcn_exp2f(-1.4426950408889634f * x)); }
;     __device__ __forceinline__ void operator()(const f32x4 (&acc)[2][2][4][2], const Unit& u, int wr, int wc, int fr, int fq) const {
;     ...
;                     for (int m = 0; m < 4; ++m) { float* gp = gates + (size_t)(row0 + ai * HALF + m * 16) * 48 + ct0;
; #pragma unroll
;                         for (int n = 0; n < 2; ++n) { const f32x4 v = acc[ai][0][m][n]; *(f32x4*)(gp + 4 * n) = (f32x4){sigm(v[0]), sigm(v[1]), sigm(v[2]), sigm(v[3])}; } }
	v_add_f32_e32 v137, 1.0, v137
	v_rcp_f32_e32 v140, v137
	v_mul_f32_e32 v137, 0xbfb8aa3b, v83
	v_exp_f32_e32 v137, v137
	s_nop 0
	v_add_f32_e32 v137, 1.0, v137
	v_rcp_f32_e32 v141, v137
	v_add_u32_e32 v137, 0x80, v2
	flat_store_dwordx4 v[142:143], v[138:141] offset:16 sc1
	s_nop 1
	v_mad_i64_i32 v[138:139], s[2:3], v137, s7, v[132:133]
	v_mul_f32_e32 v137, 0xbfb8aa3b, v64
	v_exp_f32_e32 v137, v137
	v_lshl_add_u64 v[142:143], v[138:139], 0, v[134:135]
	v_add_f32_e32 v137, 1.0, v137
	v_rcp_f32_e32 v138, v137
	v_mul_f32_e32 v137, 0xbfb8aa3b, v65
	v_exp_f32_e32 v137, v137
	s_nop 0
	v_add_f32_e32 v137, 1.0, v137
	v_rcp_f32_e32 v139, v137
	v_mul_f32_e32 v137, 0xbfb8aa3b, v66
	v_exp_f32_e32 v137, v137
	s_nop 0
	v_add_f32_e32 v137, 1.0, v137
	v_rcp_f32_e32 v140, v137
	v_mul_f32_e32 v137, 0xbfb8aa3b, v67
	v_exp_f32_e32 v137, v137
	s_nop 0
	v_add_f32_e32 v137, 1.0, v137
	v_rcp_f32_e32 v141, v137
	v_mul_f32_e32 v137, 0xbfb8aa3b, v60
	v_exp_f32_e32 v137, v137
	flat_store_dwordx4 v[142:143], v[138:141] sc1
	v_add_f32_e32 v137, 1.0, v137
	s_nop 0
	v_rcp_f32_e32 v138, v137
	v_mul_f32_e32 v137, 0xbfb8aa3b, v61
	v_exp_f32_e32 v137, v137
	s_nop 0
	v_add_f32_e32 v137, 1.0, v137
	v_rcp_f32_e32 v139, v137
	v_mul_f32_e32 v137, 0xbfb8aa3b, v62
	v_exp_f32_e32 v137, v137
	s_nop 0
	v_add_f32_e32 v137, 1.0, v137
	v_rcp_f32_e32 v140, v137
	v_mul_f32_e32 v137, 0xbfb8aa3b, v63
	v_exp_f32_e32 v137, v137
	s_nop 0
	v_add_f32_e32 v137, 1.0, v137
	v_rcp_f32_e32 v141, v137
	v_add_u32_e32 v137, 0x90, v2
	flat_store_dwordx4 v[142:143], v[138:141] offset:16 sc1
	s_nop 1
	v_mad_i64_i32 v[138:139], s[2:3], v137, s7, v[132:133]
	v_mul_f32_e32 v137, 0xbfb8aa3b, v52
	v_exp_f32_e32 v137, v137
	v_lshl_add_u64 v[142:143], v[138:139], 0, v[134:135]
	v_add_f32_e32 v137, 1.0, v137
	v_rcp_f32_e32 v138, v137
	v_mul_f32_e32 v137, 0xbfb8aa3b, v53
	v_exp_f32_e32 v137, v137
	s_nop 0
	v_add_f32_e32 v137, 1.0, v137
	v_rcp_f32_e32 v139, v137
	v_mul_f32_e32 v137, 0xbfb8aa3b, v54
	v_exp_f32_e32 v137, v137
	s_nop 0
	v_add_f32_e32 v137, 1.0, v137
	v_rcp_f32_e32 v140, v137
	v_mul_f32_e32 v137, 0xbfb8aa3b, v55
	v_exp_f32_e32 v137, v137
	s_nop 0
	v_add_f32_e32 v137, 1.0, v137
	v_rcp_f32_e32 v141, v137
	v_mul_f32_e32 v137, 0xbfb8aa3b, v44
	v_exp_f32_e32 v137, v137
	flat_store_dwordx4 v[142:143], v[138:141] sc1
	v_add_f32_e32 v137, 1.0, v137
	s_nop 0
	v_rcp_f32_e32 v138, v137
	v_mul_f32_e32 v137, 0xbfb8aa3b, v45
	v_exp_f32_e32 v137, v137
	s_nop 0
	v_add_f32_e32 v137, 1.0, v137
	v_rcp_f32_e32 v139, v137
	v_mul_f32_e32 v137, 0xbfb8aa3b, v46
	v_exp_f32_e32 v137, v137
	s_nop 0
	v_add_f32_e32 v137, 1.0, v137
	v_rcp_f32_e32 v140, v137
	v_mul_f32_e32 v137, 0xbfb8aa3b, v47
	v_exp_f32_e32 v137, v137
	s_nop 0
	v_add_f32_e32 v137, 1.0, v137
	v_rcp_f32_e32 v141, v137
	v_add_u32_e32 v137, 0xa0, v2
	flat_store_dwordx4 v[142:143], v[138:141] offset:16 sc1
	s_nop 1
	v_mad_i64_i32 v[138:139], s[2:3], v137, s7, v[132:133]
	v_mul_f32_e32 v137, 0xbfb8aa3b, v40
	v_exp_f32_e32 v137, v137
	v_lshl_add_u64 v[142:143], v[138:139], 0, v[134:135]
	v_add_f32_e32 v137, 1.0, v137
	v_rcp_f32_e32 v138, v137
	v_mul_f32_e32 v137, 0xbfb8aa3b, v41
	v_exp_f32_e32 v137, v137
	s_nop 0
	v_add_f32_e32 v137, 1.0, v137
	v_rcp_f32_e32 v139, v137
	v_mul_f32_e32 v137, 0xbfb8aa3b, v42
	v_exp_f32_e32 v137, v137
	s_nop 0
	v_add_f32_e32 v137, 1.0, v137
	v_rcp_f32_e32 v140, v137
	v_mul_f32_e32 v137, 0xbfb8aa3b, v43
	v_exp_f32_e32 v137, v137
	s_nop 0
	v_add_f32_e32 v137, 1.0, v137
	v_rcp_f32_e32 v141, v137
	v_mul_f32_e32 v137, 0xbfb8aa3b, v32
	v_exp_f32_e32 v137, v137
	flat_store_dwordx4 v[142:143], v[138:141] sc1
	v_add_f32_e32 v137, 1.0, v137
	s_nop 0
	v_rcp_f32_e32 v138, v137
	v_mul_f32_e32 v137, 0xbfb8aa3b, v33
	v_exp_f32_e32 v137, v137
	s_nop 0
	v_add_f32_e32 v137, 1.0, v137
	v_rcp_f32_e32 v139, v137
	v_mul_f32_e32 v137, 0xbfb8aa3b, v34
	v_exp_f32_e32 v137, v137
	s_nop 0
	v_add_f32_e32 v137, 1.0, v137
	v_rcp_f32_e32 v140, v137
	v_mul_f32_e32 v137, 0xbfb8aa3b, v35
	v_exp_f32_e32 v137, v137
	s_nop 0
	v_add_f32_e32 v137, 1.0, v137
	v_rcp_f32_e32 v141, v137
	v_add_u32_e32 v137, 0xb0, v2
	v_mad_i64_i32 v[132:133], s[2:3], v137, s7, v[132:133]
	flat_store_dwordx4 v[142:143], v[138:141] offset:16 sc1
	s_nop 1
	v_lshl_add_u64 v[138:139], v[132:133], 0, v[134:135]
	v_mul_f32_e32 v132, 0xbfb8aa3b, v24
	v_mul_f32_e32 v133, 0xbfb8aa3b, v25
	v_mul_f32_e32 v134, 0xbfb8aa3b, v26
	v_mul_f32_e32 v135, 0xbfb8aa3b, v27
	v_exp_f32_e32 v132, v132
	v_exp_f32_e32 v133, v133
	v_exp_f32_e32 v134, v134
	v_exp_f32_e32 v135, v135
	v_add_f32_e32 v132, 1.0, v132
	v_add_f32_e32 v133, 1.0, v133
	v_add_f32_e32 v134, 1.0, v134
	v_add_f32_e32 v135, 1.0, v135
	v_rcp_f32_e32 v132, v132
	v_rcp_f32_e32 v133, v133
	v_rcp_f32_e32 v134, v134
	v_rcp_f32_e32 v135, v135
	flat_store_dwordx4 v[138:139], v[132:135] sc1
	s_nop 1
	v_mul_f32_e32 v132, 0xbfb8aa3b, v16
	v_mul_f32_e32 v133, 0xbfb8aa3b, v17
	v_mul_f32_e32 v134, 0xbfb8aa3b, v18
	v_mul_f32_e32 v135, 0xbfb8aa3b, v19
	v_exp_f32_e32 v132, v132
	v_exp_f32_e32 v133, v133
	v_exp_f32_e32 v134, v134
	v_exp_f32_e32 v135, v135
	v_add_f32_e32 v132, 1.0, v132
	v_add_f32_e32 v133, 1.0, v133
	v_add_f32_e32 v134, 1.0, v134
	v_add_f32_e32 v135, 1.0, v135
	v_rcp_f32_e32 v132, v132
	v_rcp_f32_e32 v133, v133
	v_rcp_f32_e32 v134, v134
	v_rcp_f32_e32 v135, v135
	flat_store_dwordx4 v[138:139], v[132:135] offset:16 sc1

; __device__ __forceinline__ unsigned cvt_pk_bf16(float lo, float hi) { unsigned r; asm volatile("v_cvt_pk_bf16_f32 %0, %1, %2" : "=v"(r) : "v"(lo), "v"(hi)); return r; }
; __device__ __forceinline__ u32x4 pack8(const f32x4 a, const f32x4 b) { u32x4 w; w.x = cvt_pk_bf16(a[0], a[1]); w.y = cvt_pk_bf16(a[2], a[3]); w.z = cvt_pk_bf16(b[0], b[1]); w.w = cvt_pk_bf16(b[2], b[3]); return w; }
;     __device__ __forceinline__ void operator()(const f32x4 (&acc)[2][2][4][2], const Unit& u, int wr, int wc, int fr, int fq) const {
;     ...
;         } else if (u.pn < 10) {
;             bf16_t* base = KV + (size_t)(u.pn - 4) * kvstride;
; #pragma unroll
;             for (int ai = 0; ai < 2; ++ai)
; #pragma unroll
;                 for (int m = 0; m < 4; ++m) { const int row = row0 + ai * HALF + m * 16, b = row >> 11, s = row & 2047;
; #pragma unroll
;                     for (int bj = 0; bj < 2; ++bj) { const int ct = bj * HALF + ct0, g = ct >> 6, d = ct & 63;
;                         *(u32x4*)(base + ((size_t)((b * 4 + g) * 2048 + s)) * 64 + d) = pack8(acc[ai][bj][m][0], acc[ai][bj][m][1]); } }
.LBB0_1254:
	s_andn2_b64 vcc, exec, s[4:5]
	s_cbranch_vccnz .LBB0_1256
	s_add_i32 s14, s14, -2
	s_mul_i32 s4, s14, 0
	s_mul_hi_u32 s5, 0x400000, s14
	s_lshr_b32 s3, s15, 1
	s_add_i32 s5, s5, s4
	s_mul_i32 s4, s14, 0x400000
	s_or_b32 s2, s3, 2
	s_lshl_b64 s[4:5], s[4:5], 1
	v_and_b32_e32 v132, 56, v136
	s_add_u32 s0, s0, s4
	s_addc_u32 s1, s1, s5
	v_lshlrev_b32_e32 v132, 1, v132
	v_mov_b32_e32 v133, v3
	v_lshl_add_u64 v[132:133], s[0:1], 0, v[132:133]
	s_ashr_i32 s0, s6, 9
	s_and_b32 s0, s0, -4
	s_or_b32 s1, s0, s3
	v_and_b32_e32 v134, 0x7cf, v2
	s_lshl_b32 s1, s1, 11
	v_cvt_pk_bf16_f32 v128, v128, v129
	v_cvt_pk_bf16_f32 v129, v130, v131
	v_cvt_pk_bf16_f32 v130, v124, v125
	v_or_b32_e32 v124, s1, v134
	v_ashrrev_i32_e32 v125, 31, v124
	v_lshlrev_b64 v[124:125], 7, v[124:125]
	s_or_b32 s0, s0, s2
	v_lshl_add_u64 v[124:125], v[132:133], 0, v[124:125]
	s_lshl_b32 s0, s0, 11
	v_cvt_pk_bf16_f32 v131, v126, v127
	flat_store_dwordx4 v[124:125], v[128:131] sc1
	v_cvt_pk_bf16_f32 v120, v120, v121
	v_cvt_pk_bf16_f32 v121, v122, v123
	v_cvt_pk_bf16_f32 v122, v112, v113
	v_or_b32_e32 v112, s0, v134
	v_ashrrev_i32_e32 v113, 31, v112
	v_lshlrev_b64 v[112:113], 7, v[112:113]
	v_lshl_add_u64 v[112:113], v[132:133], 0, v[112:113]
	v_cvt_pk_bf16_f32 v123, v114, v115
	flat_store_dwordx4 v[112:113], v[120:123] sc1
	v_cvt_pk_bf16_f32 v112, v116, v117
	v_cvt_pk_bf16_f32 v113, v118, v119
	v_cvt_pk_bf16_f32 v114, v108, v109
	v_cvt_pk_bf16_f32 v115, v110, v111
	v_add_u32_e32 v2, 0x80, v2
	s_nop 0
	v_or_b32_e32 v120, 16, v134
	v_or_b32_e32 v108, s1, v120
	v_ashrrev_i32_e32 v109, 31, v108
	v_lshlrev_b64 v[108:109], 7, v[108:109]
	v_lshl_add_u64 v[108:109], v[132:133], 0, v[108:109]
	flat_store_dwordx4 v[108:109], v[112:115] sc1
	v_cvt_pk_bf16_f32 v100, v100, v101
	v_cvt_pk_bf16_f32 v101, v102, v103
	v_cvt_pk_bf16_f32 v102, v92, v93
	v_or_b32_e32 v92, s0, v120
	v_ashrrev_i32_e32 v93, 31, v92
	v_lshlrev_b64 v[92:93], 7, v[92:93]
	v_lshl_add_u64 v[92:93], v[132:133], 0, v[92:93]
	v_cvt_pk_bf16_f32 v103, v94, v95
	flat_store_dwordx4 v[92:93], v[100:103] sc1
	v_cvt_pk_bf16_f32 v92, v104, v105
	v_cvt_pk_bf16_f32 v93, v106, v107
	v_cvt_pk_bf16_f32 v94, v96, v97
	v_cvt_pk_bf16_f32 v95, v98, v99
	s_nop 1
	v_or_b32_e32 v100, 32, v134
	v_or_b32_e32 v96, s1, v100
	v_ashrrev_i32_e32 v97, 31, v96
	v_lshlrev_b64 v[96:97], 7, v[96:97]
	v_lshl_add_u64 v[96:97], v[132:133], 0, v[96:97]
	flat_store_dwordx4 v[96:97], v[92:95] sc1
	v_cvt_pk_bf16_f32 v84, v84, v85
	v_cvt_pk_bf16_f32 v85, v86, v87
	v_cvt_pk_bf16_f32 v86, v76, v77
	v_or_b32_e32 v76, s0, v100
	v_ashrrev_i32_e32 v77, 31, v76
	v_lshlrev_b64 v[76:77], 7, v[76:77]
	v_lshl_add_u64 v[76:77], v[132:133], 0, v[76:77]
	v_cvt_pk_bf16_f32 v87, v78, v79
	flat_store_dwordx4 v[76:77], v[84:87] sc1
	v_cvt_pk_bf16_f32 v76, v88, v89
	v_cvt_pk_bf16_f32 v77, v90, v91
	v_cvt_pk_bf16_f32 v78, v80, v81
	v_cvt_pk_bf16_f32 v79, v82, v83
	s_nop 1
	v_or_b32_e32 v84, 48, v134
	v_or_b32_e32 v80, s1, v84
	v_ashrrev_i32_e32 v81, 31, v80
	v_lshlrev_b64 v[80:81], 7, v[80:81]
	v_lshl_add_u64 v[80:81], v[132:133], 0, v[80:81]
	flat_store_dwordx4 v[80:81], v[76:79] sc1
	v_cvt_pk_bf16_f32 v72, v72, v73
	v_cvt_pk_bf16_f32 v73, v74, v75
	v_cvt_pk_bf16_f32 v74, v68, v69
	v_or_b32_e32 v68, s0, v84
	v_ashrrev_i32_e32 v69, 31, v68
	v_lshlrev_b64 v[68:69], 7, v[68:69]
	v_lshl_add_u64 v[68:69], v[132:133], 0, v[68:69]
	v_cvt_pk_bf16_f32 v75, v70, v71
	flat_store_dwordx4 v[68:69], v[72:75] sc1
	v_and_b32_e32 v68, 0x7cf, v2
	v_ashrrev_i32_e32 v2, 9, v2
	v_and_b32_e32 v2, -4, v2
	v_cvt_pk_bf16_f32 v64, v64, v65
	v_cvt_pk_bf16_f32 v65, v66, v67
	v_cvt_pk_bf16_f32 v66, v60, v61
	v_or_b32_e32 v60, s3, v2
	v_cvt_pk_bf16_f32 v67, v62, v63
	v_lshlrev_b32_e32 v62, 11, v60
	v_or_b32_e32 v60, v62, v68
	v_ashrrev_i32_e32 v61, 31, v60
	v_lshlrev_b64 v[60:61], 7, v[60:61]
	v_or_b32_e32 v2, s2, v2
	v_lshl_add_u64 v[60:61], v[132:133], 0, v[60:61]
	v_lshlrev_b32_e32 v2, 11, v2
	flat_store_dwordx4 v[60:61], v[64:67] sc1
	v_cvt_pk_bf16_f32 v56, v56, v57
	v_cvt_pk_bf16_f32 v57, v58, v59
	v_cvt_pk_bf16_f32 v58, v48, v49
	v_or_b32_e32 v48, v2, v68
	v_ashrrev_i32_e32 v49, 31, v48
	v_lshlrev_b64 v[48:49], 7, v[48:49]
	v_lshl_add_u64 v[48:49], v[132:133], 0, v[48:49]
	v_cvt_pk_bf16_f32 v59, v50, v51
	flat_store_dwordx4 v[48:49], v[56:59] sc1
	v_cvt_pk_bf16_f32 v48, v52, v53
	v_cvt_pk_bf16_f32 v49, v54, v55
	v_cvt_pk_bf16_f32 v50, v44, v45
	v_cvt_pk_bf16_f32 v51, v46, v47
	s_nop 1
	v_or_b32_e32 v56, 16, v68
	v_or_b32_e32 v44, v62, v56
	v_ashrrev_i32_e32 v45, 31, v44
	v_lshlrev_b64 v[44:45], 7, v[44:45]
	v_lshl_add_u64 v[44:45], v[132:133], 0, v[44:45]
	flat_store_dwordx4 v[44:45], v[48:51] sc1
	v_cvt_pk_bf16_f32 v36, v36, v37
	v_cvt_pk_bf16_f32 v37, v38, v39
	v_cvt_pk_bf16_f32 v38, v28, v29
	v_or_b32_e32 v28, v2, v56
	v_ashrrev_i32_e32 v29, 31, v28
	v_lshlrev_b64 v[28:29], 7, v[28:29]
	v_lshl_add_u64 v[28:29], v[132:133], 0, v[28:29]
	v_cvt_pk_bf16_f32 v39, v30, v31
	flat_store_dwordx4 v[28:29], v[36:39] sc1
	v_cvt_pk_bf16_f32 v28, v40, v41
	v_cvt_pk_bf16_f32 v29, v42, v43
	v_cvt_pk_bf16_f32 v30, v32, v33
	v_cvt_pk_bf16_f32 v31, v34, v35
	s_nop 1
	v_or_b32_e32 v36, 32, v68
	v_or_b32_e32 v32, v62, v36
	v_ashrrev_i32_e32 v33, 31, v32
	v_lshlrev_b64 v[32:33], 7, v[32:33]
	v_lshl_add_u64 v[32:33], v[132:133], 0, v[32:33]
	flat_store_dwordx4 v[32:33], v[28:31] sc1
	v_cvt_pk_bf16_f32 v20, v20, v21
	v_cvt_pk_bf16_f32 v21, v22, v23
	v_cvt_pk_bf16_f32 v22, v12, v13
	v_or_b32_e32 v12, v2, v36
	v_ashrrev_i32_e32 v13, 31, v12
	v_lshlrev_b64 v[12:13], 7, v[12:13]
	v_lshl_add_u64 v[12:13], v[132:133], 0, v[12:13]
	v_cvt_pk_bf16_f32 v23, v14, v15
	flat_store_dwordx4 v[12:13], v[20:23] sc1
	v_cvt_pk_bf16_f32 v12, v24, v25
	v_cvt_pk_bf16_f32 v13, v26, v27
	v_cvt_pk_bf16_f32 v14, v16, v17
	v_cvt_pk_bf16_f32 v15, v18, v19
	s_nop 1
	v_or_b32_e32 v20, 48, v68
	v_or_b32_e32 v16, v62, v20
	v_ashrrev_i32_e32 v17, 31, v16
	v_lshlrev_b64 v[16:17], 7, v[16:17]
	v_lshl_add_u64 v[16:17], v[132:133], 0, v[16:17]
	flat_store_dwordx4 v[16:17], v[12:15] sc1
	v_cvt_pk_bf16_f32 v8, v8, v9
	v_cvt_pk_bf16_f32 v9, v10, v11
	v_cvt_pk_bf16_f32 v10, v4, v5
	v_or_b32_e32 v4, v2, v20
	v_ashrrev_i32_e32 v5, 31, v4
	v_lshlrev_b64 v[4:5], 7, v[4:5]
	v_lshl_add_u64 v[4:5], v[132:133], 0, v[4:5]
	v_cvt_pk_bf16_f32 v11, v6, v7
	flat_store_dwordx4 v[4:5], v[8:11] sc1

; #define PG8_BAR __builtin_amdgcn_s_barrier()
; __device__ __forceinline__ u32x4 pack8(const f32x4 a, const f32x4 b) { u32x4 w; w.x = cvt_pk_bf16(a[0], a[1]); w.y = cvt_pk_bf16(a[2], a[3]); w.z = cvt_pk_bf16(b[0], b[1]); w.w = cvt_pk_bf16(b[2], b[3]); return w; }
; template <class Epi, class Sched, bool ALIGN_EPI = false, bool SP2 = false>
; __device__ __forceinline__ void gemm_phase(PG8_LAS unsigned char* lds, const Gemm g, const Sched& S, const Epi& E) {
;     ...
;         cur = nxt; cA = nA; cB = nB; ++ui;
;         if constexpr (ALIGN_EPI) { if (wr == 1) PG8_BAR; }
;     __device__ __forceinline__ void operator()(const f32x4 (&acc)[2][2][4][2], const Unit& u, int wr, int wc, int fr, int fq) const {
;         const int row0 = u.pm * BM + wr * 64 + fr, col0 = u.pn * BM + wc * 32 + 8 * fq;
; #pragma unroll
;         for (int ai = 0; ai < 2; ++ai)
; #pragma unroll
;             for (int m = 0; m < 4; ++m) {
;                 bf16_t* rowp = O + (size_t)(row0 + ai * HALF + m * 16) * ldc + col0;
; #pragma unroll
;                 for (int bj = 0; bj < 2; ++bj) *(u32x4*)(rowp + bj * HALF) = pack8(acc[ai][bj][m][0], acc[ai][bj][m][1]);
;             }
.LBB0_1696:
	v_lshl_add_u32 v150, s14, 8, v2
	v_lshl_or_b32 v144, s40, 8, v147
	v_ashrrev_i32_e32 v151, 31, v150
	v_ashrrev_i32_e32 v145, 31, v144
	v_lshlrev_b64 v[152:153], 11, v[150:151]
	v_lshl_add_u64 v[152:153], s[6:7], 0, v[152:153]
	v_lshlrev_b64 v[154:155], 1, v[144:145]
	v_lshl_add_u64 v[144:145], v[152:153], 0, v[154:155]
	v_cvt_pk_bf16_f32 v128, v128, v129
	v_cvt_pk_bf16_f32 v129, v130, v131
	v_cvt_pk_bf16_f32 v130, v124, v125
	v_cvt_pk_bf16_f32 v131, v126, v127
	flat_store_dwordx4 v[144:145], v[128:131] sc1
	v_cvt_pk_bf16_f32 v116, v116, v117
	v_cvt_pk_bf16_f32 v117, v118, v119
	v_cvt_pk_bf16_f32 v118, v108, v109
	v_or_b32_e32 v108, 16, v150
	v_ashrrev_i32_e32 v109, 31, v108
	v_lshlrev_b64 v[108:109], 11, v[108:109]
	v_lshl_add_u64 v[108:109], s[6:7], 0, v[108:109]
	v_cvt_pk_bf16_f32 v119, v110, v111
	flat_store_dwordx4 v[144:145], v[116:119] offset:256 sc1
	s_mov_b32 s11, 0x40000
	s_mov_b64 s[20:21], 0x40000
	v_lshl_add_u64 v[116:117], v[108:109], 0, v[154:155]
	v_cvt_pk_bf16_f32 v108, v120, v121
	v_cvt_pk_bf16_f32 v109, v122, v123
	v_cvt_pk_bf16_f32 v110, v112, v113
	v_cvt_pk_bf16_f32 v111, v114, v115
	flat_store_dwordx4 v[116:117], v[108:111] sc1
	v_cvt_pk_bf16_f32 v100, v100, v101
	v_cvt_pk_bf16_f32 v101, v102, v103
	v_cvt_pk_bf16_f32 v102, v92, v93
	v_or_b32_e32 v92, 32, v150
	v_ashrrev_i32_e32 v93, 31, v92
	v_lshlrev_b64 v[92:93], 11, v[92:93]
	v_lshl_add_u64 v[92:93], s[6:7], 0, v[92:93]
	v_cvt_pk_bf16_f32 v103, v94, v95
	flat_store_dwordx4 v[116:117], v[100:103] offset:256 sc1
	s_nop 1
	v_lshl_add_u64 v[100:101], v[92:93], 0, v[154:155]
	v_cvt_pk_bf16_f32 v92, v104, v105
	v_cvt_pk_bf16_f32 v93, v106, v107
	v_cvt_pk_bf16_f32 v94, v96, v97
	v_cvt_pk_bf16_f32 v95, v98, v99
	flat_store_dwordx4 v[100:101], v[92:95] sc1
	v_cvt_pk_bf16_f32 v84, v84, v85
	v_cvt_pk_bf16_f32 v85, v86, v87
	v_cvt_pk_bf16_f32 v86, v76, v77
	v_or_b32_e32 v76, 48, v150
	v_ashrrev_i32_e32 v77, 31, v76
	v_lshlrev_b64 v[76:77], 11, v[76:77]
	v_lshl_add_u64 v[76:77], s[6:7], 0, v[76:77]
	v_cvt_pk_bf16_f32 v87, v78, v79
	flat_store_dwordx4 v[100:101], v[84:87] offset:256 sc1
	s_nop 1
	v_lshl_add_u64 v[84:85], v[76:77], 0, v[154:155]
	v_cvt_pk_bf16_f32 v76, v88, v89
	v_cvt_pk_bf16_f32 v77, v90, v91
	v_cvt_pk_bf16_f32 v78, v80, v81
	v_cvt_pk_bf16_f32 v79, v82, v83
	flat_store_dwordx4 v[84:85], v[76:79] sc1
	v_cvt_pk_bf16_f32 v72, v72, v73
	v_cvt_pk_bf16_f32 v73, v74, v75
	v_cvt_pk_bf16_f32 v74, v68, v69
	v_cvt_pk_bf16_f32 v75, v70, v71
	flat_store_dwordx4 v[84:85], v[72:75] offset:256 sc1
	v_cvt_pk_bf16_f32 v64, v64, v65
	v_cvt_pk_bf16_f32 v65, v66, v67
	v_cvt_pk_bf16_f32 v66, v60, v61
	v_add_co_u32_e32 v60, vcc, s11, v144
	v_lshl_add_u64 v[68:69], v[144:145], 0, s[20:21]
	s_nop 0
	v_addc_co_u32_e32 v61, vcc, 0, v145, vcc
	s_mov_b32 s11, 0x48000
	v_cvt_pk_bf16_f32 v67, v62, v63
	flat_store_dwordx4 v[60:61], v[64:67] sc1
	v_cvt_pk_bf16_f32 v52, v52, v53
	v_cvt_pk_bf16_f32 v53, v54, v55
	v_cvt_pk_bf16_f32 v54, v44, v45
	v_cvt_pk_bf16_f32 v55, v46, v47
	flat_store_dwordx4 v[68:69], v[52:55] offset:256 sc1
	s_mov_b64 s[20:21], 0x48000
	v_cvt_pk_bf16_f32 v44, v56, v57
	v_cvt_pk_bf16_f32 v45, v58, v59
	v_cvt_pk_bf16_f32 v46, v48, v49
	v_add_co_u32_e32 v48, vcc, s11, v144
	v_lshl_add_u64 v[52:53], v[144:145], 0, s[20:21]
	s_nop 0
	v_addc_co_u32_e32 v49, vcc, 0, v145, vcc
	s_mov_b32 s11, 0x50000
	v_cvt_pk_bf16_f32 v47, v50, v51
	flat_store_dwordx4 v[48:49], v[44:47] sc1
	v_cvt_pk_bf16_f32 v36, v36, v37
	v_cvt_pk_bf16_f32 v37, v38, v39
	v_cvt_pk_bf16_f32 v38, v28, v29
	v_cvt_pk_bf16_f32 v39, v30, v31
	flat_store_dwordx4 v[52:53], v[36:39] offset:256 sc1
	s_mov_b64 s[20:21], 0x50000
	v_cvt_pk_bf16_f32 v28, v40, v41
	v_cvt_pk_bf16_f32 v29, v42, v43
	v_cvt_pk_bf16_f32 v30, v32, v33
	v_add_co_u32_e32 v32, vcc, s11, v144
	v_lshl_add_u64 v[36:37], v[144:145], 0, s[20:21]
	s_nop 0
	v_addc_co_u32_e32 v33, vcc, 0, v145, vcc
	s_mov_b32 s11, 0x58000
	v_cvt_pk_bf16_f32 v31, v34, v35
	flat_store_dwordx4 v[32:33], v[28:31] sc1
	v_cvt_pk_bf16_f32 v20, v20, v21
	v_cvt_pk_bf16_f32 v21, v22, v23
	v_cvt_pk_bf16_f32 v22, v12, v13
	v_cvt_pk_bf16_f32 v23, v14, v15
	flat_store_dwordx4 v[36:37], v[20:23] offset:256 sc1
	v_cvt_pk_bf16_f32 v12, v24, v25
	v_cvt_pk_bf16_f32 v13, v26, v27
	v_cvt_pk_bf16_f32 v14, v16, v17
	v_add_co_u32_e32 v16, vcc, s11, v144
	s_mov_b64 s[20:21], 0x58000
	s_nop 0
	v_addc_co_u32_e32 v17, vcc, 0, v145, vcc
	v_lshl_add_u64 v[20:21], v[144:145], 0, s[20:21]
	s_andn2_b64 vcc, exec, s[2:3]
	s_mov_b64 s[2:3], -1
	v_cvt_pk_bf16_f32 v15, v18, v19
	flat_store_dwordx4 v[16:17], v[12:15] sc1
	v_cvt_pk_bf16_f32 v8, v8, v9
	v_cvt_pk_bf16_f32 v9, v10, v11
	v_cvt_pk_bf16_f32 v10, v4, v5
	v_cvt_pk_bf16_f32 v11, v6, v7
	flat_store_dwordx4 v[20:21], v[8:11] offset:256 sc1
	s_cbranch_vccnz .LBB0_1685
	s_andn2_b64 vcc, exec, s[4:5]
	s_cbranch_vccnz .LBB0_1684
	s_barrier
	s_branch .LBB0_1684
